# speedup vs baseline: 1.1543x; 1.0168x over previous
_Z8attn_fwdPKfPKiPf:
	s_load_dwordx4 s[4:7], s[0:1], 0x0
	s_load_dwordx2 s[12:13], s[0:1], 0x10
	v_and_b32_e32 v235, 63, v0
	v_lshrrev_b32_e32 v236, 4, v0
	v_and_b32_e32 v237, 15, v0
	v_readfirstlane_b32 s17, v0
	s_nop 3
	s_lshr_b32 s17, s17, 6
	v_mul_u32_u24_e32 v229, 0x3000, v236
	v_lshl_add_u32 v229, v237, 4, v229
	v_mul_u32_u24_e32 v227, 144, v236
	v_lshl_add_u32 v227, v237, 3, v227
	v_lshlrev_b32_e32 v230, 2, v235
	v_and_b32_e32 v238, 31, v0
	v_bfe_u32 v236, v0, 5, 1
	v_mul_u32_u24_e32 v225, 144, v238
	v_lshl_add_u32 v225, v236, 4, v225
	v_add_u32_e32 v226, 36864, v225
	v_lshlrev_b32_e32 v234, 2, v236
	v_mul_u32_u24_e32 v228, 144, v235
	s_lshl_b32 s31, s17, 4
	s_add_u32 s31, s31, 36864
	v_add_u32_e32 v228, s31, v228
	s_mul_i32 s32, s17, 8704
	s_add_u32 s32, s32, 73728
	v_lshrrev_b32_e32 v231, 4, v235
	v_mul_u32_u24_e32 v239, 144, v231
	v_lshl_add_u32 v239, v237, 3, v239
	v_add_u32_e32 v239, s32, v239
	v_add_u32_e32 v240, s32, v225
	v_mul_u32_u24_e32 v241, 272, v238
	v_lshl_add_u32 v241, v236, 4, v241
	v_add_u32_e32 v241, s32, v241
	v_mul_u32_u24_e32 v242, 272, v231
	v_lshl_add_u32 v242, v237, 4, v242
	v_add_u32_e32 v242, s32, v242
	v_mul_u32_u24_e32 v243, 0x3000, v231
	v_lshl_add_u32 v243, v237, 4, v243
	v_lshlrev_b32_e32 v244, 12, v231
	v_lshl_add_u32 v244, v237, 4, v244
	s_and_b32 s33, s2, 7
	s_lshr_b32 s31, s2, 3
	s_and_b32 s39, s31, 3
	s_lshr_b32 s40, s31, 3
	s_lshr_b32 s41, s31, 2
	s_and_b32 s41, s41, 1
	s_lshl_b32 s33, s33, 1
	s_add_u32 s41, s41, s33
	s_mul_i32 s16, s40, 0x1800000
	s_lshl_b32 s31, s41, 8
	s_add_u32 s16, s16, s31
	s_add_u32 s18, s16, 4096
	s_lshr_b32 s31, s17, 1
	s_lshl_b32 s31, s31, 4
	s_and_b32 s33, s17, 1
	s_lshl_b32 s33, s33, 2
	s_add_u32 s31, s31, s33
	s_mul_i32 s31, s31, 0x3000
	s_add_u32 s19, s16, 8192
	s_add_u32 s19, s19, s31
	s_lshl_b32 s22, s40, 13
	s_lshl_b32 s31, s39, 8
	s_lshl_b32 s33, s17, 5
	s_add_u32 s31, s31, s33
	s_mul_i32 s29, s31, 0x3000
	s_add_u32 s29, s29, s16
	s_lshl_b32 s33, s40, 11
	s_add_u32 s31, s31, s33
	s_lshl_b32 s30, s31, 12
	s_lshl_b32 s31, s41, 8
	s_add_u32 s30, s30, s31
	s_mov_b32 s37, 0x46800000
	s_mov_b32 s38, 0xbf800000
	s_mov_b32 s34, 0x46800000
	s_mov_b32 s35, 0xc6616bcd
	s_mov_b32 s36, 0x3e38aa3b
	s_mov_b32 s23, 0
	s_mov_b32 s27, 0
	s_mov_b32 s42, 0
	s_waitcnt lgkmcnt(0)
	s_mov_b32 s8, s6
	s_and_b32 s9, s7, 0xffff
	s_mov_b32 s10, 0x7fffffff
	s_mov_b32 s11, 0x20000
	s_and_b32 s5, s5, 0xffff
	s_mov_b32 s6, 0x7fffffff
	s_mov_b32 s7, 0x20000
	s_and_b32 s13, s13, 0xffff
	s_mov_b32 s14, 0x7fffffff
	s_mov_b32 s15, 0x20000
	s_add_u32 s31, s18, 0x0
	buffer_load_dwordx4 v[64:67], v229, s[4:7], s31 offen
	s_add_u32 s31, s18, 0x60000
	buffer_load_dwordx4 v[68:71], v229, s[4:7], s31 offen
	buffer_load_dword v224, v230, s[8:11], s22 offen
	s_add_u32 s31, s18, 0xc0000
	buffer_load_dwordx4 v[72:75], v229, s[4:7], s31 offen
	s_add_u32 s31, s18, 0x120000
	buffer_load_dwordx4 v[76:79], v229, s[4:7], s31 offen
	s_add_u32 s31, s19, 0x0
	buffer_load_dword v80, v230, s[4:7], s31 offen
	s_add_u32 s31, s19, 0x3000
	buffer_load_dword v81, v230, s[4:7], s31 offen
	s_add_u32 s31, s19, 0x6000
	buffer_load_dword v82, v230, s[4:7], s31 offen
	s_add_u32 s31, s19, 0x9000
	buffer_load_dword v83, v230, s[4:7], s31 offen
	s_add_u32 s31, s19, 0x18000
	buffer_load_dword v84, v230, s[4:7], s31 offen
	s_add_u32 s31, s19, 0x1b000
	buffer_load_dword v85, v230, s[4:7], s31 offen
	s_add_u32 s31, s19, 0x1e000
	buffer_load_dword v86, v230, s[4:7], s31 offen
	s_add_u32 s31, s19, 0x21000
	buffer_load_dword v87, v230, s[4:7], s31 offen
	s_add_u32 s31, s29, 0x0
	buffer_load_dwordx4 v[0:3], v243, s[4:7], s31 offen nt
	s_add_u32 s31, s29, 0xc000
	buffer_load_dwordx4 v[4:7], v243, s[4:7], s31 offen nt
	s_add_u32 s31, s29, 0x18000
	buffer_load_dwordx4 v[8:11], v243, s[4:7], s31 offen nt
	s_add_u32 s31, s29, 0x24000
	buffer_load_dwordx4 v[12:15], v243, s[4:7], s31 offen nt
	s_add_u32 s31, s29, 0x30000
	buffer_load_dwordx4 v[16:19], v243, s[4:7], s31 offen nt
	s_add_u32 s31, s29, 0x3c000
	buffer_load_dwordx4 v[20:23], v243, s[4:7], s31 offen nt
	s_add_u32 s31, s29, 0x48000
	buffer_load_dwordx4 v[24:27], v243, s[4:7], s31 offen nt
	s_add_u32 s31, s29, 0x54000
	buffer_load_dwordx4 v[28:31], v243, s[4:7], s31 offen nt
	s_waitcnt vmcnt(8)
	v_cvt_pk_f16_f32 v64, v64, v65
	v_cvt_pk_f16_f32 v65, v66, v67
	ds_write_b64 v227, v[64:65] offset:0
	v_cvt_pk_f16_f32 v68, v68, v69
	v_cvt_pk_f16_f32 v69, v70, v71
	ds_write_b64 v227, v[68:69] offset:4608
	v_cvt_pk_f16_f32 v72, v72, v73
	v_cvt_pk_f16_f32 v73, v74, v75
	ds_write_b64 v227, v[72:73] offset:9216
	v_cvt_pk_f16_f32 v76, v76, v77
	v_cvt_pk_f16_f32 v77, v78, v79
	ds_write_b64 v227, v[76:77] offset:13824
	v_cvt_pk_f16_f32 v80, v80, v81
	v_cvt_pk_f16_f32 v81, v82, v83
	v_cvt_pk_f16_f32 v82, v84, v85
	v_cvt_pk_f16_f32 v83, v86, v87
	ds_write_b128 v228, v[80:83] offset:0
	s_add_u32 s31, s18, 0x180000
	buffer_load_dwordx4 v[208:211], v229, s[4:7], s31 offen
	s_add_u32 s31, s18, 0x1e0000
	buffer_load_dwordx4 v[212:215], v229, s[4:7], s31 offen
	s_add_u32 s31, s19, 0xc0000
	buffer_load_dword v216, v230, s[4:7], s31 offen
	s_add_u32 s31, s19, 0xc3000
	buffer_load_dword v217, v230, s[4:7], s31 offen
	s_add_u32 s31, s19, 0xc6000
	buffer_load_dword v218, v230, s[4:7], s31 offen
	s_add_u32 s31, s19, 0xc9000
	buffer_load_dword v219, v230, s[4:7], s31 offen
	s_add_u32 s31, s19, 0xd8000
	buffer_load_dword v220, v230, s[4:7], s31 offen
	s_add_u32 s31, s19, 0xdb000
	buffer_load_dword v221, v230, s[4:7], s31 offen
	s_add_u32 s31, s19, 0xde000
	buffer_load_dword v222, v230, s[4:7], s31 offen
	s_add_u32 s31, s19, 0xe1000
	buffer_load_dword v223, v230, s[4:7], s31 offen
	s_waitcnt vmcnt(10)
	v_mul_f32_e32 v0, s36, v0
	v_mul_f32_e32 v1, s36, v1
	v_mul_f32_e32 v2, s36, v2
	v_mul_f32_e32 v3, s36, v3
	v_cvt_pk_f16_f32 v0, v0, v1
	v_cvt_pk_f16_f32 v1, v2, v3
	ds_write_b64 v239, v[0:1] offset:0
	v_mul_f32_e32 v4, s36, v4
	v_mul_f32_e32 v5, s36, v5
	v_mul_f32_e32 v6, s36, v6
	v_mul_f32_e32 v7, s36, v7
	v_cvt_pk_f16_f32 v4, v4, v5
	v_cvt_pk_f16_f32 v5, v6, v7
	ds_write_b64 v239, v[4:5] offset:576
	v_mul_f32_e32 v8, s36, v8
	v_mul_f32_e32 v9, s36, v9
	v_mul_f32_e32 v10, s36, v10
	v_mul_f32_e32 v11, s36, v11
	v_cvt_pk_f16_f32 v8, v8, v9
	v_cvt_pk_f16_f32 v9, v10, v11
	ds_write_b64 v239, v[8:9] offset:1152
	v_mul_f32_e32 v12, s36, v12
	v_mul_f32_e32 v13, s36, v13
	v_mul_f32_e32 v14, s36, v14
	v_mul_f32_e32 v15, s36, v15
	v_cvt_pk_f16_f32 v12, v12, v13
	v_cvt_pk_f16_f32 v13, v14, v15
	ds_write_b64 v239, v[12:13] offset:1728
	v_mul_f32_e32 v16, s36, v16
	v_mul_f32_e32 v17, s36, v17
	v_mul_f32_e32 v18, s36, v18
	v_mul_f32_e32 v19, s36, v19
	v_cvt_pk_f16_f32 v16, v16, v17
	v_cvt_pk_f16_f32 v17, v18, v19
	ds_write_b64 v239, v[16:17] offset:2304
	v_mul_f32_e32 v20, s36, v20
	v_mul_f32_e32 v21, s36, v21
	v_mul_f32_e32 v22, s36, v22
	v_mul_f32_e32 v23, s36, v23
	v_cvt_pk_f16_f32 v20, v20, v21
	v_cvt_pk_f16_f32 v21, v22, v23
	ds_write_b64 v239, v[20:21] offset:2880
	v_mul_f32_e32 v24, s36, v24
	v_mul_f32_e32 v25, s36, v25
	v_mul_f32_e32 v26, s36, v26
	v_mul_f32_e32 v27, s36, v27
	v_cvt_pk_f16_f32 v24, v24, v25
	v_cvt_pk_f16_f32 v25, v26, v27
	ds_write_b64 v239, v[24:25] offset:3456
	v_mul_f32_e32 v28, s36, v28
	v_mul_f32_e32 v29, s36, v29
	v_mul_f32_e32 v30, s36, v30
	v_mul_f32_e32 v31, s36, v31
	v_cvt_pk_f16_f32 v28, v28, v29
	v_cvt_pk_f16_f32 v29, v30, v31
	ds_write_b64 v239, v[28:29] offset:4032
	s_waitcnt lgkmcnt(0)
	ds_read_b128 v[128:131], v240 offset:0
	ds_read_b128 v[132:135], v240 offset:32
	ds_read_b128 v[136:139], v240 offset:64
	ds_read_b128 v[140:143], v240 offset:96
	s_waitcnt lgkmcnt(0)
	s_barrier
	ds_read_b128 v[176:179], v225 offset:0
	ds_read_b128 v[180:183], v225 offset:32
	ds_read_b128 v[184:187], v225 offset:64
	ds_read_b128 v[188:191], v225 offset:96
	ds_read_b128 v[192:195], v225 offset:4608
	ds_read_b128 v[196:199], v225 offset:4640
	ds_read_b128 v[200:203], v225 offset:4672
	ds_read_b128 v[204:207], v225 offset:4704
	s_waitcnt lgkmcnt(0)
	v_cmp_ne_u32_e64 s[20:21], 0, v224
	v_mfma_f32_32x32x16_f16 v[64:79], v[176:179], v[128:131], 0
	v_mfma_f32_32x32x16_f16 v[64:79], v[180:183], v[132:135], v[64:79]
	v_mfma_f32_32x32x16_f16 v[64:79], v[184:187], v[136:139], v[64:79]
	v_mfma_f32_32x32x16_f16 v[64:79], v[188:191], v[140:143], v[64:79]
	v_mfma_f32_32x32x16_f16 v[80:95], v[192:195], v[128:131], 0
	v_mfma_f32_32x32x16_f16 v[80:95], v[196:199], v[132:135], v[80:95]
	v_mfma_f32_32x32x16_f16 v[80:95], v[200:203], v[136:139], v[80:95]
	v_mfma_f32_32x32x16_f16 v[80:95], v[204:207], v[140:143], v[80:95]
	s_nop 15
	s_nop 3
	s_cmp_eq_u64 s[20:21], -1
	s_cbranch_scc1 .Lpro_nomask_A
	v_lshrrev_b32_e64 v235, v234, s20
	v_bfe_u32 v236, v235, 0, 1
	v_cvt_f32_u32_e32 v236, v236
	v_sub_f32_e32 v236, 1.0, v236
	v_fmac_f32_e32 v64, s35, v236
	v_bfe_u32 v236, v235, 1, 1
	v_cvt_f32_u32_e32 v236, v236
	v_sub_f32_e32 v236, 1.0, v236
	v_fmac_f32_e32 v65, s35, v236
	v_bfe_u32 v236, v235, 2, 1
	v_cvt_f32_u32_e32 v236, v236
	v_sub_f32_e32 v236, 1.0, v236
	v_fmac_f32_e32 v66, s35, v236
	v_bfe_u32 v236, v235, 3, 1
	v_cvt_f32_u32_e32 v236, v236
	v_sub_f32_e32 v236, 1.0, v236
	v_fmac_f32_e32 v67, s35, v236
	v_bfe_u32 v236, v235, 8, 1
	v_cvt_f32_u32_e32 v236, v236
	v_sub_f32_e32 v236, 1.0, v236
	v_fmac_f32_e32 v68, s35, v236
	v_bfe_u32 v236, v235, 9, 1
	v_cvt_f32_u32_e32 v236, v236
	v_sub_f32_e32 v236, 1.0, v236
	v_fmac_f32_e32 v69, s35, v236
	v_bfe_u32 v236, v235, 10, 1
	v_cvt_f32_u32_e32 v236, v236
	v_sub_f32_e32 v236, 1.0, v236
	v_fmac_f32_e32 v70, s35, v236
	v_bfe_u32 v236, v235, 11, 1
	v_cvt_f32_u32_e32 v236, v236
	v_sub_f32_e32 v236, 1.0, v236
	v_fmac_f32_e32 v71, s35, v236
	v_bfe_u32 v236, v235, 16, 1
	v_cvt_f32_u32_e32 v236, v236
	v_sub_f32_e32 v236, 1.0, v236
	v_fmac_f32_e32 v72, s35, v236
	v_bfe_u32 v236, v235, 17, 1
	v_cvt_f32_u32_e32 v236, v236
	v_sub_f32_e32 v236, 1.0, v236
	v_fmac_f32_e32 v73, s35, v236
	v_bfe_u32 v236, v235, 18, 1
	v_cvt_f32_u32_e32 v236, v236
	v_sub_f32_e32 v236, 1.0, v236
	v_fmac_f32_e32 v74, s35, v236
	v_bfe_u32 v236, v235, 19, 1
	v_cvt_f32_u32_e32 v236, v236
	v_sub_f32_e32 v236, 1.0, v236
	v_fmac_f32_e32 v75, s35, v236
	v_bfe_u32 v236, v235, 24, 1
	v_cvt_f32_u32_e32 v236, v236
	v_sub_f32_e32 v236, 1.0, v236
	v_fmac_f32_e32 v76, s35, v236
	v_bfe_u32 v236, v235, 25, 1
	v_cvt_f32_u32_e32 v236, v236
	v_sub_f32_e32 v236, 1.0, v236
	v_fmac_f32_e32 v77, s35, v236
	v_bfe_u32 v236, v235, 26, 1
	v_cvt_f32_u32_e32 v236, v236
	v_sub_f32_e32 v236, 1.0, v236
	v_fmac_f32_e32 v78, s35, v236
	v_bfe_u32 v236, v235, 27, 1
	v_cvt_f32_u32_e32 v236, v236
	v_sub_f32_e32 v236, 1.0, v236
	v_fmac_f32_e32 v79, s35, v236
	v_lshrrev_b32_e64 v235, v234, s21
	v_bfe_u32 v236, v235, 0, 1
	v_cvt_f32_u32_e32 v236, v236
	v_sub_f32_e32 v236, 1.0, v236
	v_fmac_f32_e32 v80, s35, v236
	v_bfe_u32 v236, v235, 1, 1
	v_cvt_f32_u32_e32 v236, v236
	v_sub_f32_e32 v236, 1.0, v236
	v_fmac_f32_e32 v81, s35, v236
	v_bfe_u32 v236, v235, 2, 1
	v_cvt_f32_u32_e32 v236, v236
	v_sub_f32_e32 v236, 1.0, v236
	v_fmac_f32_e32 v82, s35, v236
	v_bfe_u32 v236, v235, 3, 1
	v_cvt_f32_u32_e32 v236, v236
	v_sub_f32_e32 v236, 1.0, v236
	v_fmac_f32_e32 v83, s35, v236
	v_bfe_u32 v236, v235, 8, 1
	v_cvt_f32_u32_e32 v236, v236
	v_sub_f32_e32 v236, 1.0, v236
	v_fmac_f32_e32 v84, s35, v236
	v_bfe_u32 v236, v235, 9, 1
	v_cvt_f32_u32_e32 v236, v236
	v_sub_f32_e32 v236, 1.0, v236
	v_fmac_f32_e32 v85, s35, v236
	v_bfe_u32 v236, v235, 10, 1
	v_cvt_f32_u32_e32 v236, v236
	v_sub_f32_e32 v236, 1.0, v236
	v_fmac_f32_e32 v86, s35, v236
	v_bfe_u32 v236, v235, 11, 1
	v_cvt_f32_u32_e32 v236, v236
	v_sub_f32_e32 v236, 1.0, v236
	v_fmac_f32_e32 v87, s35, v236
	v_bfe_u32 v236, v235, 16, 1
	v_cvt_f32_u32_e32 v236, v236
	v_sub_f32_e32 v236, 1.0, v236
	v_fmac_f32_e32 v88, s35, v236
	v_bfe_u32 v236, v235, 17, 1
	v_cvt_f32_u32_e32 v236, v236
	v_sub_f32_e32 v236, 1.0, v236
	v_fmac_f32_e32 v89, s35, v236
	v_bfe_u32 v236, v235, 18, 1
	v_cvt_f32_u32_e32 v236, v236
	v_sub_f32_e32 v236, 1.0, v236
	v_fmac_f32_e32 v90, s35, v236
	v_bfe_u32 v236, v235, 19, 1
	v_cvt_f32_u32_e32 v236, v236
	v_sub_f32_e32 v236, 1.0, v236
	v_fmac_f32_e32 v91, s35, v236
	v_bfe_u32 v236, v235, 24, 1
	v_cvt_f32_u32_e32 v236, v236
	v_sub_f32_e32 v236, 1.0, v236
	v_fmac_f32_e32 v92, s35, v236
	v_bfe_u32 v236, v235, 25, 1
	v_cvt_f32_u32_e32 v236, v236
	v_sub_f32_e32 v236, 1.0, v236
	v_fmac_f32_e32 v93, s35, v236
	v_bfe_u32 v236, v235, 26, 1
	v_cvt_f32_u32_e32 v236, v236
	v_sub_f32_e32 v236, 1.0, v236
	v_fmac_f32_e32 v94, s35, v236
	v_bfe_u32 v236, v235, 27, 1
	v_cvt_f32_u32_e32 v236, v236
	v_sub_f32_e32 v236, 1.0, v236
	v_fmac_f32_e32 v95, s35, v236
.Lpro_nomask_A:
	v_max3_f32 v235, v64, v65, v66
	v_max3_f32 v235, v235, v67, v68
	v_max3_f32 v235, v235, v69, v70
	v_max3_f32 v235, v235, v71, v72
	v_max3_f32 v235, v235, v73, v74
	v_max3_f32 v235, v235, v75, v76
	v_max3_f32 v235, v235, v77, v78
	v_max3_f32 v235, v235, v79, v80
	v_max3_f32 v235, v235, v81, v82
	v_max3_f32 v235, v235, v83, v84
	v_max3_f32 v235, v235, v85, v86
	v_max3_f32 v235, v235, v87, v88
	v_max3_f32 v235, v235, v89, v90
	v_max3_f32 v235, v235, v91, v92
	v_max3_f32 v235, v235, v93, v94
	v_max_f32_e32 v235, v235, v95
	v_mov_b32_e32 v236, v235
	s_nop 1
	v_permlane32_swap_b32_e32 v235, v236
	v_max_f32_e32 v235, v235, v236
	v_sub_f32_e32 v96, 0, v235
	v_sub_f32_e32 v97, 0, v235
	v_sub_f32_e32 v98, 0, v235
	v_sub_f32_e32 v99, 0, v235
	v_sub_f32_e32 v100, 0, v235
	v_sub_f32_e32 v101, 0, v235
	v_sub_f32_e32 v102, 0, v235
	v_sub_f32_e32 v103, 0, v235
	v_sub_f32_e32 v104, 0, v235
	v_sub_f32_e32 v105, 0, v235
	v_sub_f32_e32 v106, 0, v235
	v_sub_f32_e32 v107, 0, v235
	v_sub_f32_e32 v108, 0, v235
	v_sub_f32_e32 v109, 0, v235
	v_sub_f32_e32 v110, 0, v235
	v_sub_f32_e32 v111, 0, v235
	v_sub_f32_e32 v64, v64, v235
	v_sub_f32_e32 v65, v65, v235
	v_sub_f32_e32 v66, v66, v235
	v_sub_f32_e32 v67, v67, v235
	v_sub_f32_e32 v68, v68, v235
	v_sub_f32_e32 v69, v69, v235
	v_sub_f32_e32 v70, v70, v235
	v_sub_f32_e32 v71, v71, v235
	v_sub_f32_e32 v72, v72, v235
	v_sub_f32_e32 v73, v73, v235
	v_sub_f32_e32 v74, v74, v235
	v_sub_f32_e32 v75, v75, v235
	v_sub_f32_e32 v76, v76, v235
	v_sub_f32_e32 v77, v77, v235
	v_sub_f32_e32 v78, v78, v235
	v_sub_f32_e32 v79, v79, v235
	v_mov_b32_e32 v0, 0
	v_mov_b32_e32 v1, 0
	v_mov_b32_e32 v2, 0
	v_mov_b32_e32 v3, 0
	v_mov_b32_e32 v4, 0
	v_mov_b32_e32 v5, 0
	v_mov_b32_e32 v6, 0
	v_mov_b32_e32 v7, 0
	v_mov_b32_e32 v8, 0
	v_mov_b32_e32 v9, 0
	v_mov_b32_e32 v10, 0
	v_mov_b32_e32 v11, 0
	v_mov_b32_e32 v12, 0
	v_mov_b32_e32 v13, 0
	v_mov_b32_e32 v14, 0
	v_mov_b32_e32 v15, 0
	v_mov_b32_e32 v16, 0
	v_mov_b32_e32 v17, 0
	v_mov_b32_e32 v18, 0
	v_mov_b32_e32 v19, 0
	v_mov_b32_e32 v20, 0
	v_mov_b32_e32 v21, 0
	v_mov_b32_e32 v22, 0
	v_mov_b32_e32 v23, 0
	v_mov_b32_e32 v24, 0
	v_mov_b32_e32 v25, 0
	v_mov_b32_e32 v26, 0
	v_mov_b32_e32 v27, 0
	v_mov_b32_e32 v28, 0
	v_mov_b32_e32 v29, 0
	v_mov_b32_e32 v30, 0
	v_mov_b32_e32 v31, 0
	v_mov_b32_e32 v232, 0
	s_cmp_lt_u32 s17, 4
	s_cbranch_scc1 .Lnoprio
	s_setprio 1
.Lnoprio:
	s_waitcnt vmcnt(8)
	v_cmp_ne_u32_e64 s[20:21], 0, v224
	s_add_u32 s31, s23, 1
	s_and_b32 s31, s31, 31
	s_lshl_b32 s31, s31, 8
	s_add_u32 s26, s31, s22
	s_add_u32 s31, s23, 3
	s_and_b32 s31, s31, 31
	s_mul_i32 s31, s31, 0xc0000
	s_add_u32 s24, s31, s18
	s_add_u32 s31, s23, 2
	s_and_b32 s31, s31, 31
	s_mul_i32 s31, s31, 0xc0000
	s_add_u32 s25, s31, s19
	s_cmp_eq_u64 s[20:21], -1
	s_cselect_b32 s34, s37, s38
	ds_read_b128 v[176:179], v225 offset:4608
	s_add_u32 s31, s29, 0xc00000
	buffer_load_dwordx4 v[32:35], v243, s[4:7], s31 offen nt
	s_add_u32 s31, s29, 0xc0c000
	buffer_load_dwordx4 v[36:39], v243, s[4:7], s31 offen nt
	buffer_load_dword v224, v230, s[8:11], s26 offen
	v_exp_f32_e32 v64, v64
	v_exp_f32_e32 v65, v65
	v_cvt_pk_f16_f32 v208, v208, v209
	v_cvt_pk_f16_f32 v209, v210, v211
	ds_read_b128 v[180:183], v225 offset:4640
	v_exp_f32_e32 v66, v66
	v_exp_f32_e32 v67, v67
	v_cvt_pk_f16_f32 v212, v212, v213
	v_cvt_pk_f16_f32 v160, v64, v65
	v_add_f32_e32 v64, v64, v65
	v_cvt_pk_f16_f32 v213, v214, v215
	ds_write_b64 v227, v[208:209] offset:18432
	ds_write_b64 v227, v[212:213] offset:23040
	ds_read_b128 v[184:187], v225 offset:4672
	v_exp_f32_e32 v68, v68
	v_exp_f32_e32 v69, v69
	v_cvt_pk_f16_f32 v161, v66, v67
	v_add_f32_e32 v66, v66, v67
	ds_read_b128 v[188:191], v225 offset:4704
	v_exp_f32_e32 v70, v70
	v_exp_f32_e32 v71, v71
	v_cvt_pk_f16_f32 v162, v68, v69
	v_add_f32_e32 v68, v68, v69
	v_add_f32_e32 v231, v64, v66
	ds_read_b128 v[192:195], v226 offset:0
	v_exp_f32_e32 v72, v72
	v_exp_f32_e32 v73, v73
	v_cvt_pk_f16_f32 v163, v70, v71
	v_add_f32_e32 v70, v70, v71
	v_add_f32_e32 v231, v231, v68
	ds_read_b128 v[196:199], v226 offset:4608
	v_exp_f32_e32 v74, v74
	v_exp_f32_e32 v75, v75
	v_cvt_pk_f16_f32 v164, v72, v73
	v_add_f32_e32 v72, v72, v73
	v_add_f32_e32 v231, v231, v70
	ds_read_b128 v[200:203], v226 offset:32
	v_exp_f32_e32 v76, v76
	v_exp_f32_e32 v77, v77
	v_cvt_pk_f16_f32 v165, v74, v75
	v_add_f32_e32 v74, v74, v75
	v_add_f32_e32 v231, v231, v72
	ds_read_b128 v[204:207], v226 offset:4640
	v_exp_f32_e32 v78, v78
	v_exp_f32_e32 v79, v79
	v_cvt_pk_f16_f32 v166, v76, v77
	v_add_f32_e32 v76, v76, v77
	v_add_f32_e32 v231, v231, v74
	v_cvt_pk_f16_f32 v167, v78, v79
	v_add_f32_e32 v78, v78, v79
	v_add_f32_e32 v231, v231, v76
	v_add_f32_e32 v231, v231, v78
	v_cmp_nge_f32_e32 vcc, s34, v231
	s_cbranch_vccnz .Lovf_a00p
.Lovfret_a00p:
	v_add_f32_e32 v232, v232, v231
	s_waitcnt lgkmcnt(4)
	v_mfma_f32_32x32x16_f16 v[64:79], v[176:179], v[128:131], v[96:111]
	v_mfma_f32_32x32x16_f16 v[64:79], v[180:183], v[132:135], v[64:79]
	buffer_load_dwordx4 v[208:211], v229, s[4:7], s24 offen
	v_mfma_f32_32x32x16_f16 v[64:79], v[184:187], v[136:139], v[64:79]
	s_add_u32 s31, s24, 0x60000
	buffer_load_dwordx4 v[212:215], v229, s[4:7], s31 offen
	v_mfma_f32_32x32x16_f16 v[64:79], v[188:191], v[140:143], v[64:79]
	s_waitcnt lgkmcnt(0)
	v_mfma_f32_32x32x16_f16 v[0:15], v[192:195], v[160:163], v[0:15]
	v_mfma_f32_32x32x16_f16 v[16:31], v[196:199], v[160:163], v[16:31]
	v_mfma_f32_32x32x16_f16 v[0:15], v[200:203], v[164:167], v[0:15]
	v_mfma_f32_32x32x16_f16 v[16:31], v[204:207], v[164:167], v[16:31]
	s_nop 7
	ds_read_b128 v[176:179], v225 offset:9216
	s_waitcnt vmcnt(5)
	v_exp_f32_e32 v64, v64
	v_exp_f32_e32 v65, v65
	v_cvt_pk_f16_f32 v216, v216, v217
	v_cvt_pk_f16_f32 v217, v218, v219
	ds_read_b128 v[180:183], v225 offset:9248
	v_exp_f32_e32 v66, v66
	v_exp_f32_e32 v67, v67
	v_cvt_pk_f16_f32 v218, v220, v221
	v_cvt_pk_f16_f32 v160, v64, v65
	v_add_f32_e32 v64, v64, v65
	v_cvt_pk_f16_f32 v219, v222, v223
	ds_write_b128 v228, v[216:219] offset:9216
	ds_read_b128 v[184:187], v225 offset:9280
	v_exp_f32_e32 v68, v68
	v_exp_f32_e32 v69, v69
	v_cvt_pk_f16_f32 v161, v66, v67
	v_add_f32_e32 v66, v66, v67
	ds_read_b128 v[188:191], v225 offset:9312
	v_exp_f32_e32 v70, v70
	v_exp_f32_e32 v71, v71
	v_cvt_pk_f16_f32 v162, v68, v69
	v_add_f32_e32 v68, v68, v69
	v_add_f32_e32 v231, v64, v66
	ds_read_b128 v[192:195], v226 offset:64
	v_exp_f32_e32 v72, v72
	v_exp_f32_e32 v73, v73
	v_cvt_pk_f16_f32 v163, v70, v71
	v_add_f32_e32 v70, v70, v71
	v_add_f32_e32 v231, v231, v68
	ds_read_b128 v[196:199], v226 offset:4672
	v_exp_f32_e32 v74, v74
	v_exp_f32_e32 v75, v75
	v_cvt_pk_f16_f32 v164, v72, v73
	v_add_f32_e32 v72, v72, v73
	v_add_f32_e32 v231, v231, v70
	ds_read_b128 v[200:203], v226 offset:96
	v_exp_f32_e32 v76, v76
	v_exp_f32_e32 v77, v77
	v_cvt_pk_f16_f32 v165, v74, v75
	v_add_f32_e32 v74, v74, v75
	v_add_f32_e32 v231, v231, v72
	ds_read_b128 v[204:207], v226 offset:4704
	v_exp_f32_e32 v78, v78
	v_exp_f32_e32 v79, v79
	v_cvt_pk_f16_f32 v166, v76, v77
	v_add_f32_e32 v76, v76, v77
	v_add_f32_e32 v231, v231, v74
	v_cvt_pk_f16_f32 v167, v78, v79
	v_add_f32_e32 v78, v78, v79
	v_add_f32_e32 v231, v231, v76
	v_add_f32_e32 v231, v231, v78
	v_cmp_nge_f32_e32 vcc, s34, v231
	s_cbranch_vccnz .Lovf_a01p
.Lovfret_a01p:
	v_add_f32_e32 v232, v232, v231
	s_waitcnt lgkmcnt(4)
	v_mfma_f32_32x32x16_f16 v[64:79], v[176:179], v[128:131], v[96:111]
	buffer_load_dword v216, v230, s[4:7], s25 offen
	v_mfma_f32_32x32x16_f16 v[64:79], v[180:183], v[132:135], v[64:79]
	s_add_u32 s31, s25, 0x3000
	buffer_load_dword v217, v230, s[4:7], s31 offen
	v_mfma_f32_32x32x16_f16 v[64:79], v[184:187], v[136:139], v[64:79]
	s_add_u32 s31, s25, 0x6000
	buffer_load_dword v218, v230, s[4:7], s31 offen
	v_mfma_f32_32x32x16_f16 v[64:79], v[188:191], v[140:143], v[64:79]
	s_add_u32 s31, s25, 0x9000
	buffer_load_dword v219, v230, s[4:7], s31 offen
	s_waitcnt lgkmcnt(0)
	v_mfma_f32_32x32x16_f16 v[0:15], v[192:195], v[160:163], v[0:15]
	s_add_u32 s31, s25, 0x18000
	buffer_load_dword v220, v230, s[4:7], s31 offen
	v_mfma_f32_32x32x16_f16 v[16:31], v[196:199], v[160:163], v[16:31]
	s_add_u32 s31, s25, 0x1b000
	buffer_load_dword v221, v230, s[4:7], s31 offen
	v_mfma_f32_32x32x16_f16 v[0:15], v[200:203], v[164:167], v[0:15]
	s_add_u32 s31, s25, 0x1e000
	buffer_load_dword v222, v230, s[4:7], s31 offen
	v_mfma_f32_32x32x16_f16 v[16:31], v[204:207], v[164:167], v[16:31]
	s_add_u32 s31, s25, 0x21000
	buffer_load_dword v223, v230, s[4:7], s31 offen
	s_nop 7
	s_waitcnt lgkmcnt(6)
	s_barrier
	s_add_u32 s23, s23, 1
	s_waitcnt vmcnt(8)
	v_cmp_ne_u32_e64 s[20:21], 0, v224
	s_add_u32 s31, s23, 1
	s_and_b32 s31, s31, 31
	s_lshl_b32 s31, s31, 8
	s_add_u32 s26, s31, s22
	s_add_u32 s31, s23, 3
	s_and_b32 s31, s31, 31
	s_mul_i32 s31, s31, 0xc0000
	s_add_u32 s24, s31, s18
	s_add_u32 s31, s23, 2
	s_and_b32 s31, s31, 31
	s_mul_i32 s31, s31, 0xc0000
	s_add_u32 s25, s31, s19
	s_cmp_eq_u64 s[20:21], -1
	s_cselect_b32 s34, s37, s38
	ds_read_b128 v[176:179], v225 offset:13824
	s_add_u32 s31, s29, 0xc18000
	buffer_load_dwordx4 v[40:43], v243, s[4:7], s31 offen nt
	s_add_u32 s31, s29, 0xc24000
	buffer_load_dwordx4 v[44:47], v243, s[4:7], s31 offen nt
	buffer_load_dword v224, v230, s[8:11], s26 offen
	v_exp_f32_e32 v64, v64
	v_exp_f32_e32 v65, v65
	v_cvt_pk_f16_f32 v208, v208, v209
	v_cvt_pk_f16_f32 v209, v210, v211
	ds_read_b128 v[180:183], v225 offset:13856
	v_exp_f32_e32 v66, v66
	v_exp_f32_e32 v67, v67
	v_cvt_pk_f16_f32 v212, v212, v213
	v_cvt_pk_f16_f32 v160, v64, v65
	v_add_f32_e32 v64, v64, v65
	v_cvt_pk_f16_f32 v213, v214, v215
	ds_write_b64 v227, v[208:209] offset:27648
	ds_write_b64 v227, v[212:213] offset:32256
	ds_read_b128 v[184:187], v225 offset:13888
	v_exp_f32_e32 v68, v68
	v_exp_f32_e32 v69, v69
	v_cvt_pk_f16_f32 v161, v66, v67
	v_add_f32_e32 v66, v66, v67
	ds_read_b128 v[188:191], v225 offset:13920
	v_exp_f32_e32 v70, v70
	v_exp_f32_e32 v71, v71
	v_cvt_pk_f16_f32 v162, v68, v69
	v_add_f32_e32 v68, v68, v69
	v_add_f32_e32 v231, v64, v66
	ds_read_b128 v[192:195], v226 offset:9216
	v_exp_f32_e32 v72, v72
	v_exp_f32_e32 v73, v73
	v_cvt_pk_f16_f32 v163, v70, v71
	v_add_f32_e32 v70, v70, v71
	v_add_f32_e32 v231, v231, v68
	ds_read_b128 v[196:199], v226 offset:13824
	v_exp_f32_e32 v74, v74
	v_exp_f32_e32 v75, v75
	v_cvt_pk_f16_f32 v164, v72, v73
	v_add_f32_e32 v72, v72, v73
	v_add_f32_e32 v231, v231, v70
	ds_read_b128 v[200:203], v226 offset:9248
	v_exp_f32_e32 v76, v76
	v_exp_f32_e32 v77, v77
	v_cvt_pk_f16_f32 v165, v74, v75
	v_add_f32_e32 v74, v74, v75
	v_add_f32_e32 v231, v231, v72
	ds_read_b128 v[204:207], v226 offset:13856
	v_exp_f32_e32 v78, v78
	v_exp_f32_e32 v79, v79
	v_cvt_pk_f16_f32 v166, v76, v77
	v_add_f32_e32 v76, v76, v77
	v_add_f32_e32 v231, v231, v74
	v_cvt_pk_f16_f32 v167, v78, v79
	v_add_f32_e32 v78, v78, v79
	v_add_f32_e32 v231, v231, v76
	v_add_f32_e32 v231, v231, v78
	v_cmp_nge_f32_e32 vcc, s34, v231
	s_cbranch_vccnz .Lovf_a10p
.Lovfret_a10p:
	v_add_f32_e32 v232, v232, v231
	s_waitcnt lgkmcnt(4)
	v_mfma_f32_32x32x16_f16 v[64:79], v[176:179], v[128:131], v[96:111]
	v_mfma_f32_32x32x16_f16 v[64:79], v[180:183], v[132:135], v[64:79]
	buffer_load_dwordx4 v[208:211], v229, s[4:7], s24 offen
	v_mfma_f32_32x32x16_f16 v[64:79], v[184:187], v[136:139], v[64:79]
	s_add_u32 s31, s24, 0x60000
	buffer_load_dwordx4 v[212:215], v229, s[4:7], s31 offen
	v_mfma_f32_32x32x16_f16 v[64:79], v[188:191], v[140:143], v[64:79]
	s_waitcnt lgkmcnt(0)
	v_mfma_f32_32x32x16_f16 v[0:15], v[192:195], v[160:163], v[0:15]
	v_mfma_f32_32x32x16_f16 v[16:31], v[196:199], v[160:163], v[16:31]
	v_mfma_f32_32x32x16_f16 v[0:15], v[200:203], v[164:167], v[0:15]
	v_mfma_f32_32x32x16_f16 v[16:31], v[204:207], v[164:167], v[16:31]
	s_nop 7
	ds_read_b128 v[176:179], v225 offset:18432
	s_waitcnt vmcnt(5)
	v_exp_f32_e32 v64, v64
	v_exp_f32_e32 v65, v65
	v_cvt_pk_f16_f32 v216, v216, v217
	v_cvt_pk_f16_f32 v217, v218, v219
	ds_read_b128 v[180:183], v225 offset:18464
	v_exp_f32_e32 v66, v66
	v_exp_f32_e32 v67, v67
	v_cvt_pk_f16_f32 v218, v220, v221
	v_cvt_pk_f16_f32 v160, v64, v65
	v_add_f32_e32 v64, v64, v65
	v_cvt_pk_f16_f32 v219, v222, v223
	ds_write_b128 v228, v[216:219] offset:18432
	ds_read_b128 v[184:187], v225 offset:18496
	v_exp_f32_e32 v68, v68
	v_exp_f32_e32 v69, v69
	v_cvt_pk_f16_f32 v161, v66, v67
	v_add_f32_e32 v66, v66, v67
	ds_read_b128 v[188:191], v225 offset:18528
	v_exp_f32_e32 v70, v70
	v_exp_f32_e32 v71, v71
	v_cvt_pk_f16_f32 v162, v68, v69
	v_add_f32_e32 v68, v68, v69
	v_add_f32_e32 v231, v64, v66
	ds_read_b128 v[192:195], v226 offset:9280
	v_exp_f32_e32 v72, v72
	v_exp_f32_e32 v73, v73
	v_cvt_pk_f16_f32 v163, v70, v71
	v_add_f32_e32 v70, v70, v71
	v_add_f32_e32 v231, v231, v68
	ds_read_b128 v[196:199], v226 offset:13888
	v_exp_f32_e32 v74, v74
	v_exp_f32_e32 v75, v75
	v_cvt_pk_f16_f32 v164, v72, v73
	v_add_f32_e32 v72, v72, v73
	v_add_f32_e32 v231, v231, v70
	ds_read_b128 v[200:203], v226 offset:9312
	v_exp_f32_e32 v76, v76
	v_exp_f32_e32 v77, v77
	v_cvt_pk_f16_f32 v165, v74, v75
	v_add_f32_e32 v74, v74, v75
	v_add_f32_e32 v231, v231, v72
	ds_read_b128 v[204:207], v226 offset:13920
	v_exp_f32_e32 v78, v78
	v_exp_f32_e32 v79, v79
	v_cvt_pk_f16_f32 v166, v76, v77
	v_add_f32_e32 v76, v76, v77
	v_add_f32_e32 v231, v231, v74
	v_cvt_pk_f16_f32 v167, v78, v79
	v_add_f32_e32 v78, v78, v79
	v_add_f32_e32 v231, v231, v76
	v_add_f32_e32 v231, v231, v78
	v_cmp_nge_f32_e32 vcc, s34, v231
	s_cbranch_vccnz .Lovf_a11p
.Lovfret_a11p:
	v_add_f32_e32 v232, v232, v231
	s_waitcnt lgkmcnt(4)
	v_mfma_f32_32x32x16_f16 v[64:79], v[176:179], v[128:131], v[96:111]
	buffer_load_dword v216, v230, s[4:7], s25 offen
	v_mfma_f32_32x32x16_f16 v[64:79], v[180:183], v[132:135], v[64:79]
	s_add_u32 s31, s25, 0x3000
	buffer_load_dword v217, v230, s[4:7], s31 offen
	v_mfma_f32_32x32x16_f16 v[64:79], v[184:187], v[136:139], v[64:79]
	s_add_u32 s31, s25, 0x6000
	buffer_load_dword v218, v230, s[4:7], s31 offen
	v_mfma_f32_32x32x16_f16 v[64:79], v[188:191], v[140:143], v[64:79]
	s_add_u32 s31, s25, 0x9000
	buffer_load_dword v219, v230, s[4:7], s31 offen
	s_waitcnt lgkmcnt(0)
	v_mfma_f32_32x32x16_f16 v[0:15], v[192:195], v[160:163], v[0:15]
	s_add_u32 s31, s25, 0x18000
	buffer_load_dword v220, v230, s[4:7], s31 offen
	v_mfma_f32_32x32x16_f16 v[16:31], v[196:199], v[160:163], v[16:31]
	s_add_u32 s31, s25, 0x1b000
	buffer_load_dword v221, v230, s[4:7], s31 offen
	v_mfma_f32_32x32x16_f16 v[0:15], v[200:203], v[164:167], v[0:15]
	s_add_u32 s31, s25, 0x1e000
	buffer_load_dword v222, v230, s[4:7], s31 offen
	v_mfma_f32_32x32x16_f16 v[16:31], v[204:207], v[164:167], v[16:31]
	s_add_u32 s31, s25, 0x21000
	buffer_load_dword v223, v230, s[4:7], s31 offen
	s_nop 7
	s_waitcnt lgkmcnt(6)
	s_barrier
	s_add_u32 s23, s23, 1
	s_waitcnt vmcnt(8)
	v_cmp_ne_u32_e64 s[20:21], 0, v224
	s_add_u32 s31, s23, 1
	s_and_b32 s31, s31, 31
	s_lshl_b32 s31, s31, 8
	s_add_u32 s26, s31, s22
	s_add_u32 s31, s23, 3
	s_and_b32 s31, s31, 31
	s_mul_i32 s31, s31, 0xc0000
	s_add_u32 s24, s31, s18
	s_add_u32 s31, s23, 2
	s_and_b32 s31, s31, 31
	s_mul_i32 s31, s31, 0xc0000
	s_add_u32 s25, s31, s19
	s_cmp_eq_u64 s[20:21], -1
	s_cselect_b32 s34, s37, s38
	ds_read_b128 v[176:179], v225 offset:23040
	s_add_u32 s31, s29, 0xc30000
	buffer_load_dwordx4 v[48:51], v243, s[4:7], s31 offen nt
	s_add_u32 s31, s29, 0xc3c000
	buffer_load_dwordx4 v[52:55], v243, s[4:7], s31 offen nt
	buffer_load_dword v224, v230, s[8:11], s26 offen
	v_exp_f32_e32 v64, v64
	v_exp_f32_e32 v65, v65
	v_cvt_pk_f16_f32 v208, v208, v209
	v_cvt_pk_f16_f32 v209, v210, v211
	ds_read_b128 v[180:183], v225 offset:23072
	v_exp_f32_e32 v66, v66
	v_exp_f32_e32 v67, v67
	v_cvt_pk_f16_f32 v212, v212, v213
	v_cvt_pk_f16_f32 v160, v64, v65
	v_add_f32_e32 v64, v64, v65
	v_cvt_pk_f16_f32 v213, v214, v215
	ds_write_b64 v227, v[208:209] offset:0
	ds_write_b64 v227, v[212:213] offset:4608
	ds_read_b128 v[184:187], v225 offset:23104
	v_exp_f32_e32 v68, v68
	v_exp_f32_e32 v69, v69
	v_cvt_pk_f16_f32 v161, v66, v67
	v_add_f32_e32 v66, v66, v67
	ds_read_b128 v[188:191], v225 offset:23136
	v_exp_f32_e32 v70, v70
	v_exp_f32_e32 v71, v71
	v_cvt_pk_f16_f32 v162, v68, v69
	v_add_f32_e32 v68, v68, v69
	v_add_f32_e32 v231, v64, v66
	ds_read_b128 v[192:195], v226 offset:18432
	v_exp_f32_e32 v72, v72
	v_exp_f32_e32 v73, v73
	v_cvt_pk_f16_f32 v163, v70, v71
	v_add_f32_e32 v70, v70, v71
	v_add_f32_e32 v231, v231, v68
	ds_read_b128 v[196:199], v226 offset:23040
	v_exp_f32_e32 v74, v74
	v_exp_f32_e32 v75, v75
	v_cvt_pk_f16_f32 v164, v72, v73
	v_add_f32_e32 v72, v72, v73
	v_add_f32_e32 v231, v231, v70
	ds_read_b128 v[200:203], v226 offset:18464
	v_exp_f32_e32 v76, v76
	v_exp_f32_e32 v77, v77
	v_cvt_pk_f16_f32 v165, v74, v75
	v_add_f32_e32 v74, v74, v75
	v_add_f32_e32 v231, v231, v72
	ds_read_b128 v[204:207], v226 offset:23072
	v_exp_f32_e32 v78, v78
	v_exp_f32_e32 v79, v79
	v_cvt_pk_f16_f32 v166, v76, v77
	v_add_f32_e32 v76, v76, v77
	v_add_f32_e32 v231, v231, v74
	v_cvt_pk_f16_f32 v167, v78, v79
	v_add_f32_e32 v78, v78, v79
	v_add_f32_e32 v231, v231, v76
	v_add_f32_e32 v231, v231, v78
	v_cmp_nge_f32_e32 vcc, s34, v231
	s_cbranch_vccnz .Lovf_a20p
.Lovfret_a20p:
	v_add_f32_e32 v232, v232, v231
	s_waitcnt lgkmcnt(4)
	v_mfma_f32_32x32x16_f16 v[64:79], v[176:179], v[128:131], v[96:111]
	v_mfma_f32_32x32x16_f16 v[64:79], v[180:183], v[132:135], v[64:79]
	buffer_load_dwordx4 v[208:211], v229, s[4:7], s24 offen
	v_mfma_f32_32x32x16_f16 v[64:79], v[184:187], v[136:139], v[64:79]
	s_add_u32 s31, s24, 0x60000
	buffer_load_dwordx4 v[212:215], v229, s[4:7], s31 offen
	v_mfma_f32_32x32x16_f16 v[64:79], v[188:191], v[140:143], v[64:79]
	s_waitcnt lgkmcnt(0)
	v_mfma_f32_32x32x16_f16 v[0:15], v[192:195], v[160:163], v[0:15]
	v_mfma_f32_32x32x16_f16 v[16:31], v[196:199], v[160:163], v[16:31]
	v_mfma_f32_32x32x16_f16 v[0:15], v[200:203], v[164:167], v[0:15]
	v_mfma_f32_32x32x16_f16 v[16:31], v[204:207], v[164:167], v[16:31]
	s_nop 7
	ds_read_b128 v[176:179], v225 offset:27648
	s_waitcnt vmcnt(5)
	v_exp_f32_e32 v64, v64
	v_exp_f32_e32 v65, v65
	v_cvt_pk_f16_f32 v216, v216, v217
	v_cvt_pk_f16_f32 v217, v218, v219
	ds_read_b128 v[180:183], v225 offset:27680
	v_exp_f32_e32 v66, v66
	v_exp_f32_e32 v67, v67
	v_cvt_pk_f16_f32 v218, v220, v221
	v_cvt_pk_f16_f32 v160, v64, v65
	v_add_f32_e32 v64, v64, v65
	v_cvt_pk_f16_f32 v219, v222, v223
	ds_write_b128 v228, v[216:219] offset:27648
	ds_read_b128 v[184:187], v225 offset:27712
	v_exp_f32_e32 v68, v68
	v_exp_f32_e32 v69, v69
	v_cvt_pk_f16_f32 v161, v66, v67
	v_add_f32_e32 v66, v66, v67
	ds_read_b128 v[188:191], v225 offset:27744
	v_exp_f32_e32 v70, v70
	v_exp_f32_e32 v71, v71
	v_cvt_pk_f16_f32 v162, v68, v69
	v_add_f32_e32 v68, v68, v69
	v_add_f32_e32 v231, v64, v66
	ds_read_b128 v[192:195], v226 offset:18496
	v_exp_f32_e32 v72, v72
	v_exp_f32_e32 v73, v73
	v_cvt_pk_f16_f32 v163, v70, v71
	v_add_f32_e32 v70, v70, v71
	v_add_f32_e32 v231, v231, v68
	ds_read_b128 v[196:199], v226 offset:23104
	v_exp_f32_e32 v74, v74
	v_exp_f32_e32 v75, v75
	v_cvt_pk_f16_f32 v164, v72, v73
	v_add_f32_e32 v72, v72, v73
	v_add_f32_e32 v231, v231, v70
	ds_read_b128 v[200:203], v226 offset:18528
	v_exp_f32_e32 v76, v76
	v_exp_f32_e32 v77, v77
	v_cvt_pk_f16_f32 v165, v74, v75
	v_add_f32_e32 v74, v74, v75
	v_add_f32_e32 v231, v231, v72
	ds_read_b128 v[204:207], v226 offset:23136
	v_exp_f32_e32 v78, v78
	v_exp_f32_e32 v79, v79
	v_cvt_pk_f16_f32 v166, v76, v77
	v_add_f32_e32 v76, v76, v77
	v_add_f32_e32 v231, v231, v74
	v_cvt_pk_f16_f32 v167, v78, v79
	v_add_f32_e32 v78, v78, v79
	v_add_f32_e32 v231, v231, v76
	v_add_f32_e32 v231, v231, v78
	v_cmp_nge_f32_e32 vcc, s34, v231
	s_cbranch_vccnz .Lovf_a21p
.Lovfret_a21p:
	v_add_f32_e32 v232, v232, v231
	s_waitcnt lgkmcnt(4)
	v_mfma_f32_32x32x16_f16 v[64:79], v[176:179], v[128:131], v[96:111]
	buffer_load_dword v216, v230, s[4:7], s25 offen
	v_mfma_f32_32x32x16_f16 v[64:79], v[180:183], v[132:135], v[64:79]
	s_add_u32 s31, s25, 0x3000
	buffer_load_dword v217, v230, s[4:7], s31 offen
	v_mfma_f32_32x32x16_f16 v[64:79], v[184:187], v[136:139], v[64:79]
	s_add_u32 s31, s25, 0x6000
	buffer_load_dword v218, v230, s[4:7], s31 offen
	v_mfma_f32_32x32x16_f16 v[64:79], v[188:191], v[140:143], v[64:79]
	s_add_u32 s31, s25, 0x9000
	buffer_load_dword v219, v230, s[4:7], s31 offen
	s_waitcnt lgkmcnt(0)
	v_mfma_f32_32x32x16_f16 v[0:15], v[192:195], v[160:163], v[0:15]
	s_add_u32 s31, s25, 0x18000
	buffer_load_dword v220, v230, s[4:7], s31 offen
	v_mfma_f32_32x32x16_f16 v[16:31], v[196:199], v[160:163], v[16:31]
	s_add_u32 s31, s25, 0x1b000
	buffer_load_dword v221, v230, s[4:7], s31 offen
	v_mfma_f32_32x32x16_f16 v[0:15], v[200:203], v[164:167], v[0:15]
	s_add_u32 s31, s25, 0x1e000
	buffer_load_dword v222, v230, s[4:7], s31 offen
	v_mfma_f32_32x32x16_f16 v[16:31], v[204:207], v[164:167], v[16:31]
	s_add_u32 s31, s25, 0x21000
	buffer_load_dword v223, v230, s[4:7], s31 offen
	s_nop 7
	s_waitcnt lgkmcnt(6)
	s_barrier
	s_add_u32 s23, s23, 1
	s_waitcnt vmcnt(8)
	v_cmp_ne_u32_e64 s[20:21], 0, v224
	s_add_u32 s31, s23, 1
	s_and_b32 s31, s31, 31
	s_lshl_b32 s31, s31, 8
	s_add_u32 s26, s31, s22
	s_add_u32 s31, s23, 3
	s_and_b32 s31, s31, 31
	s_mul_i32 s31, s31, 0xc0000
	s_add_u32 s24, s31, s18
	s_add_u32 s31, s23, 2
	s_and_b32 s31, s31, 31
	s_mul_i32 s31, s31, 0xc0000
	s_add_u32 s25, s31, s19
	s_cmp_eq_u64 s[20:21], -1
	s_cselect_b32 s34, s37, s38
	ds_read_b128 v[176:179], v225 offset:32256
	s_add_u32 s31, s29, 0xc48000
	buffer_load_dwordx4 v[56:59], v243, s[4:7], s31 offen nt
	s_add_u32 s31, s29, 0xc54000
	buffer_load_dwordx4 v[60:63], v243, s[4:7], s31 offen nt
	buffer_load_dword v224, v230, s[8:11], s26 offen
	v_exp_f32_e32 v64, v64
	v_exp_f32_e32 v65, v65
	v_cvt_pk_f16_f32 v208, v208, v209
	v_cvt_pk_f16_f32 v209, v210, v211
	ds_read_b128 v[180:183], v225 offset:32288
	v_exp_f32_e32 v66, v66
	v_exp_f32_e32 v67, v67
	v_cvt_pk_f16_f32 v212, v212, v213
	v_cvt_pk_f16_f32 v160, v64, v65
	v_add_f32_e32 v64, v64, v65
	v_cvt_pk_f16_f32 v213, v214, v215
	ds_write_b64 v227, v[208:209] offset:9216
	ds_write_b64 v227, v[212:213] offset:13824
	ds_read_b128 v[184:187], v225 offset:32320
	v_exp_f32_e32 v68, v68
	v_exp_f32_e32 v69, v69
	v_cvt_pk_f16_f32 v161, v66, v67
	v_add_f32_e32 v66, v66, v67
	ds_read_b128 v[188:191], v225 offset:32352
	v_exp_f32_e32 v70, v70
	v_exp_f32_e32 v71, v71
	v_cvt_pk_f16_f32 v162, v68, v69
	v_add_f32_e32 v68, v68, v69
	v_add_f32_e32 v231, v64, v66
	ds_read_b128 v[192:195], v226 offset:27648
	v_exp_f32_e32 v72, v72
	v_exp_f32_e32 v73, v73
	v_cvt_pk_f16_f32 v163, v70, v71
	v_add_f32_e32 v70, v70, v71
	v_add_f32_e32 v231, v231, v68
	ds_read_b128 v[196:199], v226 offset:32256
	v_exp_f32_e32 v74, v74
	v_exp_f32_e32 v75, v75
	v_cvt_pk_f16_f32 v164, v72, v73
	v_add_f32_e32 v72, v72, v73
	v_add_f32_e32 v231, v231, v70
	ds_read_b128 v[200:203], v226 offset:27680
	v_exp_f32_e32 v76, v76
	v_exp_f32_e32 v77, v77
	v_cvt_pk_f16_f32 v165, v74, v75
	v_add_f32_e32 v74, v74, v75
	v_add_f32_e32 v231, v231, v72
	ds_read_b128 v[204:207], v226 offset:32288
	v_exp_f32_e32 v78, v78
	v_exp_f32_e32 v79, v79
	v_cvt_pk_f16_f32 v166, v76, v77
	v_add_f32_e32 v76, v76, v77
	v_add_f32_e32 v231, v231, v74
	v_cvt_pk_f16_f32 v167, v78, v79
	v_add_f32_e32 v78, v78, v79
	v_add_f32_e32 v231, v231, v76
	v_add_f32_e32 v231, v231, v78
	v_cmp_nge_f32_e32 vcc, s34, v231
	s_cbranch_vccnz .Lovf_a30p
.Lovfret_a30p:
	v_add_f32_e32 v232, v232, v231
	s_waitcnt lgkmcnt(4)
	v_mfma_f32_32x32x16_f16 v[64:79], v[176:179], v[128:131], v[96:111]
	v_mfma_f32_32x32x16_f16 v[64:79], v[180:183], v[132:135], v[64:79]
	buffer_load_dwordx4 v[208:211], v229, s[4:7], s24 offen
	v_mfma_f32_32x32x16_f16 v[64:79], v[184:187], v[136:139], v[64:79]
	s_add_u32 s31, s24, 0x60000
	buffer_load_dwordx4 v[212:215], v229, s[4:7], s31 offen
	v_mfma_f32_32x32x16_f16 v[64:79], v[188:191], v[140:143], v[64:79]
	s_waitcnt lgkmcnt(0)
	v_mfma_f32_32x32x16_f16 v[0:15], v[192:195], v[160:163], v[0:15]
	v_mfma_f32_32x32x16_f16 v[16:31], v[196:199], v[160:163], v[16:31]
	v_mfma_f32_32x32x16_f16 v[0:15], v[200:203], v[164:167], v[0:15]
	v_mfma_f32_32x32x16_f16 v[16:31], v[204:207], v[164:167], v[16:31]
	s_nop 7
	ds_read_b128 v[176:179], v225 offset:0
	s_waitcnt vmcnt(5)
	v_exp_f32_e32 v64, v64
	v_exp_f32_e32 v65, v65
	v_cvt_pk_f16_f32 v216, v216, v217
	v_cvt_pk_f16_f32 v217, v218, v219
	ds_read_b128 v[180:183], v225 offset:32
	v_exp_f32_e32 v66, v66
	v_exp_f32_e32 v67, v67
	v_cvt_pk_f16_f32 v218, v220, v221
	v_cvt_pk_f16_f32 v160, v64, v65
	v_add_f32_e32 v64, v64, v65
	v_cvt_pk_f16_f32 v219, v222, v223
	ds_write_b128 v228, v[216:219] offset:0
	ds_read_b128 v[184:187], v225 offset:64
	v_exp_f32_e32 v68, v68
	v_exp_f32_e32 v69, v69
	v_cvt_pk_f16_f32 v161, v66, v67
	v_add_f32_e32 v66, v66, v67
	ds_read_b128 v[188:191], v225 offset:96
	v_exp_f32_e32 v70, v70
	v_exp_f32_e32 v71, v71
	v_cvt_pk_f16_f32 v162, v68, v69
	v_add_f32_e32 v68, v68, v69
	v_add_f32_e32 v231, v64, v66
	ds_read_b128 v[192:195], v226 offset:27712
	v_exp_f32_e32 v72, v72
	v_exp_f32_e32 v73, v73
	v_cvt_pk_f16_f32 v163, v70, v71
	v_add_f32_e32 v70, v70, v71
	v_add_f32_e32 v231, v231, v68
	ds_read_b128 v[196:199], v226 offset:32320
	v_exp_f32_e32 v74, v74
	v_exp_f32_e32 v75, v75
	v_cvt_pk_f16_f32 v164, v72, v73
	v_add_f32_e32 v72, v72, v73
	v_add_f32_e32 v231, v231, v70
	ds_read_b128 v[200:203], v226 offset:27744
	v_exp_f32_e32 v76, v76
	v_exp_f32_e32 v77, v77
	v_cvt_pk_f16_f32 v165, v74, v75
	v_add_f32_e32 v74, v74, v75
	v_add_f32_e32 v231, v231, v72
	ds_read_b128 v[204:207], v226 offset:32352
	v_exp_f32_e32 v78, v78
	v_exp_f32_e32 v79, v79
	v_cvt_pk_f16_f32 v166, v76, v77
	v_add_f32_e32 v76, v76, v77
	v_add_f32_e32 v231, v231, v74
	v_cvt_pk_f16_f32 v167, v78, v79
	v_add_f32_e32 v78, v78, v79
	v_add_f32_e32 v231, v231, v76
	v_add_f32_e32 v231, v231, v78
	v_cmp_nge_f32_e32 vcc, s34, v231
	s_cbranch_vccnz .Lovf_a31p
.Lovfret_a31p:
	v_add_f32_e32 v232, v232, v231
	s_waitcnt lgkmcnt(4)
	v_mfma_f32_32x32x16_f16 v[64:79], v[176:179], v[128:131], v[96:111]
	buffer_load_dword v216, v230, s[4:7], s25 offen
	v_mfma_f32_32x32x16_f16 v[64:79], v[180:183], v[132:135], v[64:79]
	s_add_u32 s31, s25, 0x3000
	buffer_load_dword v217, v230, s[4:7], s31 offen
	v_mfma_f32_32x32x16_f16 v[64:79], v[184:187], v[136:139], v[64:79]
	s_add_u32 s31, s25, 0x6000
	buffer_load_dword v218, v230, s[4:7], s31 offen
	v_mfma_f32_32x32x16_f16 v[64:79], v[188:191], v[140:143], v[64:79]
	s_add_u32 s31, s25, 0x9000
	buffer_load_dword v219, v230, s[4:7], s31 offen
	s_waitcnt lgkmcnt(0)
	v_mfma_f32_32x32x16_f16 v[0:15], v[192:195], v[160:163], v[0:15]
	s_add_u32 s31, s25, 0x18000
	buffer_load_dword v220, v230, s[4:7], s31 offen
	v_mfma_f32_32x32x16_f16 v[16:31], v[196:199], v[160:163], v[16:31]
	s_add_u32 s31, s25, 0x1b000
	buffer_load_dword v221, v230, s[4:7], s31 offen
	v_mfma_f32_32x32x16_f16 v[0:15], v[200:203], v[164:167], v[0:15]
	s_add_u32 s31, s25, 0x1e000
	buffer_load_dword v222, v230, s[4:7], s31 offen
	v_mfma_f32_32x32x16_f16 v[16:31], v[204:207], v[164:167], v[16:31]
	s_add_u32 s31, s25, 0x21000
	buffer_load_dword v223, v230, s[4:7], s31 offen
	s_nop 7
	s_waitcnt lgkmcnt(6)
	s_barrier
	s_add_u32 s23, s23, 1
	s_waitcnt vmcnt(8)
	v_cmp_ne_u32_e64 s[20:21], 0, v224
	v_mul_f32_e32 v32, s36, v32
	v_mul_f32_e32 v33, s36, v33
	v_mul_f32_e32 v34, s36, v34
	v_mul_f32_e32 v35, s36, v35
	v_cvt_pk_f16_f32 v32, v32, v33
	v_cvt_pk_f16_f32 v33, v34, v35
	ds_write_b64 v239, v[32:33] offset:0
	v_mul_f32_e32 v36, s36, v36
	v_mul_f32_e32 v37, s36, v37
	v_mul_f32_e32 v38, s36, v38
	v_mul_f32_e32 v39, s36, v39
	v_cvt_pk_f16_f32 v36, v36, v37
	v_cvt_pk_f16_f32 v37, v38, v39
	ds_write_b64 v239, v[36:37] offset:576
	v_mul_f32_e32 v40, s36, v40
	v_mul_f32_e32 v41, s36, v41
	v_mul_f32_e32 v42, s36, v42
	v_mul_f32_e32 v43, s36, v43
	v_cvt_pk_f16_f32 v40, v40, v41
	v_cvt_pk_f16_f32 v41, v42, v43
	ds_write_b64 v239, v[40:41] offset:1152
	v_mul_f32_e32 v44, s36, v44
	v_mul_f32_e32 v45, s36, v45
	v_mul_f32_e32 v46, s36, v46
	v_mul_f32_e32 v47, s36, v47
	v_cvt_pk_f16_f32 v44, v44, v45
	v_cvt_pk_f16_f32 v45, v46, v47
	ds_write_b64 v239, v[44:45] offset:1728
	v_mul_f32_e32 v48, s36, v48
	v_mul_f32_e32 v49, s36, v49
	v_mul_f32_e32 v50, s36, v50
	v_mul_f32_e32 v51, s36, v51
	v_cvt_pk_f16_f32 v48, v48, v49
	v_cvt_pk_f16_f32 v49, v50, v51
	ds_write_b64 v239, v[48:49] offset:2304
	v_mul_f32_e32 v52, s36, v52
	v_mul_f32_e32 v53, s36, v53
	v_mul_f32_e32 v54, s36, v54
	v_mul_f32_e32 v55, s36, v55
	v_cvt_pk_f16_f32 v52, v52, v53
	v_cvt_pk_f16_f32 v53, v54, v55
	ds_write_b64 v239, v[52:53] offset:2880
	v_mul_f32_e32 v56, s36, v56
	v_mul_f32_e32 v57, s36, v57
	v_mul_f32_e32 v58, s36, v58
	v_mul_f32_e32 v59, s36, v59
	v_cvt_pk_f16_f32 v56, v56, v57
	v_cvt_pk_f16_f32 v57, v58, v59
	ds_write_b64 v239, v[56:57] offset:3456
	v_mul_f32_e32 v60, s36, v60
	v_mul_f32_e32 v61, s36, v61
	v_mul_f32_e32 v62, s36, v62
	v_mul_f32_e32 v63, s36, v63
	v_cvt_pk_f16_f32 v60, v60, v61
	v_cvt_pk_f16_f32 v61, v62, v63
	ds_write_b64 v239, v[60:61] offset:4032
	s_waitcnt lgkmcnt(0)
	ds_read_b128 v[144:147], v240 offset:0
	ds_read_b128 v[148:151], v240 offset:32
	ds_read_b128 v[152:155], v240 offset:64
	ds_read_b128 v[156:159], v240 offset:96
	s_waitcnt lgkmcnt(0)
	ds_read_b128 v[192:195], v225 offset:4608
	ds_read_b128 v[196:199], v225 offset:4640
	ds_read_b128 v[200:203], v225 offset:4672
	ds_read_b128 v[204:207], v225 offset:4704
	s_waitcnt lgkmcnt(0)
	v_mfma_f32_32x32x16_f16 v[160:175], v[176:179], v[144:147], 0
	v_mfma_f32_32x32x16_f16 v[160:175], v[180:183], v[148:151], v[160:175]
	v_mfma_f32_32x32x16_f16 v[160:175], v[184:187], v[152:155], v[160:175]
	v_mfma_f32_32x32x16_f16 v[160:175], v[188:191], v[156:159], v[160:175]
	v_mfma_f32_32x32x16_f16 v[80:95], v[192:195], v[144:147], 0
	v_mfma_f32_32x32x16_f16 v[80:95], v[196:199], v[148:151], v[80:95]
	v_mfma_f32_32x32x16_f16 v[80:95], v[200:203], v[152:155], v[80:95]
	v_mfma_f32_32x32x16_f16 v[80:95], v[204:207], v[156:159], v[80:95]
	s_nop 15
	s_nop 3
	s_cmp_eq_u64 s[20:21], -1
	s_cbranch_scc1 .Lpro_nomask_B
	v_lshrrev_b32_e64 v235, v234, s20
	v_bfe_u32 v236, v235, 0, 1
	v_cvt_f32_u32_e32 v236, v236
	v_sub_f32_e32 v236, 1.0, v236
	v_fmac_f32_e32 v160, s35, v236
	v_bfe_u32 v236, v235, 1, 1
	v_cvt_f32_u32_e32 v236, v236
	v_sub_f32_e32 v236, 1.0, v236
	v_fmac_f32_e32 v161, s35, v236
	v_bfe_u32 v236, v235, 2, 1
	v_cvt_f32_u32_e32 v236, v236
	v_sub_f32_e32 v236, 1.0, v236
	v_fmac_f32_e32 v162, s35, v236
	v_bfe_u32 v236, v235, 3, 1
	v_cvt_f32_u32_e32 v236, v236
	v_sub_f32_e32 v236, 1.0, v236
	v_fmac_f32_e32 v163, s35, v236
	v_bfe_u32 v236, v235, 8, 1
	v_cvt_f32_u32_e32 v236, v236
	v_sub_f32_e32 v236, 1.0, v236
	v_fmac_f32_e32 v164, s35, v236
	v_bfe_u32 v236, v235, 9, 1
	v_cvt_f32_u32_e32 v236, v236
	v_sub_f32_e32 v236, 1.0, v236
	v_fmac_f32_e32 v165, s35, v236
	v_bfe_u32 v236, v235, 10, 1
	v_cvt_f32_u32_e32 v236, v236
	v_sub_f32_e32 v236, 1.0, v236
	v_fmac_f32_e32 v166, s35, v236
	v_bfe_u32 v236, v235, 11, 1
	v_cvt_f32_u32_e32 v236, v236
	v_sub_f32_e32 v236, 1.0, v236
	v_fmac_f32_e32 v167, s35, v236
	v_bfe_u32 v236, v235, 16, 1
	v_cvt_f32_u32_e32 v236, v236
	v_sub_f32_e32 v236, 1.0, v236
	v_fmac_f32_e32 v168, s35, v236
	v_bfe_u32 v236, v235, 17, 1
	v_cvt_f32_u32_e32 v236, v236
	v_sub_f32_e32 v236, 1.0, v236
	v_fmac_f32_e32 v169, s35, v236
	v_bfe_u32 v236, v235, 18, 1
	v_cvt_f32_u32_e32 v236, v236
	v_sub_f32_e32 v236, 1.0, v236
	v_fmac_f32_e32 v170, s35, v236
	v_bfe_u32 v236, v235, 19, 1
	v_cvt_f32_u32_e32 v236, v236
	v_sub_f32_e32 v236, 1.0, v236
	v_fmac_f32_e32 v171, s35, v236
	v_bfe_u32 v236, v235, 24, 1
	v_cvt_f32_u32_e32 v236, v236
	v_sub_f32_e32 v236, 1.0, v236
	v_fmac_f32_e32 v172, s35, v236
	v_bfe_u32 v236, v235, 25, 1
	v_cvt_f32_u32_e32 v236, v236
	v_sub_f32_e32 v236, 1.0, v236
	v_fmac_f32_e32 v173, s35, v236
	v_bfe_u32 v236, v235, 26, 1
	v_cvt_f32_u32_e32 v236, v236
	v_sub_f32_e32 v236, 1.0, v236
	v_fmac_f32_e32 v174, s35, v236
	v_bfe_u32 v236, v235, 27, 1
	v_cvt_f32_u32_e32 v236, v236
	v_sub_f32_e32 v236, 1.0, v236
	v_fmac_f32_e32 v175, s35, v236
	v_lshrrev_b32_e64 v235, v234, s21
	v_bfe_u32 v236, v235, 0, 1
	v_cvt_f32_u32_e32 v236, v236
	v_sub_f32_e32 v236, 1.0, v236
	v_fmac_f32_e32 v80, s35, v236
	v_bfe_u32 v236, v235, 1, 1
	v_cvt_f32_u32_e32 v236, v236
	v_sub_f32_e32 v236, 1.0, v236
	v_fmac_f32_e32 v81, s35, v236
	v_bfe_u32 v236, v235, 2, 1
	v_cvt_f32_u32_e32 v236, v236
	v_sub_f32_e32 v236, 1.0, v236
	v_fmac_f32_e32 v82, s35, v236
	v_bfe_u32 v236, v235, 3, 1
	v_cvt_f32_u32_e32 v236, v236
	v_sub_f32_e32 v236, 1.0, v236
	v_fmac_f32_e32 v83, s35, v236
	v_bfe_u32 v236, v235, 8, 1
	v_cvt_f32_u32_e32 v236, v236
	v_sub_f32_e32 v236, 1.0, v236
	v_fmac_f32_e32 v84, s35, v236
	v_bfe_u32 v236, v235, 9, 1
	v_cvt_f32_u32_e32 v236, v236
	v_sub_f32_e32 v236, 1.0, v236
	v_fmac_f32_e32 v85, s35, v236
	v_bfe_u32 v236, v235, 10, 1
	v_cvt_f32_u32_e32 v236, v236
	v_sub_f32_e32 v236, 1.0, v236
	v_fmac_f32_e32 v86, s35, v236
	v_bfe_u32 v236, v235, 11, 1
	v_cvt_f32_u32_e32 v236, v236
	v_sub_f32_e32 v236, 1.0, v236
	v_fmac_f32_e32 v87, s35, v236
	v_bfe_u32 v236, v235, 16, 1
	v_cvt_f32_u32_e32 v236, v236
	v_sub_f32_e32 v236, 1.0, v236
	v_fmac_f32_e32 v88, s35, v236
	v_bfe_u32 v236, v235, 17, 1
	v_cvt_f32_u32_e32 v236, v236
	v_sub_f32_e32 v236, 1.0, v236
	v_fmac_f32_e32 v89, s35, v236
	v_bfe_u32 v236, v235, 18, 1
	v_cvt_f32_u32_e32 v236, v236
	v_sub_f32_e32 v236, 1.0, v236
	v_fmac_f32_e32 v90, s35, v236
	v_bfe_u32 v236, v235, 19, 1
	v_cvt_f32_u32_e32 v236, v236
	v_sub_f32_e32 v236, 1.0, v236
	v_fmac_f32_e32 v91, s35, v236
	v_bfe_u32 v236, v235, 24, 1
	v_cvt_f32_u32_e32 v236, v236
	v_sub_f32_e32 v236, 1.0, v236
	v_fmac_f32_e32 v92, s35, v236
	v_bfe_u32 v236, v235, 25, 1
	v_cvt_f32_u32_e32 v236, v236
	v_sub_f32_e32 v236, 1.0, v236
	v_fmac_f32_e32 v93, s35, v236
	v_bfe_u32 v236, v235, 26, 1
	v_cvt_f32_u32_e32 v236, v236
	v_sub_f32_e32 v236, 1.0, v236
	v_fmac_f32_e32 v94, s35, v236
	v_bfe_u32 v236, v235, 27, 1
	v_cvt_f32_u32_e32 v236, v236
	v_sub_f32_e32 v236, 1.0, v236
	v_fmac_f32_e32 v95, s35, v236
.Lpro_nomask_B:
	v_max3_f32 v235, v160, v161, v162
	v_max3_f32 v235, v235, v163, v164
	v_max3_f32 v235, v235, v165, v166
	v_max3_f32 v235, v235, v167, v168
	v_max3_f32 v235, v235, v169, v170
	v_max3_f32 v235, v235, v171, v172
	v_max3_f32 v235, v235, v173, v174
	v_max3_f32 v235, v235, v175, v80
	v_max3_f32 v235, v235, v81, v82
	v_max3_f32 v235, v235, v83, v84
	v_max3_f32 v235, v235, v85, v86
	v_max3_f32 v235, v235, v87, v88
	v_max3_f32 v235, v235, v89, v90
	v_max3_f32 v235, v235, v91, v92
	v_max3_f32 v235, v235, v93, v94
	v_max_f32_e32 v235, v235, v95
	v_mov_b32_e32 v236, v235
	s_nop 1
	v_permlane32_swap_b32_e32 v235, v236
	v_max_f32_e32 v235, v235, v236
	v_sub_f32_e32 v112, 0, v235
	v_sub_f32_e32 v113, 0, v235
	v_sub_f32_e32 v114, 0, v235
	v_sub_f32_e32 v115, 0, v235
	v_sub_f32_e32 v116, 0, v235
	v_sub_f32_e32 v117, 0, v235
	v_sub_f32_e32 v118, 0, v235
	v_sub_f32_e32 v119, 0, v235
	v_sub_f32_e32 v120, 0, v235
	v_sub_f32_e32 v121, 0, v235
	v_sub_f32_e32 v122, 0, v235
	v_sub_f32_e32 v123, 0, v235
	v_sub_f32_e32 v124, 0, v235
	v_sub_f32_e32 v125, 0, v235
	v_sub_f32_e32 v126, 0, v235
	v_sub_f32_e32 v127, 0, v235
	v_mov_b32_e32 v32, 0
	v_mov_b32_e32 v33, 0
	v_mov_b32_e32 v34, 0
	v_mov_b32_e32 v35, 0
	v_mov_b32_e32 v36, 0
	v_mov_b32_e32 v37, 0
	v_mov_b32_e32 v38, 0
	v_mov_b32_e32 v39, 0
	v_mov_b32_e32 v40, 0
	v_mov_b32_e32 v41, 0
	v_mov_b32_e32 v42, 0
	v_mov_b32_e32 v43, 0
	v_mov_b32_e32 v44, 0
	v_mov_b32_e32 v45, 0
	v_mov_b32_e32 v46, 0
	v_mov_b32_e32 v47, 0
	v_mov_b32_e32 v48, 0
	v_mov_b32_e32 v49, 0
	v_mov_b32_e32 v50, 0
	v_mov_b32_e32 v51, 0
	v_mov_b32_e32 v52, 0
	v_mov_b32_e32 v53, 0
	v_mov_b32_e32 v54, 0
	v_mov_b32_e32 v55, 0
	v_mov_b32_e32 v56, 0
	v_mov_b32_e32 v57, 0
	v_mov_b32_e32 v58, 0
	v_mov_b32_e32 v59, 0
	v_mov_b32_e32 v60, 0
	v_mov_b32_e32 v61, 0
	v_mov_b32_e32 v62, 0
	v_mov_b32_e32 v63, 0
	v_mov_b32_e32 v168, 0
	v_mov_b32_e32 v169, 0
	v_mov_b32_e32 v170, 0
	v_mov_b32_e32 v171, 0
	v_mov_b32_e32 v172, 0
	v_mov_b32_e32 v173, 0
	v_mov_b32_e32 v174, 0
	v_mov_b32_e32 v175, 0
	v_mov_b32_e32 v233, 0
	s_mov_b32 s27, 0
.Lbody:
	s_waitcnt vmcnt(8)
	v_cmp_ne_u32_e64 s[20:21], 0, v224
	s_add_u32 s31, s23, 1
	s_and_b32 s31, s31, 31
	s_lshl_b32 s31, s31, 8
	s_add_u32 s26, s31, s22
	s_add_u32 s31, s23, 3
	s_and_b32 s31, s31, 31
	s_mul_i32 s31, s31, 0xc0000
	s_add_u32 s24, s31, s18
	s_add_u32 s31, s23, 2
	s_and_b32 s31, s31, 31
	s_mul_i32 s31, s31, 0xc0000
	s_add_u32 s25, s31, s19
	s_cmp_eq_u64 s[20:21], -1
	s_cselect_b32 s34, s37, s38
	s_waitcnt lgkmcnt(4)
	v_mfma_f32_32x32x16_f16 v[80:95], v[176:179], v[144:147], v[112:127]
	ds_read_b128 v[176:179], v225 offset:4608
	buffer_load_dword v224, v230, s[8:11], s26 offen
	v_exp_f32_e32 v64, v64
	v_exp_f32_e32 v65, v65
	v_cvt_pk_f16_f32 v208, v208, v209
	v_cvt_pk_f16_f32 v209, v210, v211
	v_mfma_f32_32x32x16_f16 v[80:95], v[180:183], v[148:151], v[80:95]
	ds_read_b128 v[180:183], v225 offset:4640
	v_exp_f32_e32 v66, v66
	v_exp_f32_e32 v67, v67
	v_cvt_pk_f16_f32 v212, v212, v213
	v_cvt_pk_f16_f32 v160, v64, v65
	v_add_f32_e32 v64, v64, v65
	v_cvt_pk_f16_f32 v213, v214, v215
	v_mfma_f32_32x32x16_f16 v[80:95], v[184:187], v[152:155], v[80:95]
	ds_write_b64 v227, v[208:209] offset:18432
	ds_write_b64 v227, v[212:213] offset:23040
	ds_read_b128 v[184:187], v225 offset:4672
	v_exp_f32_e32 v68, v68
	v_exp_f32_e32 v69, v69
	v_cvt_pk_f16_f32 v161, v66, v67
	v_add_f32_e32 v66, v66, v67
	v_mfma_f32_32x32x16_f16 v[80:95], v[188:191], v[156:159], v[80:95]
	ds_read_b128 v[188:191], v225 offset:4704
	v_exp_f32_e32 v70, v70
	v_exp_f32_e32 v71, v71
	v_cvt_pk_f16_f32 v162, v68, v69
	v_add_f32_e32 v68, v68, v69
	v_add_f32_e32 v231, v64, v66
	s_waitcnt lgkmcnt(6)
	v_mfma_f32_32x32x16_f16 v[32:47], v[192:195], v[168:171], v[32:47]
	ds_read_b128 v[192:195], v226 offset:0
	v_exp_f32_e32 v72, v72
	v_exp_f32_e32 v73, v73
	v_cvt_pk_f16_f32 v163, v70, v71
	v_add_f32_e32 v70, v70, v71
	v_add_f32_e32 v231, v231, v68
	v_mfma_f32_32x32x16_f16 v[48:63], v[196:199], v[168:171], v[48:63]
	ds_read_b128 v[196:199], v226 offset:4608
	v_exp_f32_e32 v74, v74
	v_exp_f32_e32 v75, v75
	v_cvt_pk_f16_f32 v164, v72, v73
	v_add_f32_e32 v72, v72, v73
	v_add_f32_e32 v231, v231, v70
	v_mfma_f32_32x32x16_f16 v[32:47], v[200:203], v[172:175], v[32:47]
	ds_read_b128 v[200:203], v226 offset:32
	v_exp_f32_e32 v76, v76
	v_exp_f32_e32 v77, v77
	v_cvt_pk_f16_f32 v165, v74, v75
	v_add_f32_e32 v74, v74, v75
	v_add_f32_e32 v231, v231, v72
	v_mfma_f32_32x32x16_f16 v[48:63], v[204:207], v[172:175], v[48:63]
	ds_read_b128 v[204:207], v226 offset:4640
	v_exp_f32_e32 v78, v78
	v_exp_f32_e32 v79, v79
	v_cvt_pk_f16_f32 v166, v76, v77
	v_add_f32_e32 v76, v76, v77
	v_add_f32_e32 v231, v231, v74
	v_cvt_pk_f16_f32 v167, v78, v79
	v_add_f32_e32 v78, v78, v79
	v_add_f32_e32 v231, v231, v76
	v_add_f32_e32 v231, v231, v78
	v_cmp_nge_f32_e32 vcc, s34, v231
	s_cbranch_vccnz .Lovf_a00
.Lovfret_a00:
	v_add_f32_e32 v232, v232, v231
	s_waitcnt lgkmcnt(4)
	v_mfma_f32_32x32x16_f16 v[64:79], v[176:179], v[128:131], v[96:111]
	v_exp_f32_e32 v80, v80
	v_exp_f32_e32 v81, v81
	v_mfma_f32_32x32x16_f16 v[64:79], v[180:183], v[132:135], v[64:79]
	buffer_load_dwordx4 v[208:211], v229, s[4:7], s24 offen
	v_exp_f32_e32 v82, v82
	v_exp_f32_e32 v83, v83
	v_cvt_pk_f16_f32 v168, v80, v81
	v_add_f32_e32 v80, v80, v81
	v_mfma_f32_32x32x16_f16 v[64:79], v[184:187], v[136:139], v[64:79]
	s_add_u32 s31, s24, 0x60000
	buffer_load_dwordx4 v[212:215], v229, s[4:7], s31 offen
	v_exp_f32_e32 v84, v84
	v_exp_f32_e32 v85, v85
	v_cvt_pk_f16_f32 v169, v82, v83
	v_add_f32_e32 v82, v82, v83
	v_mfma_f32_32x32x16_f16 v[64:79], v[188:191], v[140:143], v[64:79]
	v_exp_f32_e32 v86, v86
	v_exp_f32_e32 v87, v87
	v_cvt_pk_f16_f32 v170, v84, v85
	v_add_f32_e32 v84, v84, v85
	v_add_f32_e32 v231, v80, v82
	s_waitcnt lgkmcnt(0)
	v_mfma_f32_32x32x16_f16 v[0:15], v[192:195], v[160:163], v[0:15]
	v_exp_f32_e32 v88, v88
	v_exp_f32_e32 v89, v89
	v_cvt_pk_f16_f32 v171, v86, v87
	v_add_f32_e32 v86, v86, v87
	v_add_f32_e32 v231, v231, v84
	v_mfma_f32_32x32x16_f16 v[16:31], v[196:199], v[160:163], v[16:31]
	v_exp_f32_e32 v90, v90
	v_exp_f32_e32 v91, v91
	v_cvt_pk_f16_f32 v172, v88, v89
	v_add_f32_e32 v88, v88, v89
	v_add_f32_e32 v231, v231, v86
	v_mfma_f32_32x32x16_f16 v[0:15], v[200:203], v[164:167], v[0:15]
	v_exp_f32_e32 v92, v92
	v_exp_f32_e32 v93, v93
	v_cvt_pk_f16_f32 v173, v90, v91
	v_add_f32_e32 v90, v90, v91
	v_add_f32_e32 v231, v231, v88
	v_mfma_f32_32x32x16_f16 v[16:31], v[204:207], v[164:167], v[16:31]
	v_exp_f32_e32 v94, v94
	v_exp_f32_e32 v95, v95
	v_cvt_pk_f16_f32 v174, v92, v93
	v_add_f32_e32 v92, v92, v93
	v_add_f32_e32 v231, v231, v90
	v_cvt_pk_f16_f32 v175, v94, v95
	v_add_f32_e32 v94, v94, v95
	v_add_f32_e32 v231, v231, v92
	v_add_f32_e32 v231, v231, v94
	v_cmp_nge_f32_e32 vcc, s34, v231
	s_cbranch_vccnz .Lovf_b00
.Lovfret_b00:
	v_add_f32_e32 v233, v233, v231
	s_waitcnt lgkmcnt(4)
	v_mfma_f32_32x32x16_f16 v[80:95], v[176:179], v[144:147], v[112:127]
	ds_read_b128 v[176:179], v225 offset:9216
	s_waitcnt vmcnt(3)
	v_exp_f32_e32 v64, v64
	v_exp_f32_e32 v65, v65
	v_cvt_pk_f16_f32 v216, v216, v217
	v_cvt_pk_f16_f32 v217, v218, v219
	v_mfma_f32_32x32x16_f16 v[80:95], v[180:183], v[148:151], v[80:95]
	ds_read_b128 v[180:183], v225 offset:9248
	v_exp_f32_e32 v66, v66
	v_exp_f32_e32 v67, v67
	v_cvt_pk_f16_f32 v218, v220, v221
	v_cvt_pk_f16_f32 v160, v64, v65
	v_add_f32_e32 v64, v64, v65
	v_cvt_pk_f16_f32 v219, v222, v223
	v_mfma_f32_32x32x16_f16 v[80:95], v[184:187], v[152:155], v[80:95]
	ds_write_b128 v228, v[216:219] offset:9216
	ds_read_b128 v[184:187], v225 offset:9280
	v_exp_f32_e32 v68, v68
	v_exp_f32_e32 v69, v69
	v_cvt_pk_f16_f32 v161, v66, v67
	v_add_f32_e32 v66, v66, v67
	v_mfma_f32_32x32x16_f16 v[80:95], v[188:191], v[156:159], v[80:95]
	ds_read_b128 v[188:191], v225 offset:9312
	v_exp_f32_e32 v70, v70
	v_exp_f32_e32 v71, v71
	v_cvt_pk_f16_f32 v162, v68, v69
	v_add_f32_e32 v68, v68, v69
	v_add_f32_e32 v231, v64, v66
	s_waitcnt lgkmcnt(5)
	v_mfma_f32_32x32x16_f16 v[32:47], v[192:195], v[168:171], v[32:47]
	ds_read_b128 v[192:195], v226 offset:64
	v_exp_f32_e32 v72, v72
	v_exp_f32_e32 v73, v73
	v_cvt_pk_f16_f32 v163, v70, v71
	v_add_f32_e32 v70, v70, v71
	v_add_f32_e32 v231, v231, v68
	v_mfma_f32_32x32x16_f16 v[48:63], v[196:199], v[168:171], v[48:63]
	ds_read_b128 v[196:199], v226 offset:4672
	v_exp_f32_e32 v74, v74
	v_exp_f32_e32 v75, v75
	v_cvt_pk_f16_f32 v164, v72, v73
	v_add_f32_e32 v72, v72, v73
	v_add_f32_e32 v231, v231, v70
	v_mfma_f32_32x32x16_f16 v[32:47], v[200:203], v[172:175], v[32:47]
	ds_read_b128 v[200:203], v226 offset:96
	v_exp_f32_e32 v76, v76
	v_exp_f32_e32 v77, v77
	v_cvt_pk_f16_f32 v165, v74, v75
	v_add_f32_e32 v74, v74, v75
	v_add_f32_e32 v231, v231, v72
	v_mfma_f32_32x32x16_f16 v[48:63], v[204:207], v[172:175], v[48:63]
	ds_read_b128 v[204:207], v226 offset:4704
	v_exp_f32_e32 v78, v78
	v_exp_f32_e32 v79, v79
	v_cvt_pk_f16_f32 v166, v76, v77
	v_add_f32_e32 v76, v76, v77
	v_add_f32_e32 v231, v231, v74
	v_cvt_pk_f16_f32 v167, v78, v79
	v_add_f32_e32 v78, v78, v79
	v_add_f32_e32 v231, v231, v76
	v_add_f32_e32 v231, v231, v78
	v_cmp_nge_f32_e32 vcc, s34, v231
	s_cbranch_vccnz .Lovf_a01
.Lovfret_a01:
	v_add_f32_e32 v232, v232, v231
	s_waitcnt lgkmcnt(4)
	v_mfma_f32_32x32x16_f16 v[64:79], v[176:179], v[128:131], v[96:111]
	buffer_load_dword v216, v230, s[4:7], s25 offen
	v_exp_f32_e32 v80, v80
	v_exp_f32_e32 v81, v81
	v_mfma_f32_32x32x16_f16 v[64:79], v[180:183], v[132:135], v[64:79]
	s_add_u32 s31, s25, 0x3000
	buffer_load_dword v217, v230, s[4:7], s31 offen
	v_exp_f32_e32 v82, v82
	v_exp_f32_e32 v83, v83
	v_cvt_pk_f16_f32 v168, v80, v81
	v_add_f32_e32 v80, v80, v81
	v_mfma_f32_32x32x16_f16 v[64:79], v[184:187], v[136:139], v[64:79]
	s_add_u32 s31, s25, 0x6000
	buffer_load_dword v218, v230, s[4:7], s31 offen
	v_exp_f32_e32 v84, v84
	v_exp_f32_e32 v85, v85
	v_cvt_pk_f16_f32 v169, v82, v83
	v_add_f32_e32 v82, v82, v83
	v_mfma_f32_32x32x16_f16 v[64:79], v[188:191], v[140:143], v[64:79]
	s_add_u32 s31, s25, 0x9000
	buffer_load_dword v219, v230, s[4:7], s31 offen
	v_exp_f32_e32 v86, v86
	v_exp_f32_e32 v87, v87
	v_cvt_pk_f16_f32 v170, v84, v85
	v_add_f32_e32 v84, v84, v85
	v_add_f32_e32 v231, v80, v82
	s_waitcnt lgkmcnt(0)
	v_mfma_f32_32x32x16_f16 v[0:15], v[192:195], v[160:163], v[0:15]
	s_add_u32 s31, s25, 0x18000
	buffer_load_dword v220, v230, s[4:7], s31 offen
	v_exp_f32_e32 v88, v88
	v_exp_f32_e32 v89, v89
	v_cvt_pk_f16_f32 v171, v86, v87
	v_add_f32_e32 v86, v86, v87
	v_add_f32_e32 v231, v231, v84
	v_mfma_f32_32x32x16_f16 v[16:31], v[196:199], v[160:163], v[16:31]
	s_add_u32 s31, s25, 0x1b000
	buffer_load_dword v221, v230, s[4:7], s31 offen
	v_exp_f32_e32 v90, v90
	v_exp_f32_e32 v91, v91
	v_cvt_pk_f16_f32 v172, v88, v89
	v_add_f32_e32 v88, v88, v89
	v_add_f32_e32 v231, v231, v86
	v_mfma_f32_32x32x16_f16 v[0:15], v[200:203], v[164:167], v[0:15]
	s_add_u32 s31, s25, 0x1e000
	buffer_load_dword v222, v230, s[4:7], s31 offen
	v_exp_f32_e32 v92, v92
	v_exp_f32_e32 v93, v93
	v_cvt_pk_f16_f32 v173, v90, v91
	v_add_f32_e32 v90, v90, v91
	v_add_f32_e32 v231, v231, v88
	v_mfma_f32_32x32x16_f16 v[16:31], v[204:207], v[164:167], v[16:31]
	s_add_u32 s31, s25, 0x21000
	buffer_load_dword v223, v230, s[4:7], s31 offen
	v_exp_f32_e32 v94, v94
	v_exp_f32_e32 v95, v95
	v_cvt_pk_f16_f32 v174, v92, v93
	v_add_f32_e32 v92, v92, v93
	v_add_f32_e32 v231, v231, v90
	v_cvt_pk_f16_f32 v175, v94, v95
	v_add_f32_e32 v94, v94, v95
	v_add_f32_e32 v231, v231, v92
	v_add_f32_e32 v231, v231, v94
	v_cmp_nge_f32_e32 vcc, s34, v231
	s_cbranch_vccnz .Lovf_b01
.Lovfret_b01:
	v_add_f32_e32 v233, v233, v231
	s_waitcnt lgkmcnt(6)
	s_barrier
	s_add_u32 s23, s23, 1
	s_waitcnt vmcnt(8)
	v_cmp_ne_u32_e64 s[20:21], 0, v224
	s_add_u32 s31, s23, 1
	s_and_b32 s31, s31, 31
	s_lshl_b32 s31, s31, 8
	s_add_u32 s26, s31, s22
	s_add_u32 s31, s23, 3
	s_and_b32 s31, s31, 31
	s_mul_i32 s31, s31, 0xc0000
	s_add_u32 s24, s31, s18
	s_add_u32 s31, s23, 2
	s_and_b32 s31, s31, 31
	s_mul_i32 s31, s31, 0xc0000
	s_add_u32 s25, s31, s19
	s_cmp_eq_u64 s[20:21], -1
	s_cselect_b32 s34, s37, s38
	s_waitcnt lgkmcnt(4)
	v_mfma_f32_32x32x16_f16 v[80:95], v[176:179], v[144:147], v[112:127]
	ds_read_b128 v[176:179], v225 offset:13824
	buffer_load_dword v224, v230, s[8:11], s26 offen
	v_exp_f32_e32 v64, v64
	v_exp_f32_e32 v65, v65
	v_cvt_pk_f16_f32 v208, v208, v209
	v_cvt_pk_f16_f32 v209, v210, v211
	v_mfma_f32_32x32x16_f16 v[80:95], v[180:183], v[148:151], v[80:95]
	ds_read_b128 v[180:183], v225 offset:13856
	v_exp_f32_e32 v66, v66
	v_exp_f32_e32 v67, v67
	v_cvt_pk_f16_f32 v212, v212, v213
	v_cvt_pk_f16_f32 v160, v64, v65
	v_add_f32_e32 v64, v64, v65
	v_cvt_pk_f16_f32 v213, v214, v215
	v_mfma_f32_32x32x16_f16 v[80:95], v[184:187], v[152:155], v[80:95]
	ds_write_b64 v227, v[208:209] offset:27648
	ds_write_b64 v227, v[212:213] offset:32256
	ds_read_b128 v[184:187], v225 offset:13888
	v_exp_f32_e32 v68, v68
	v_exp_f32_e32 v69, v69
	v_cvt_pk_f16_f32 v161, v66, v67
	v_add_f32_e32 v66, v66, v67
	v_mfma_f32_32x32x16_f16 v[80:95], v[188:191], v[156:159], v[80:95]
	ds_read_b128 v[188:191], v225 offset:13920
	v_exp_f32_e32 v70, v70
	v_exp_f32_e32 v71, v71
	v_cvt_pk_f16_f32 v162, v68, v69
	v_add_f32_e32 v68, v68, v69
	v_add_f32_e32 v231, v64, v66
	s_waitcnt lgkmcnt(6)
	v_mfma_f32_32x32x16_f16 v[32:47], v[192:195], v[168:171], v[32:47]
	ds_read_b128 v[192:195], v226 offset:9216
	v_exp_f32_e32 v72, v72
	v_exp_f32_e32 v73, v73
	v_cvt_pk_f16_f32 v163, v70, v71
	v_add_f32_e32 v70, v70, v71
	v_add_f32_e32 v231, v231, v68
	v_mfma_f32_32x32x16_f16 v[48:63], v[196:199], v[168:171], v[48:63]
	ds_read_b128 v[196:199], v226 offset:13824
	v_exp_f32_e32 v74, v74
	v_exp_f32_e32 v75, v75
	v_cvt_pk_f16_f32 v164, v72, v73
	v_add_f32_e32 v72, v72, v73
	v_add_f32_e32 v231, v231, v70
	v_mfma_f32_32x32x16_f16 v[32:47], v[200:203], v[172:175], v[32:47]
	ds_read_b128 v[200:203], v226 offset:9248
	v_exp_f32_e32 v76, v76
	v_exp_f32_e32 v77, v77
	v_cvt_pk_f16_f32 v165, v74, v75
	v_add_f32_e32 v74, v74, v75
	v_add_f32_e32 v231, v231, v72
	v_mfma_f32_32x32x16_f16 v[48:63], v[204:207], v[172:175], v[48:63]
	ds_read_b128 v[204:207], v226 offset:13856
	v_exp_f32_e32 v78, v78
	v_exp_f32_e32 v79, v79
	v_cvt_pk_f16_f32 v166, v76, v77
	v_add_f32_e32 v76, v76, v77
	v_add_f32_e32 v231, v231, v74
	v_cvt_pk_f16_f32 v167, v78, v79
	v_add_f32_e32 v78, v78, v79
	v_add_f32_e32 v231, v231, v76
	v_add_f32_e32 v231, v231, v78
	v_cmp_nge_f32_e32 vcc, s34, v231
	s_cbranch_vccnz .Lovf_a10

.Lovfret_b10:
	v_add_f32_e32 v233, v233, v231
	s_waitcnt lgkmcnt(4)
	v_mfma_f32_32x32x16_f16 v[80:95], v[176:179], v[144:147], v[112:127]
	ds_read_b128 v[176:179], v225 offset:18432
	s_waitcnt vmcnt(3)
	v_exp_f32_e32 v64, v64
	v_exp_f32_e32 v65, v65
	v_cvt_pk_f16_f32 v216, v216, v217
	v_cvt_pk_f16_f32 v217, v218, v219
	v_mfma_f32_32x32x16_f16 v[80:95], v[180:183], v[148:151], v[80:95]
	ds_read_b128 v[180:183], v225 offset:18464
	v_exp_f32_e32 v66, v66
	v_exp_f32_e32 v67, v67
	v_cvt_pk_f16_f32 v218, v220, v221
	v_cvt_pk_f16_f32 v160, v64, v65
	v_add_f32_e32 v64, v64, v65
	v_cvt_pk_f16_f32 v219, v222, v223
	v_mfma_f32_32x32x16_f16 v[80:95], v[184:187], v[152:155], v[80:95]
	ds_write_b128 v228, v[216:219] offset:18432
	ds_read_b128 v[184:187], v225 offset:18496
	v_exp_f32_e32 v68, v68
	v_exp_f32_e32 v69, v69
	v_cvt_pk_f16_f32 v161, v66, v67
	v_add_f32_e32 v66, v66, v67
	v_mfma_f32_32x32x16_f16 v[80:95], v[188:191], v[156:159], v[80:95]
	ds_read_b128 v[188:191], v225 offset:18528
	v_exp_f32_e32 v70, v70
	v_exp_f32_e32 v71, v71
	v_cvt_pk_f16_f32 v162, v68, v69
	v_add_f32_e32 v68, v68, v69
	v_add_f32_e32 v231, v64, v66
	s_waitcnt lgkmcnt(5)
	v_mfma_f32_32x32x16_f16 v[32:47], v[192:195], v[168:171], v[32:47]
	ds_read_b128 v[192:195], v226 offset:9280
	v_exp_f32_e32 v72, v72
	v_exp_f32_e32 v73, v73
	v_cvt_pk_f16_f32 v163, v70, v71
	v_add_f32_e32 v70, v70, v71
	v_add_f32_e32 v231, v231, v68
	v_mfma_f32_32x32x16_f16 v[48:63], v[196:199], v[168:171], v[48:63]
	ds_read_b128 v[196:199], v226 offset:13888
	v_exp_f32_e32 v74, v74
	v_exp_f32_e32 v75, v75
	v_cvt_pk_f16_f32 v164, v72, v73
	v_add_f32_e32 v72, v72, v73
	v_add_f32_e32 v231, v231, v70
	v_mfma_f32_32x32x16_f16 v[32:47], v[200:203], v[172:175], v[32:47]
	ds_read_b128 v[200:203], v226 offset:9312
	v_exp_f32_e32 v76, v76
	v_exp_f32_e32 v77, v77
	v_cvt_pk_f16_f32 v165, v74, v75
	v_add_f32_e32 v74, v74, v75
	v_add_f32_e32 v231, v231, v72
	v_mfma_f32_32x32x16_f16 v[48:63], v[204:207], v[172:175], v[48:63]
	ds_read_b128 v[204:207], v226 offset:13920
	v_exp_f32_e32 v78, v78
	v_exp_f32_e32 v79, v79
	v_cvt_pk_f16_f32 v166, v76, v77
	v_add_f32_e32 v76, v76, v77
	v_add_f32_e32 v231, v231, v74
	v_cvt_pk_f16_f32 v167, v78, v79
	v_add_f32_e32 v78, v78, v79
	v_add_f32_e32 v231, v231, v76
	v_add_f32_e32 v231, v231, v78
	v_cmp_nge_f32_e32 vcc, s34, v231
	s_cbranch_vccnz .Lovf_a11

.Lovfret_b11:
	v_add_f32_e32 v233, v233, v231
	s_waitcnt lgkmcnt(6)
	s_barrier
	s_add_u32 s23, s23, 1
	s_waitcnt vmcnt(8)
	v_cmp_ne_u32_e64 s[20:21], 0, v224
	s_add_u32 s31, s23, 1
	s_and_b32 s31, s31, 31
	s_lshl_b32 s31, s31, 8
	s_add_u32 s26, s31, s22
	s_add_u32 s31, s23, 3
	s_and_b32 s31, s31, 31
	s_mul_i32 s31, s31, 0xc0000
	s_add_u32 s24, s31, s18
	s_add_u32 s31, s23, 2
	s_and_b32 s31, s31, 31
	s_mul_i32 s31, s31, 0xc0000
	s_add_u32 s25, s31, s19
	s_cmp_eq_u64 s[20:21], -1
	s_cselect_b32 s34, s37, s38
	s_waitcnt lgkmcnt(4)
	v_mfma_f32_32x32x16_f16 v[80:95], v[176:179], v[144:147], v[112:127]
	ds_read_b128 v[176:179], v225 offset:23040
	buffer_load_dword v224, v230, s[8:11], s26 offen
	v_exp_f32_e32 v64, v64
	v_exp_f32_e32 v65, v65
	v_cvt_pk_f16_f32 v208, v208, v209
	v_cvt_pk_f16_f32 v209, v210, v211
	v_mfma_f32_32x32x16_f16 v[80:95], v[180:183], v[148:151], v[80:95]
	ds_read_b128 v[180:183], v225 offset:23072
	v_exp_f32_e32 v66, v66
	v_exp_f32_e32 v67, v67
	v_cvt_pk_f16_f32 v212, v212, v213
	v_cvt_pk_f16_f32 v160, v64, v65
	v_add_f32_e32 v64, v64, v65
	v_cvt_pk_f16_f32 v213, v214, v215
	v_mfma_f32_32x32x16_f16 v[80:95], v[184:187], v[152:155], v[80:95]
	ds_write_b64 v227, v[208:209] offset:0
	ds_write_b64 v227, v[212:213] offset:4608
	ds_read_b128 v[184:187], v225 offset:23104
	v_exp_f32_e32 v68, v68
	v_exp_f32_e32 v69, v69
	v_cvt_pk_f16_f32 v161, v66, v67
	v_add_f32_e32 v66, v66, v67
	v_mfma_f32_32x32x16_f16 v[80:95], v[188:191], v[156:159], v[80:95]
	ds_read_b128 v[188:191], v225 offset:23136
	v_exp_f32_e32 v70, v70
	v_exp_f32_e32 v71, v71
	v_cvt_pk_f16_f32 v162, v68, v69
	v_add_f32_e32 v68, v68, v69
	v_add_f32_e32 v231, v64, v66
	s_waitcnt lgkmcnt(6)
	v_mfma_f32_32x32x16_f16 v[32:47], v[192:195], v[168:171], v[32:47]
	ds_read_b128 v[192:195], v226 offset:18432
	v_exp_f32_e32 v72, v72
	v_exp_f32_e32 v73, v73
	v_cvt_pk_f16_f32 v163, v70, v71
	v_add_f32_e32 v70, v70, v71
	v_add_f32_e32 v231, v231, v68
	v_mfma_f32_32x32x16_f16 v[48:63], v[196:199], v[168:171], v[48:63]
	ds_read_b128 v[196:199], v226 offset:23040
	v_exp_f32_e32 v74, v74
	v_exp_f32_e32 v75, v75
	v_cvt_pk_f16_f32 v164, v72, v73
	v_add_f32_e32 v72, v72, v73
	v_add_f32_e32 v231, v231, v70
	v_mfma_f32_32x32x16_f16 v[32:47], v[200:203], v[172:175], v[32:47]
	ds_read_b128 v[200:203], v226 offset:18464
	v_exp_f32_e32 v76, v76
	v_exp_f32_e32 v77, v77
	v_cvt_pk_f16_f32 v165, v74, v75
	v_add_f32_e32 v74, v74, v75
	v_add_f32_e32 v231, v231, v72
	v_mfma_f32_32x32x16_f16 v[48:63], v[204:207], v[172:175], v[48:63]
	ds_read_b128 v[204:207], v226 offset:23072
	v_exp_f32_e32 v78, v78
	v_exp_f32_e32 v79, v79
	v_cvt_pk_f16_f32 v166, v76, v77
	v_add_f32_e32 v76, v76, v77
	v_add_f32_e32 v231, v231, v74
	v_cvt_pk_f16_f32 v167, v78, v79
	v_add_f32_e32 v78, v78, v79
	v_add_f32_e32 v231, v231, v76
	v_add_f32_e32 v231, v231, v78
	v_cmp_nge_f32_e32 vcc, s34, v231
	s_cbranch_vccnz .Lovf_a20

.Lovfret_b20:
	v_add_f32_e32 v233, v233, v231
	s_waitcnt lgkmcnt(4)
	v_mfma_f32_32x32x16_f16 v[80:95], v[176:179], v[144:147], v[112:127]
	ds_read_b128 v[176:179], v225 offset:27648
	s_waitcnt vmcnt(3)
	v_exp_f32_e32 v64, v64
	v_exp_f32_e32 v65, v65
	v_cvt_pk_f16_f32 v216, v216, v217
	v_cvt_pk_f16_f32 v217, v218, v219
	v_mfma_f32_32x32x16_f16 v[80:95], v[180:183], v[148:151], v[80:95]
	ds_read_b128 v[180:183], v225 offset:27680
	v_exp_f32_e32 v66, v66
	v_exp_f32_e32 v67, v67
	v_cvt_pk_f16_f32 v218, v220, v221
	v_cvt_pk_f16_f32 v160, v64, v65
	v_add_f32_e32 v64, v64, v65
	v_cvt_pk_f16_f32 v219, v222, v223
	v_mfma_f32_32x32x16_f16 v[80:95], v[184:187], v[152:155], v[80:95]
	ds_write_b128 v228, v[216:219] offset:27648
	ds_read_b128 v[184:187], v225 offset:27712
	v_exp_f32_e32 v68, v68
	v_exp_f32_e32 v69, v69
	v_cvt_pk_f16_f32 v161, v66, v67
	v_add_f32_e32 v66, v66, v67
	v_mfma_f32_32x32x16_f16 v[80:95], v[188:191], v[156:159], v[80:95]
	ds_read_b128 v[188:191], v225 offset:27744
	v_exp_f32_e32 v70, v70
	v_exp_f32_e32 v71, v71
	v_cvt_pk_f16_f32 v162, v68, v69
	v_add_f32_e32 v68, v68, v69
	v_add_f32_e32 v231, v64, v66
	s_waitcnt lgkmcnt(5)
	v_mfma_f32_32x32x16_f16 v[32:47], v[192:195], v[168:171], v[32:47]
	ds_read_b128 v[192:195], v226 offset:18496
	v_exp_f32_e32 v72, v72
	v_exp_f32_e32 v73, v73
	v_cvt_pk_f16_f32 v163, v70, v71
	v_add_f32_e32 v70, v70, v71
	v_add_f32_e32 v231, v231, v68
	v_mfma_f32_32x32x16_f16 v[48:63], v[196:199], v[168:171], v[48:63]
	ds_read_b128 v[196:199], v226 offset:23104
	v_exp_f32_e32 v74, v74
	v_exp_f32_e32 v75, v75
	v_cvt_pk_f16_f32 v164, v72, v73
	v_add_f32_e32 v72, v72, v73
	v_add_f32_e32 v231, v231, v70
	v_mfma_f32_32x32x16_f16 v[32:47], v[200:203], v[172:175], v[32:47]
	ds_read_b128 v[200:203], v226 offset:18528
	v_exp_f32_e32 v76, v76
	v_exp_f32_e32 v77, v77
	v_cvt_pk_f16_f32 v165, v74, v75
	v_add_f32_e32 v74, v74, v75
	v_add_f32_e32 v231, v231, v72
	v_mfma_f32_32x32x16_f16 v[48:63], v[204:207], v[172:175], v[48:63]
	ds_read_b128 v[204:207], v226 offset:23136
	v_exp_f32_e32 v78, v78
	v_exp_f32_e32 v79, v79
	v_cvt_pk_f16_f32 v166, v76, v77
	v_add_f32_e32 v76, v76, v77
	v_add_f32_e32 v231, v231, v74
	v_cvt_pk_f16_f32 v167, v78, v79
	v_add_f32_e32 v78, v78, v79
	v_add_f32_e32 v231, v231, v76
	v_add_f32_e32 v231, v231, v78
	v_cmp_nge_f32_e32 vcc, s34, v231
	s_cbranch_vccnz .Lovf_a21

.Lovfret_b21:
	v_add_f32_e32 v233, v233, v231
	s_waitcnt lgkmcnt(6)
	s_barrier
	s_add_u32 s23, s23, 1
	s_waitcnt vmcnt(8)
	v_cmp_ne_u32_e64 s[20:21], 0, v224
	s_add_u32 s31, s23, 1
	s_and_b32 s31, s31, 31
	s_lshl_b32 s31, s31, 8
	s_add_u32 s26, s31, s22
	s_add_u32 s31, s23, 3
	s_and_b32 s31, s31, 31
	s_mul_i32 s31, s31, 0xc0000
	s_add_u32 s24, s31, s18
	s_add_u32 s31, s23, 2
	s_and_b32 s31, s31, 31
	s_mul_i32 s31, s31, 0xc0000
	s_add_u32 s25, s31, s19
	s_cmp_eq_u64 s[20:21], -1
	s_cselect_b32 s34, s37, s38
	s_waitcnt lgkmcnt(4)
	v_mfma_f32_32x32x16_f16 v[80:95], v[176:179], v[144:147], v[112:127]
	ds_read_b128 v[176:179], v225 offset:32256
	buffer_load_dword v224, v230, s[8:11], s26 offen
	v_exp_f32_e32 v64, v64
	v_exp_f32_e32 v65, v65
	v_cvt_pk_f16_f32 v208, v208, v209
	v_cvt_pk_f16_f32 v209, v210, v211
	v_mfma_f32_32x32x16_f16 v[80:95], v[180:183], v[148:151], v[80:95]
	ds_read_b128 v[180:183], v225 offset:32288
	v_exp_f32_e32 v66, v66
	v_exp_f32_e32 v67, v67
	v_cvt_pk_f16_f32 v212, v212, v213
	v_cvt_pk_f16_f32 v160, v64, v65
	v_add_f32_e32 v64, v64, v65
	v_cvt_pk_f16_f32 v213, v214, v215
	v_mfma_f32_32x32x16_f16 v[80:95], v[184:187], v[152:155], v[80:95]
	ds_write_b64 v227, v[208:209] offset:9216
	ds_write_b64 v227, v[212:213] offset:13824
	ds_read_b128 v[184:187], v225 offset:32320
	v_exp_f32_e32 v68, v68
	v_exp_f32_e32 v69, v69
	v_cvt_pk_f16_f32 v161, v66, v67
	v_add_f32_e32 v66, v66, v67
	v_mfma_f32_32x32x16_f16 v[80:95], v[188:191], v[156:159], v[80:95]
	ds_read_b128 v[188:191], v225 offset:32352
	v_exp_f32_e32 v70, v70
	v_exp_f32_e32 v71, v71
	v_cvt_pk_f16_f32 v162, v68, v69
	v_add_f32_e32 v68, v68, v69
	v_add_f32_e32 v231, v64, v66
	s_waitcnt lgkmcnt(6)
	v_mfma_f32_32x32x16_f16 v[32:47], v[192:195], v[168:171], v[32:47]
	ds_read_b128 v[192:195], v226 offset:27648
	v_exp_f32_e32 v72, v72
	v_exp_f32_e32 v73, v73
	v_cvt_pk_f16_f32 v163, v70, v71
	v_add_f32_e32 v70, v70, v71
	v_add_f32_e32 v231, v231, v68
	v_mfma_f32_32x32x16_f16 v[48:63], v[196:199], v[168:171], v[48:63]
	ds_read_b128 v[196:199], v226 offset:32256
	v_exp_f32_e32 v74, v74
	v_exp_f32_e32 v75, v75
	v_cvt_pk_f16_f32 v164, v72, v73
	v_add_f32_e32 v72, v72, v73
	v_add_f32_e32 v231, v231, v70
	v_mfma_f32_32x32x16_f16 v[32:47], v[200:203], v[172:175], v[32:47]
	ds_read_b128 v[200:203], v226 offset:27680
	v_exp_f32_e32 v76, v76
	v_exp_f32_e32 v77, v77
	v_cvt_pk_f16_f32 v165, v74, v75
	v_add_f32_e32 v74, v74, v75
	v_add_f32_e32 v231, v231, v72
	v_mfma_f32_32x32x16_f16 v[48:63], v[204:207], v[172:175], v[48:63]
	ds_read_b128 v[204:207], v226 offset:32288
	v_exp_f32_e32 v78, v78
	v_exp_f32_e32 v79, v79
	v_cvt_pk_f16_f32 v166, v76, v77
	v_add_f32_e32 v76, v76, v77
	v_add_f32_e32 v231, v231, v74
	v_cvt_pk_f16_f32 v167, v78, v79
	v_add_f32_e32 v78, v78, v79
	v_add_f32_e32 v231, v231, v76
	v_add_f32_e32 v231, v231, v78
	v_cmp_nge_f32_e32 vcc, s34, v231
	s_cbranch_vccnz .Lovf_a30

.Lovfret_b30:
	v_add_f32_e32 v233, v233, v231
	s_waitcnt lgkmcnt(4)
	v_mfma_f32_32x32x16_f16 v[80:95], v[176:179], v[144:147], v[112:127]
	ds_read_b128 v[176:179], v225 offset:0
	s_waitcnt vmcnt(3)
	v_exp_f32_e32 v64, v64
	v_exp_f32_e32 v65, v65
	v_cvt_pk_f16_f32 v216, v216, v217
	v_cvt_pk_f16_f32 v217, v218, v219
	v_mfma_f32_32x32x16_f16 v[80:95], v[180:183], v[148:151], v[80:95]
	ds_read_b128 v[180:183], v225 offset:32
	v_exp_f32_e32 v66, v66
	v_exp_f32_e32 v67, v67
	v_cvt_pk_f16_f32 v218, v220, v221
	v_cvt_pk_f16_f32 v160, v64, v65
	v_add_f32_e32 v64, v64, v65
	v_cvt_pk_f16_f32 v219, v222, v223
	v_mfma_f32_32x32x16_f16 v[80:95], v[184:187], v[152:155], v[80:95]
	ds_write_b128 v228, v[216:219] offset:0
	ds_read_b128 v[184:187], v225 offset:64
	v_exp_f32_e32 v68, v68
	v_exp_f32_e32 v69, v69
	v_cvt_pk_f16_f32 v161, v66, v67
	v_add_f32_e32 v66, v66, v67
	v_mfma_f32_32x32x16_f16 v[80:95], v[188:191], v[156:159], v[80:95]
	ds_read_b128 v[188:191], v225 offset:96
	v_exp_f32_e32 v70, v70
	v_exp_f32_e32 v71, v71
	v_cvt_pk_f16_f32 v162, v68, v69
	v_add_f32_e32 v68, v68, v69
	v_add_f32_e32 v231, v64, v66
	s_waitcnt lgkmcnt(5)
	v_mfma_f32_32x32x16_f16 v[32:47], v[192:195], v[168:171], v[32:47]
	ds_read_b128 v[192:195], v226 offset:27712
	v_exp_f32_e32 v72, v72
	v_exp_f32_e32 v73, v73
	v_cvt_pk_f16_f32 v163, v70, v71
	v_add_f32_e32 v70, v70, v71
	v_add_f32_e32 v231, v231, v68
	v_mfma_f32_32x32x16_f16 v[48:63], v[196:199], v[168:171], v[48:63]
	ds_read_b128 v[196:199], v226 offset:32320
	v_exp_f32_e32 v74, v74
	v_exp_f32_e32 v75, v75
	v_cvt_pk_f16_f32 v164, v72, v73
	v_add_f32_e32 v72, v72, v73
	v_add_f32_e32 v231, v231, v70
	v_mfma_f32_32x32x16_f16 v[32:47], v[200:203], v[172:175], v[32:47]
	ds_read_b128 v[200:203], v226 offset:27744
	v_exp_f32_e32 v76, v76
	v_exp_f32_e32 v77, v77
	v_cvt_pk_f16_f32 v165, v74, v75
	v_add_f32_e32 v74, v74, v75
	v_add_f32_e32 v231, v231, v72
	v_mfma_f32_32x32x16_f16 v[48:63], v[204:207], v[172:175], v[48:63]
	ds_read_b128 v[204:207], v226 offset:32352
	v_exp_f32_e32 v78, v78
	v_exp_f32_e32 v79, v79
	v_cvt_pk_f16_f32 v166, v76, v77
	v_add_f32_e32 v76, v76, v77
	v_add_f32_e32 v231, v231, v74
	v_cvt_pk_f16_f32 v167, v78, v79
	v_add_f32_e32 v78, v78, v79
	v_add_f32_e32 v231, v231, v76
	v_add_f32_e32 v231, v231, v78
	v_cmp_nge_f32_e32 vcc, s34, v231
	s_cbranch_vccnz .Lovf_a31

.Lovfret_b31:
	v_add_f32_e32 v233, v233, v231
	s_waitcnt lgkmcnt(6)
	s_barrier
	s_add_u32 s23, s23, 1
	s_add_u32 s27, s27, 1
	s_cmp_eq_u32 s27, 7
	s_cbranch_scc0 .Lbody
	s_nop 15
	s_nop 7
	v_mov_b32_e32 v235, v232
	v_mov_b32_e32 v236, v232
	s_nop 1
	v_permlane32_swap_b32_e32 v235, v236
	v_add_f32_e32 v236, v235, v236
	v_rcp_f32_e32 v237, v236
	s_nop 0
	v_fma_f32 v238, -v236, v237, 1.0
	v_fmac_f32_e32 v237, v238, v237
	v_mul_f32_e32 v0, v237, v0
	v_mul_f32_e32 v1, v237, v1
	v_mul_f32_e32 v2, v237, v2
	v_mul_f32_e32 v3, v237, v3
	v_mul_f32_e32 v4, v237, v4
	v_mul_f32_e32 v5, v237, v5
	v_mul_f32_e32 v6, v237, v6
	v_mul_f32_e32 v7, v237, v7
	v_mul_f32_e32 v8, v237, v8
	v_mul_f32_e32 v9, v237, v9
	v_mul_f32_e32 v10, v237, v10
	v_mul_f32_e32 v11, v237, v11
	v_mul_f32_e32 v12, v237, v12
	v_mul_f32_e32 v13, v237, v13
	v_mul_f32_e32 v14, v237, v14
	v_mul_f32_e32 v15, v237, v15
	v_mul_f32_e32 v16, v237, v16
	v_mul_f32_e32 v17, v237, v17
	v_mul_f32_e32 v18, v237, v18
	v_mul_f32_e32 v19, v237, v19
	v_mul_f32_e32 v20, v237, v20
	v_mul_f32_e32 v21, v237, v21
	v_mul_f32_e32 v22, v237, v22
	v_mul_f32_e32 v23, v237, v23
	v_mul_f32_e32 v24, v237, v24
	v_mul_f32_e32 v25, v237, v25
	v_mul_f32_e32 v26, v237, v26
	v_mul_f32_e32 v27, v237, v27
	v_mul_f32_e32 v28, v237, v28
	v_mul_f32_e32 v29, v237, v29
	v_mul_f32_e32 v30, v237, v30
	v_mul_f32_e32 v31, v237, v31
	ds_write_b128 v241, v[0:3] offset:0
	ds_write_b128 v241, v[16:19] offset:128
	ds_write_b128 v241, v[4:7] offset:32
	ds_write_b128 v241, v[20:23] offset:160
	ds_write_b128 v241, v[8:11] offset:64
	ds_write_b128 v241, v[24:27] offset:192
	ds_write_b128 v241, v[12:15] offset:96
	ds_write_b128 v241, v[28:31] offset:224
	s_waitcnt lgkmcnt(0)
	ds_read_b128 v[0:3], v242 offset:0
	ds_read_b128 v[4:7], v242 offset:1088
	ds_read_b128 v[8:11], v242 offset:2176
	ds_read_b128 v[12:15], v242 offset:3264
	ds_read_b128 v[16:19], v242 offset:4352
	ds_read_b128 v[20:23], v242 offset:5440
	ds_read_b128 v[24:27], v242 offset:6528
	ds_read_b128 v[28:31], v242 offset:7616
	s_waitcnt lgkmcnt(7)
	s_add_u32 s31, s30, 0x0
	buffer_store_dwordx4 v[0:3], v244, s[12:15], s31 offen nt sc1
	s_waitcnt lgkmcnt(6)
	s_add_u32 s31, s30, 0x4000
	buffer_store_dwordx4 v[4:7], v244, s[12:15], s31 offen nt sc1
	s_waitcnt lgkmcnt(5)
	s_add_u32 s31, s30, 0x8000
	buffer_store_dwordx4 v[8:11], v244, s[12:15], s31 offen nt sc1
	s_waitcnt lgkmcnt(4)
	s_add_u32 s31, s30, 0xc000
	buffer_store_dwordx4 v[12:15], v244, s[12:15], s31 offen nt sc1
	s_waitcnt lgkmcnt(3)
	s_add_u32 s31, s30, 0x10000
	buffer_store_dwordx4 v[16:19], v244, s[12:15], s31 offen nt sc1
	s_waitcnt lgkmcnt(2)
	s_add_u32 s31, s30, 0x14000
	buffer_store_dwordx4 v[20:23], v244, s[12:15], s31 offen nt sc1
	s_waitcnt lgkmcnt(1)
	s_add_u32 s31, s30, 0x18000
	buffer_store_dwordx4 v[24:27], v244, s[12:15], s31 offen nt sc1
	s_waitcnt lgkmcnt(0)
	s_add_u32 s31, s30, 0x1c000
	buffer_store_dwordx4 v[28:31], v244, s[12:15], s31 offen nt sc1
	s_nop 1
	s_waitcnt vmcnt(8)
	v_cmp_ne_u32_e64 s[20:21], 0, v224
	s_add_u32 s31, s23, 1
	s_and_b32 s31, s31, 31
	s_lshl_b32 s31, s31, 8
	s_add_u32 s26, s31, s22
	s_add_u32 s31, s23, 3
	s_and_b32 s31, s31, 31
	s_mul_i32 s31, s31, 0xc0000
	s_add_u32 s24, s31, s18
	s_add_u32 s31, s23, 2
	s_and_b32 s31, s31, 31
	s_mul_i32 s31, s31, 0xc0000
	s_add_u32 s25, s31, s19
	s_cmp_eq_u64 s[20:21], -1
	s_cselect_b32 s34, s37, s38
	s_waitcnt lgkmcnt(4)
	v_mfma_f32_32x32x16_f16 v[80:95], v[176:179], v[144:147], v[112:127]
	ds_read_b128 v[176:179], v225 offset:4608
	buffer_load_dword v224, v230, s[8:11], s26 offen
	v_cvt_pk_f16_f32 v208, v208, v209
	v_cvt_pk_f16_f32 v209, v210, v211
	v_mfma_f32_32x32x16_f16 v[80:95], v[180:183], v[148:151], v[80:95]
	ds_read_b128 v[180:183], v225 offset:4640
	v_cvt_pk_f16_f32 v212, v212, v213
	v_cvt_pk_f16_f32 v213, v214, v215
	v_mfma_f32_32x32x16_f16 v[80:95], v[184:187], v[152:155], v[80:95]
	ds_write_b64 v227, v[208:209] offset:18432
	ds_write_b64 v227, v[212:213] offset:23040
	ds_read_b128 v[184:187], v225 offset:4672
	v_mfma_f32_32x32x16_f16 v[80:95], v[188:191], v[156:159], v[80:95]
	ds_read_b128 v[188:191], v225 offset:4704
	s_waitcnt lgkmcnt(6)
	v_mfma_f32_32x32x16_f16 v[32:47], v[192:195], v[168:171], v[32:47]
	ds_read_b128 v[192:195], v226 offset:0
	v_mfma_f32_32x32x16_f16 v[48:63], v[196:199], v[168:171], v[48:63]
	ds_read_b128 v[196:199], v226 offset:4608
	v_mfma_f32_32x32x16_f16 v[32:47], v[200:203], v[172:175], v[32:47]
	ds_read_b128 v[200:203], v226 offset:32
	v_mfma_f32_32x32x16_f16 v[48:63], v[204:207], v[172:175], v[48:63]
	ds_read_b128 v[204:207], v226 offset:4640
	s_nop 7
	v_exp_f32_e32 v80, v80
	v_exp_f32_e32 v81, v81
	buffer_load_dwordx4 v[208:211], v229, s[4:7], s24 offen
	v_exp_f32_e32 v82, v82
	v_exp_f32_e32 v83, v83
	v_cvt_pk_f16_f32 v168, v80, v81
	v_add_f32_e32 v80, v80, v81
	s_add_u32 s31, s24, 0x60000
	buffer_load_dwordx4 v[212:215], v229, s[4:7], s31 offen
	v_exp_f32_e32 v84, v84
	v_exp_f32_e32 v85, v85
	v_cvt_pk_f16_f32 v169, v82, v83
	v_add_f32_e32 v82, v82, v83
	v_exp_f32_e32 v86, v86
	v_exp_f32_e32 v87, v87
	v_cvt_pk_f16_f32 v170, v84, v85
	v_add_f32_e32 v84, v84, v85
	v_add_f32_e32 v231, v80, v82
	v_exp_f32_e32 v88, v88
	v_exp_f32_e32 v89, v89
	v_cvt_pk_f16_f32 v171, v86, v87
	v_add_f32_e32 v86, v86, v87
	v_add_f32_e32 v231, v231, v84
	v_exp_f32_e32 v90, v90
	v_exp_f32_e32 v91, v91
	v_cvt_pk_f16_f32 v172, v88, v89
	v_add_f32_e32 v88, v88, v89
	v_add_f32_e32 v231, v231, v86
	v_exp_f32_e32 v92, v92
	v_exp_f32_e32 v93, v93
	v_cvt_pk_f16_f32 v173, v90, v91
	v_add_f32_e32 v90, v90, v91
	v_add_f32_e32 v231, v231, v88
	v_exp_f32_e32 v94, v94
	v_exp_f32_e32 v95, v95
	v_cvt_pk_f16_f32 v174, v92, v93
	v_add_f32_e32 v92, v92, v93
	v_add_f32_e32 v231, v231, v90
	v_cvt_pk_f16_f32 v175, v94, v95
	v_add_f32_e32 v94, v94, v95
	v_add_f32_e32 v231, v231, v92
	v_add_f32_e32 v231, v231, v94
	v_cmp_nge_f32_e32 vcc, s34, v231
	s_cbranch_vccnz .Lovf_b00q
.Lovfret_b00q:
	v_add_f32_e32 v233, v233, v231
	s_waitcnt lgkmcnt(4)
	v_mfma_f32_32x32x16_f16 v[80:95], v[176:179], v[144:147], v[112:127]
	ds_read_b128 v[176:179], v225 offset:9216
	s_waitcnt vmcnt(3)
	v_cvt_pk_f16_f32 v216, v216, v217
	v_cvt_pk_f16_f32 v217, v218, v219
	v_mfma_f32_32x32x16_f16 v[80:95], v[180:183], v[148:151], v[80:95]
	ds_read_b128 v[180:183], v225 offset:9248
	v_cvt_pk_f16_f32 v218, v220, v221
	v_cvt_pk_f16_f32 v219, v222, v223
	v_mfma_f32_32x32x16_f16 v[80:95], v[184:187], v[152:155], v[80:95]
	ds_write_b128 v228, v[216:219] offset:9216
	ds_read_b128 v[184:187], v225 offset:9280
	v_mfma_f32_32x32x16_f16 v[80:95], v[188:191], v[156:159], v[80:95]
	ds_read_b128 v[188:191], v225 offset:9312
	s_waitcnt lgkmcnt(5)
	v_mfma_f32_32x32x16_f16 v[32:47], v[192:195], v[168:171], v[32:47]
	ds_read_b128 v[192:195], v226 offset:64
	v_mfma_f32_32x32x16_f16 v[48:63], v[196:199], v[168:171], v[48:63]
	ds_read_b128 v[196:199], v226 offset:4672
	v_mfma_f32_32x32x16_f16 v[32:47], v[200:203], v[172:175], v[32:47]
	ds_read_b128 v[200:203], v226 offset:96
	v_mfma_f32_32x32x16_f16 v[48:63], v[204:207], v[172:175], v[48:63]
	ds_read_b128 v[204:207], v226 offset:4704
	s_nop 7
	buffer_load_dword v216, v230, s[4:7], s25 offen
	v_exp_f32_e32 v80, v80
	v_exp_f32_e32 v81, v81
	s_add_u32 s31, s25, 0x3000
	buffer_load_dword v217, v230, s[4:7], s31 offen
	v_exp_f32_e32 v82, v82
	v_exp_f32_e32 v83, v83
	v_cvt_pk_f16_f32 v168, v80, v81
	v_add_f32_e32 v80, v80, v81
	s_add_u32 s31, s25, 0x6000
	buffer_load_dword v218, v230, s[4:7], s31 offen
	v_exp_f32_e32 v84, v84
	v_exp_f32_e32 v85, v85
	v_cvt_pk_f16_f32 v169, v82, v83
	v_add_f32_e32 v82, v82, v83
	s_add_u32 s31, s25, 0x9000
	buffer_load_dword v219, v230, s[4:7], s31 offen
	v_exp_f32_e32 v86, v86
	v_exp_f32_e32 v87, v87
	v_cvt_pk_f16_f32 v170, v84, v85
	v_add_f32_e32 v84, v84, v85
	v_add_f32_e32 v231, v80, v82
	s_add_u32 s31, s25, 0x18000
	buffer_load_dword v220, v230, s[4:7], s31 offen
	v_exp_f32_e32 v88, v88
	v_exp_f32_e32 v89, v89
	v_cvt_pk_f16_f32 v171, v86, v87
	v_add_f32_e32 v86, v86, v87
	v_add_f32_e32 v231, v231, v84
	s_add_u32 s31, s25, 0x1b000
	buffer_load_dword v221, v230, s[4:7], s31 offen
	v_exp_f32_e32 v90, v90
	v_exp_f32_e32 v91, v91
	v_cvt_pk_f16_f32 v172, v88, v89
	v_add_f32_e32 v88, v88, v89
	v_add_f32_e32 v231, v231, v86
	s_add_u32 s31, s25, 0x1e000
	buffer_load_dword v222, v230, s[4:7], s31 offen
	v_exp_f32_e32 v92, v92
	v_exp_f32_e32 v93, v93
	v_cvt_pk_f16_f32 v173, v90, v91
	v_add_f32_e32 v90, v90, v91
	v_add_f32_e32 v231, v231, v88
	s_add_u32 s31, s25, 0x21000
	buffer_load_dword v223, v230, s[4:7], s31 offen
	v_exp_f32_e32 v94, v94
	v_exp_f32_e32 v95, v95
	v_cvt_pk_f16_f32 v174, v92, v93
	v_add_f32_e32 v92, v92, v93
	v_add_f32_e32 v231, v231, v90
	v_cvt_pk_f16_f32 v175, v94, v95
	v_add_f32_e32 v94, v94, v95
	v_add_f32_e32 v231, v231, v92
	v_add_f32_e32 v231, v231, v94
	v_cmp_nge_f32_e32 vcc, s34, v231
	s_cbranch_vccnz .Lovf_b01q
.Lovfret_b01q:
	v_add_f32_e32 v233, v233, v231
	s_waitcnt lgkmcnt(6)
	s_barrier
	s_add_u32 s23, s23, 1
	s_waitcnt vmcnt(8)
	v_cmp_ne_u32_e64 s[20:21], 0, v224
	s_add_u32 s31, s23, 1
	s_and_b32 s31, s31, 31
	s_lshl_b32 s31, s31, 8
	s_add_u32 s26, s31, s22
	s_add_u32 s31, s23, 3
	s_and_b32 s31, s31, 31
	s_mul_i32 s31, s31, 0xc0000
	s_add_u32 s24, s31, s18
	s_add_u32 s31, s23, 2
	s_and_b32 s31, s31, 31
	s_mul_i32 s31, s31, 0xc0000
	s_add_u32 s25, s31, s19
	s_cmp_eq_u64 s[20:21], -1
	s_cselect_b32 s34, s37, s38
	s_waitcnt lgkmcnt(4)
	v_mfma_f32_32x32x16_f16 v[80:95], v[176:179], v[144:147], v[112:127]
	ds_read_b128 v[176:179], v225 offset:13824
	buffer_load_dword v224, v230, s[8:11], s26 offen
	v_cvt_pk_f16_f32 v208, v208, v209
	v_cvt_pk_f16_f32 v209, v210, v211
	v_mfma_f32_32x32x16_f16 v[80:95], v[180:183], v[148:151], v[80:95]
	ds_read_b128 v[180:183], v225 offset:13856
	v_cvt_pk_f16_f32 v212, v212, v213
	v_cvt_pk_f16_f32 v213, v214, v215
	v_mfma_f32_32x32x16_f16 v[80:95], v[184:187], v[152:155], v[80:95]
	ds_write_b64 v227, v[208:209] offset:27648
	ds_write_b64 v227, v[212:213] offset:32256
	ds_read_b128 v[184:187], v225 offset:13888
	v_mfma_f32_32x32x16_f16 v[80:95], v[188:191], v[156:159], v[80:95]
	ds_read_b128 v[188:191], v225 offset:13920
	s_waitcnt lgkmcnt(6)
	v_mfma_f32_32x32x16_f16 v[32:47], v[192:195], v[168:171], v[32:47]
	ds_read_b128 v[192:195], v226 offset:9216
	v_mfma_f32_32x32x16_f16 v[48:63], v[196:199], v[168:171], v[48:63]
	ds_read_b128 v[196:199], v226 offset:13824
	v_mfma_f32_32x32x16_f16 v[32:47], v[200:203], v[172:175], v[32:47]
	ds_read_b128 v[200:203], v226 offset:9248
	v_mfma_f32_32x32x16_f16 v[48:63], v[204:207], v[172:175], v[48:63]
	ds_read_b128 v[204:207], v226 offset:13856
	s_nop 7
	v_exp_f32_e32 v80, v80
	v_exp_f32_e32 v81, v81
	buffer_load_dwordx4 v[208:211], v229, s[4:7], s24 offen
	v_exp_f32_e32 v82, v82
	v_exp_f32_e32 v83, v83
	v_cvt_pk_f16_f32 v168, v80, v81
	v_add_f32_e32 v80, v80, v81
	s_add_u32 s31, s24, 0x60000
	buffer_load_dwordx4 v[212:215], v229, s[4:7], s31 offen
	v_exp_f32_e32 v84, v84
	v_exp_f32_e32 v85, v85
	v_cvt_pk_f16_f32 v169, v82, v83
	v_add_f32_e32 v82, v82, v83
	v_exp_f32_e32 v86, v86
	v_exp_f32_e32 v87, v87
	v_cvt_pk_f16_f32 v170, v84, v85
	v_add_f32_e32 v84, v84, v85
	v_add_f32_e32 v231, v80, v82
	v_exp_f32_e32 v88, v88
	v_exp_f32_e32 v89, v89
	v_cvt_pk_f16_f32 v171, v86, v87
	v_add_f32_e32 v86, v86, v87
	v_add_f32_e32 v231, v231, v84
	v_exp_f32_e32 v90, v90
	v_exp_f32_e32 v91, v91
	v_cvt_pk_f16_f32 v172, v88, v89
	v_add_f32_e32 v88, v88, v89
	v_add_f32_e32 v231, v231, v86
	v_exp_f32_e32 v92, v92
	v_exp_f32_e32 v93, v93
	v_cvt_pk_f16_f32 v173, v90, v91
	v_add_f32_e32 v90, v90, v91
	v_add_f32_e32 v231, v231, v88
	v_exp_f32_e32 v94, v94
	v_exp_f32_e32 v95, v95
	v_cvt_pk_f16_f32 v174, v92, v93
	v_add_f32_e32 v92, v92, v93
	v_add_f32_e32 v231, v231, v90
	v_cvt_pk_f16_f32 v175, v94, v95
	v_add_f32_e32 v94, v94, v95
	v_add_f32_e32 v231, v231, v92
	v_add_f32_e32 v231, v231, v94
	v_cmp_nge_f32_e32 vcc, s34, v231
	s_cbranch_vccnz .Lovf_b10q
.Lovfret_b10q:
	v_add_f32_e32 v233, v233, v231
	s_waitcnt lgkmcnt(4)
	v_mfma_f32_32x32x16_f16 v[80:95], v[176:179], v[144:147], v[112:127]
	ds_read_b128 v[176:179], v225 offset:18432
	s_waitcnt vmcnt(3)
	v_cvt_pk_f16_f32 v216, v216, v217
	v_cvt_pk_f16_f32 v217, v218, v219
	v_mfma_f32_32x32x16_f16 v[80:95], v[180:183], v[148:151], v[80:95]
	ds_read_b128 v[180:183], v225 offset:18464
	v_cvt_pk_f16_f32 v218, v220, v221
	v_cvt_pk_f16_f32 v219, v222, v223
	v_mfma_f32_32x32x16_f16 v[80:95], v[184:187], v[152:155], v[80:95]
	ds_write_b128 v228, v[216:219] offset:18432
	ds_read_b128 v[184:187], v225 offset:18496
	v_mfma_f32_32x32x16_f16 v[80:95], v[188:191], v[156:159], v[80:95]
	ds_read_b128 v[188:191], v225 offset:18528
	s_waitcnt lgkmcnt(5)
	v_mfma_f32_32x32x16_f16 v[32:47], v[192:195], v[168:171], v[32:47]
	ds_read_b128 v[192:195], v226 offset:9280
	v_mfma_f32_32x32x16_f16 v[48:63], v[196:199], v[168:171], v[48:63]
	ds_read_b128 v[196:199], v226 offset:13888
	v_mfma_f32_32x32x16_f16 v[32:47], v[200:203], v[172:175], v[32:47]
	ds_read_b128 v[200:203], v226 offset:9312
	v_mfma_f32_32x32x16_f16 v[48:63], v[204:207], v[172:175], v[48:63]
	ds_read_b128 v[204:207], v226 offset:13920
	s_nop 7
	buffer_load_dword v216, v230, s[4:7], s25 offen
	v_exp_f32_e32 v80, v80
	v_exp_f32_e32 v81, v81
	s_add_u32 s31, s25, 0x3000
	buffer_load_dword v217, v230, s[4:7], s31 offen
	v_exp_f32_e32 v82, v82
	v_exp_f32_e32 v83, v83
	v_cvt_pk_f16_f32 v168, v80, v81
	v_add_f32_e32 v80, v80, v81
	s_add_u32 s31, s25, 0x6000
	buffer_load_dword v218, v230, s[4:7], s31 offen
	v_exp_f32_e32 v84, v84
	v_exp_f32_e32 v85, v85
	v_cvt_pk_f16_f32 v169, v82, v83
	v_add_f32_e32 v82, v82, v83
	s_add_u32 s31, s25, 0x9000
	buffer_load_dword v219, v230, s[4:7], s31 offen
	v_exp_f32_e32 v86, v86
	v_exp_f32_e32 v87, v87
	v_cvt_pk_f16_f32 v170, v84, v85
	v_add_f32_e32 v84, v84, v85
	v_add_f32_e32 v231, v80, v82
	s_add_u32 s31, s25, 0x18000
	buffer_load_dword v220, v230, s[4:7], s31 offen
	v_exp_f32_e32 v88, v88
	v_exp_f32_e32 v89, v89
	v_cvt_pk_f16_f32 v171, v86, v87
	v_add_f32_e32 v86, v86, v87
	v_add_f32_e32 v231, v231, v84
	s_add_u32 s31, s25, 0x1b000
	buffer_load_dword v221, v230, s[4:7], s31 offen
	v_exp_f32_e32 v90, v90
	v_exp_f32_e32 v91, v91
	v_cvt_pk_f16_f32 v172, v88, v89
	v_add_f32_e32 v88, v88, v89
	v_add_f32_e32 v231, v231, v86
	s_add_u32 s31, s25, 0x1e000
	buffer_load_dword v222, v230, s[4:7], s31 offen
	v_exp_f32_e32 v92, v92
	v_exp_f32_e32 v93, v93
	v_cvt_pk_f16_f32 v173, v90, v91
	v_add_f32_e32 v90, v90, v91
	v_add_f32_e32 v231, v231, v88
	s_add_u32 s31, s25, 0x21000
	buffer_load_dword v223, v230, s[4:7], s31 offen
	v_exp_f32_e32 v94, v94
	v_exp_f32_e32 v95, v95
	v_cvt_pk_f16_f32 v174, v92, v93
	v_add_f32_e32 v92, v92, v93
	v_add_f32_e32 v231, v231, v90
	v_cvt_pk_f16_f32 v175, v94, v95
	v_add_f32_e32 v94, v94, v95
	v_add_f32_e32 v231, v231, v92
	v_add_f32_e32 v231, v231, v94
	v_cmp_nge_f32_e32 vcc, s34, v231
	s_cbranch_vccnz .Lovf_b11q
.Lovfret_b11q:
	v_add_f32_e32 v233, v233, v231
	s_waitcnt lgkmcnt(6)
	s_barrier
	s_add_u32 s23, s23, 1
	s_waitcnt vmcnt(8)
	v_cmp_ne_u32_e64 s[20:21], 0, v224
	s_add_u32 s31, s23, 1
	s_and_b32 s31, s31, 31
	s_lshl_b32 s31, s31, 8
	s_add_u32 s26, s31, s22
	s_add_u32 s31, s23, 3
	s_and_b32 s31, s31, 31
	s_mul_i32 s31, s31, 0xc0000
	s_add_u32 s24, s31, s18
	s_add_u32 s31, s23, 2
	s_and_b32 s31, s31, 31
	s_mul_i32 s31, s31, 0xc0000
	s_add_u32 s25, s31, s19
	s_cmp_eq_u64 s[20:21], -1
	s_cselect_b32 s34, s37, s38
	s_waitcnt lgkmcnt(4)
	v_mfma_f32_32x32x16_f16 v[80:95], v[176:179], v[144:147], v[112:127]
	ds_read_b128 v[176:179], v225 offset:23040
	buffer_load_dword v224, v230, s[8:11], s26 offen
	v_cvt_pk_f16_f32 v208, v208, v209
	v_cvt_pk_f16_f32 v209, v210, v211
	v_mfma_f32_32x32x16_f16 v[80:95], v[180:183], v[148:151], v[80:95]
	ds_read_b128 v[180:183], v225 offset:23072
	v_cvt_pk_f16_f32 v212, v212, v213
	v_cvt_pk_f16_f32 v213, v214, v215
	v_mfma_f32_32x32x16_f16 v[80:95], v[184:187], v[152:155], v[80:95]
	ds_write_b64 v227, v[208:209] offset:0
	ds_write_b64 v227, v[212:213] offset:4608
	ds_read_b128 v[184:187], v225 offset:23104
	v_mfma_f32_32x32x16_f16 v[80:95], v[188:191], v[156:159], v[80:95]
	ds_read_b128 v[188:191], v225 offset:23136
	s_waitcnt lgkmcnt(6)
	v_mfma_f32_32x32x16_f16 v[32:47], v[192:195], v[168:171], v[32:47]
	ds_read_b128 v[192:195], v226 offset:18432
	v_mfma_f32_32x32x16_f16 v[48:63], v[196:199], v[168:171], v[48:63]
	ds_read_b128 v[196:199], v226 offset:23040
	v_mfma_f32_32x32x16_f16 v[32:47], v[200:203], v[172:175], v[32:47]
	ds_read_b128 v[200:203], v226 offset:18464
	v_mfma_f32_32x32x16_f16 v[48:63], v[204:207], v[172:175], v[48:63]
	ds_read_b128 v[204:207], v226 offset:23072
	s_nop 7
	v_exp_f32_e32 v80, v80
	v_exp_f32_e32 v81, v81
	buffer_load_dwordx4 v[208:211], v229, s[4:7], s24 offen
	v_exp_f32_e32 v82, v82
	v_exp_f32_e32 v83, v83
	v_cvt_pk_f16_f32 v168, v80, v81
	v_add_f32_e32 v80, v80, v81
	s_add_u32 s31, s24, 0x60000
	buffer_load_dwordx4 v[212:215], v229, s[4:7], s31 offen
	v_exp_f32_e32 v84, v84
	v_exp_f32_e32 v85, v85
	v_cvt_pk_f16_f32 v169, v82, v83
	v_add_f32_e32 v82, v82, v83
	v_exp_f32_e32 v86, v86
	v_exp_f32_e32 v87, v87
	v_cvt_pk_f16_f32 v170, v84, v85
	v_add_f32_e32 v84, v84, v85
	v_add_f32_e32 v231, v80, v82
	v_exp_f32_e32 v88, v88
	v_exp_f32_e32 v89, v89
	v_cvt_pk_f16_f32 v171, v86, v87
	v_add_f32_e32 v86, v86, v87
	v_add_f32_e32 v231, v231, v84
	v_exp_f32_e32 v90, v90
	v_exp_f32_e32 v91, v91
	v_cvt_pk_f16_f32 v172, v88, v89
	v_add_f32_e32 v88, v88, v89
	v_add_f32_e32 v231, v231, v86
	v_exp_f32_e32 v92, v92
	v_exp_f32_e32 v93, v93
	v_cvt_pk_f16_f32 v173, v90, v91
	v_add_f32_e32 v90, v90, v91
	v_add_f32_e32 v231, v231, v88
	v_exp_f32_e32 v94, v94
	v_exp_f32_e32 v95, v95
	v_cvt_pk_f16_f32 v174, v92, v93
	v_add_f32_e32 v92, v92, v93
	v_add_f32_e32 v231, v231, v90
	v_cvt_pk_f16_f32 v175, v94, v95
	v_add_f32_e32 v94, v94, v95
	v_add_f32_e32 v231, v231, v92
	v_add_f32_e32 v231, v231, v94
	v_cmp_nge_f32_e32 vcc, s34, v231
	s_cbranch_vccnz .Lovf_b20q
.Lovfret_b20q:
	v_add_f32_e32 v233, v233, v231
	s_waitcnt lgkmcnt(4)
	v_mfma_f32_32x32x16_f16 v[80:95], v[176:179], v[144:147], v[112:127]
	ds_read_b128 v[176:179], v225 offset:27648
	s_waitcnt vmcnt(3)
	v_cvt_pk_f16_f32 v216, v216, v217
	v_cvt_pk_f16_f32 v217, v218, v219
	v_mfma_f32_32x32x16_f16 v[80:95], v[180:183], v[148:151], v[80:95]
	ds_read_b128 v[180:183], v225 offset:27680
	v_cvt_pk_f16_f32 v218, v220, v221
	v_cvt_pk_f16_f32 v219, v222, v223
	v_mfma_f32_32x32x16_f16 v[80:95], v[184:187], v[152:155], v[80:95]
	ds_write_b128 v228, v[216:219] offset:27648
	ds_read_b128 v[184:187], v225 offset:27712
	v_mfma_f32_32x32x16_f16 v[80:95], v[188:191], v[156:159], v[80:95]
	ds_read_b128 v[188:191], v225 offset:27744
	s_waitcnt lgkmcnt(5)
	v_mfma_f32_32x32x16_f16 v[32:47], v[192:195], v[168:171], v[32:47]
	ds_read_b128 v[192:195], v226 offset:18496
	v_mfma_f32_32x32x16_f16 v[48:63], v[196:199], v[168:171], v[48:63]
	ds_read_b128 v[196:199], v226 offset:23104
	v_mfma_f32_32x32x16_f16 v[32:47], v[200:203], v[172:175], v[32:47]
	ds_read_b128 v[200:203], v226 offset:18528
	v_mfma_f32_32x32x16_f16 v[48:63], v[204:207], v[172:175], v[48:63]
	ds_read_b128 v[204:207], v226 offset:23136
	s_nop 7
	buffer_load_dword v216, v230, s[4:7], s25 offen
	v_exp_f32_e32 v80, v80
	v_exp_f32_e32 v81, v81
	s_add_u32 s31, s25, 0x3000
	buffer_load_dword v217, v230, s[4:7], s31 offen
	v_exp_f32_e32 v82, v82
	v_exp_f32_e32 v83, v83
	v_cvt_pk_f16_f32 v168, v80, v81
	v_add_f32_e32 v80, v80, v81
	s_add_u32 s31, s25, 0x6000
	buffer_load_dword v218, v230, s[4:7], s31 offen
	v_exp_f32_e32 v84, v84
	v_exp_f32_e32 v85, v85
	v_cvt_pk_f16_f32 v169, v82, v83
	v_add_f32_e32 v82, v82, v83
	s_add_u32 s31, s25, 0x9000
	buffer_load_dword v219, v230, s[4:7], s31 offen
	v_exp_f32_e32 v86, v86
	v_exp_f32_e32 v87, v87
	v_cvt_pk_f16_f32 v170, v84, v85
	v_add_f32_e32 v84, v84, v85
	v_add_f32_e32 v231, v80, v82
	s_add_u32 s31, s25, 0x18000
	buffer_load_dword v220, v230, s[4:7], s31 offen
	v_exp_f32_e32 v88, v88
	v_exp_f32_e32 v89, v89
	v_cvt_pk_f16_f32 v171, v86, v87
	v_add_f32_e32 v86, v86, v87
	v_add_f32_e32 v231, v231, v84
	s_add_u32 s31, s25, 0x1b000
	buffer_load_dword v221, v230, s[4:7], s31 offen
	v_exp_f32_e32 v90, v90
	v_exp_f32_e32 v91, v91
	v_cvt_pk_f16_f32 v172, v88, v89
	v_add_f32_e32 v88, v88, v89
	v_add_f32_e32 v231, v231, v86
	s_add_u32 s31, s25, 0x1e000
	buffer_load_dword v222, v230, s[4:7], s31 offen
	v_exp_f32_e32 v92, v92
	v_exp_f32_e32 v93, v93
	v_cvt_pk_f16_f32 v173, v90, v91
	v_add_f32_e32 v90, v90, v91
	v_add_f32_e32 v231, v231, v88
	s_add_u32 s31, s25, 0x21000
	buffer_load_dword v223, v230, s[4:7], s31 offen
	v_exp_f32_e32 v94, v94
	v_exp_f32_e32 v95, v95
	v_cvt_pk_f16_f32 v174, v92, v93
	v_add_f32_e32 v92, v92, v93
	v_add_f32_e32 v231, v231, v90
	v_cvt_pk_f16_f32 v175, v94, v95
	v_add_f32_e32 v94, v94, v95
	v_add_f32_e32 v231, v231, v92
	v_add_f32_e32 v231, v231, v94
	v_cmp_nge_f32_e32 vcc, s34, v231
	s_cbranch_vccnz .Lovf_b21q
.Lovfret_b21q:
	v_add_f32_e32 v233, v233, v231
	s_waitcnt lgkmcnt(6)
	s_barrier
	s_add_u32 s23, s23, 1
	s_waitcnt vmcnt(8)
	v_cmp_ne_u32_e64 s[20:21], 0, v224
	s_add_u32 s31, s23, 1
	s_and_b32 s31, s31, 31
	s_lshl_b32 s31, s31, 8
	s_add_u32 s26, s31, s22
	s_add_u32 s31, s23, 3
	s_and_b32 s31, s31, 31
	s_mul_i32 s31, s31, 0xc0000
	s_add_u32 s24, s31, s18
	s_add_u32 s31, s23, 2
	s_and_b32 s31, s31, 31
	s_mul_i32 s31, s31, 0xc0000
	s_add_u32 s25, s31, s19
	s_cmp_eq_u64 s[20:21], -1
	s_cselect_b32 s34, s37, s38
	s_waitcnt lgkmcnt(4)
	v_mfma_f32_32x32x16_f16 v[80:95], v[176:179], v[144:147], v[112:127]
	ds_read_b128 v[176:179], v225 offset:32256
	buffer_load_dword v224, v230, s[8:11], s26 offen
	v_cvt_pk_f16_f32 v208, v208, v209
	v_cvt_pk_f16_f32 v209, v210, v211
	v_mfma_f32_32x32x16_f16 v[80:95], v[180:183], v[148:151], v[80:95]
	ds_read_b128 v[180:183], v225 offset:32288
	v_cvt_pk_f16_f32 v212, v212, v213
	v_cvt_pk_f16_f32 v213, v214, v215
	v_mfma_f32_32x32x16_f16 v[80:95], v[184:187], v[152:155], v[80:95]
	ds_write_b64 v227, v[208:209] offset:9216
	ds_write_b64 v227, v[212:213] offset:13824
	ds_read_b128 v[184:187], v225 offset:32320
	v_mfma_f32_32x32x16_f16 v[80:95], v[188:191], v[156:159], v[80:95]
	ds_read_b128 v[188:191], v225 offset:32352
	s_waitcnt lgkmcnt(6)
	v_mfma_f32_32x32x16_f16 v[32:47], v[192:195], v[168:171], v[32:47]
	ds_read_b128 v[192:195], v226 offset:27648
	v_mfma_f32_32x32x16_f16 v[48:63], v[196:199], v[168:171], v[48:63]
	ds_read_b128 v[196:199], v226 offset:32256
	v_mfma_f32_32x32x16_f16 v[32:47], v[200:203], v[172:175], v[32:47]
	ds_read_b128 v[200:203], v226 offset:27680
	v_mfma_f32_32x32x16_f16 v[48:63], v[204:207], v[172:175], v[48:63]
	ds_read_b128 v[204:207], v226 offset:32288
	s_nop 7
	v_exp_f32_e32 v80, v80
	v_exp_f32_e32 v81, v81
	buffer_load_dwordx4 v[208:211], v229, s[4:7], s24 offen
	v_exp_f32_e32 v82, v82
	v_exp_f32_e32 v83, v83
	v_cvt_pk_f16_f32 v168, v80, v81
	v_add_f32_e32 v80, v80, v81
	s_add_u32 s31, s24, 0x60000
	buffer_load_dwordx4 v[212:215], v229, s[4:7], s31 offen
	v_exp_f32_e32 v84, v84
	v_exp_f32_e32 v85, v85
	v_cvt_pk_f16_f32 v169, v82, v83
	v_add_f32_e32 v82, v82, v83
	v_exp_f32_e32 v86, v86
	v_exp_f32_e32 v87, v87
	v_cvt_pk_f16_f32 v170, v84, v85
	v_add_f32_e32 v84, v84, v85
	v_add_f32_e32 v231, v80, v82
	v_exp_f32_e32 v88, v88
	v_exp_f32_e32 v89, v89
	v_cvt_pk_f16_f32 v171, v86, v87
	v_add_f32_e32 v86, v86, v87
	v_add_f32_e32 v231, v231, v84
	v_exp_f32_e32 v90, v90
	v_exp_f32_e32 v91, v91
	v_cvt_pk_f16_f32 v172, v88, v89
	v_add_f32_e32 v88, v88, v89
	v_add_f32_e32 v231, v231, v86
	v_exp_f32_e32 v92, v92
	v_exp_f32_e32 v93, v93
	v_cvt_pk_f16_f32 v173, v90, v91
	v_add_f32_e32 v90, v90, v91
	v_add_f32_e32 v231, v231, v88
	v_exp_f32_e32 v94, v94
	v_exp_f32_e32 v95, v95
	v_cvt_pk_f16_f32 v174, v92, v93
	v_add_f32_e32 v92, v92, v93
	v_add_f32_e32 v231, v231, v90
	v_cvt_pk_f16_f32 v175, v94, v95
	v_add_f32_e32 v94, v94, v95
	v_add_f32_e32 v231, v231, v92
	v_add_f32_e32 v231, v231, v94
	v_cmp_nge_f32_e32 vcc, s34, v231
	s_cbranch_vccnz .Lovf_b30q
.Lovfret_b30q:
	v_add_f32_e32 v233, v233, v231
	s_waitcnt lgkmcnt(4)
	v_mfma_f32_32x32x16_f16 v[80:95], v[176:179], v[144:147], v[112:127]
	ds_read_b128 v[176:179], v225 offset:0
	s_waitcnt vmcnt(3)
	v_cvt_pk_f16_f32 v216, v216, v217
	v_cvt_pk_f16_f32 v217, v218, v219
	v_mfma_f32_32x32x16_f16 v[80:95], v[180:183], v[148:151], v[80:95]
	ds_read_b128 v[180:183], v225 offset:32
	v_cvt_pk_f16_f32 v218, v220, v221
	v_cvt_pk_f16_f32 v219, v222, v223
	v_mfma_f32_32x32x16_f16 v[80:95], v[184:187], v[152:155], v[80:95]
	ds_write_b128 v228, v[216:219] offset:0
	ds_read_b128 v[184:187], v225 offset:64
	v_mfma_f32_32x32x16_f16 v[80:95], v[188:191], v[156:159], v[80:95]
	ds_read_b128 v[188:191], v225 offset:96
	s_waitcnt lgkmcnt(5)
	v_mfma_f32_32x32x16_f16 v[32:47], v[192:195], v[168:171], v[32:47]
	ds_read_b128 v[192:195], v226 offset:27712
	v_mfma_f32_32x32x16_f16 v[48:63], v[196:199], v[168:171], v[48:63]
	ds_read_b128 v[196:199], v226 offset:32320
	v_mfma_f32_32x32x16_f16 v[32:47], v[200:203], v[172:175], v[32:47]
	ds_read_b128 v[200:203], v226 offset:27744
	v_mfma_f32_32x32x16_f16 v[48:63], v[204:207], v[172:175], v[48:63]
	ds_read_b128 v[204:207], v226 offset:32352
	s_nop 7
	buffer_load_dword v216, v230, s[4:7], s25 offen
	v_exp_f32_e32 v80, v80
	v_exp_f32_e32 v81, v81
	s_add_u32 s31, s25, 0x3000
	buffer_load_dword v217, v230, s[4:7], s31 offen
	v_exp_f32_e32 v82, v82
	v_exp_f32_e32 v83, v83
	v_cvt_pk_f16_f32 v168, v80, v81
	v_add_f32_e32 v80, v80, v81
	s_add_u32 s31, s25, 0x6000
	buffer_load_dword v218, v230, s[4:7], s31 offen
	v_exp_f32_e32 v84, v84
	v_exp_f32_e32 v85, v85
	v_cvt_pk_f16_f32 v169, v82, v83
	v_add_f32_e32 v82, v82, v83
	s_add_u32 s31, s25, 0x9000
	buffer_load_dword v219, v230, s[4:7], s31 offen
	v_exp_f32_e32 v86, v86
	v_exp_f32_e32 v87, v87
	v_cvt_pk_f16_f32 v170, v84, v85
	v_add_f32_e32 v84, v84, v85
	v_add_f32_e32 v231, v80, v82
	s_add_u32 s31, s25, 0x18000
	buffer_load_dword v220, v230, s[4:7], s31 offen
	v_exp_f32_e32 v88, v88
	v_exp_f32_e32 v89, v89
	v_cvt_pk_f16_f32 v171, v86, v87
	v_add_f32_e32 v86, v86, v87
	v_add_f32_e32 v231, v231, v84
	s_add_u32 s31, s25, 0x1b000
	buffer_load_dword v221, v230, s[4:7], s31 offen
	v_exp_f32_e32 v90, v90
	v_exp_f32_e32 v91, v91
	v_cvt_pk_f16_f32 v172, v88, v89
	v_add_f32_e32 v88, v88, v89
	v_add_f32_e32 v231, v231, v86
	s_add_u32 s31, s25, 0x1e000
	buffer_load_dword v222, v230, s[4:7], s31 offen
	v_exp_f32_e32 v92, v92
	v_exp_f32_e32 v93, v93
	v_cvt_pk_f16_f32 v173, v90, v91
	v_add_f32_e32 v90, v90, v91
	v_add_f32_e32 v231, v231, v88
	s_add_u32 s31, s25, 0x21000
	buffer_load_dword v223, v230, s[4:7], s31 offen
	v_exp_f32_e32 v94, v94
	v_exp_f32_e32 v95, v95
	v_cvt_pk_f16_f32 v174, v92, v93
	v_add_f32_e32 v92, v92, v93
	v_add_f32_e32 v231, v231, v90
	v_cvt_pk_f16_f32 v175, v94, v95
	v_add_f32_e32 v94, v94, v95
	v_add_f32_e32 v231, v231, v92
	v_add_f32_e32 v231, v231, v94
	v_cmp_nge_f32_e32 vcc, s34, v231
	s_cbranch_vccnz .Lovf_b31q
.Lovfret_b31q:
	v_add_f32_e32 v233, v233, v231
	s_waitcnt lgkmcnt(6)
	s_barrier
	s_add_u32 s23, s23, 1
	s_waitcnt lgkmcnt(0)
	v_mfma_f32_32x32x16_f16 v[32:47], v[192:195], v[168:171], v[32:47]
	v_mfma_f32_32x32x16_f16 v[48:63], v[196:199], v[168:171], v[48:63]
	v_mfma_f32_32x32x16_f16 v[32:47], v[200:203], v[172:175], v[32:47]
	v_mfma_f32_32x32x16_f16 v[48:63], v[204:207], v[172:175], v[48:63]
	s_nop 15
	s_nop 7
	v_mov_b32_e32 v235, v233
	v_mov_b32_e32 v236, v233
	s_nop 1
	v_permlane32_swap_b32_e32 v235, v236
	v_add_f32_e32 v236, v235, v236
	v_rcp_f32_e32 v237, v236
	s_nop 0
	v_fma_f32 v238, -v236, v237, 1.0
	v_fmac_f32_e32 v237, v238, v237
	v_mul_f32_e32 v32, v237, v32
	v_mul_f32_e32 v33, v237, v33
	v_mul_f32_e32 v34, v237, v34
	v_mul_f32_e32 v35, v237, v35
	v_mul_f32_e32 v36, v237, v36
	v_mul_f32_e32 v37, v237, v37
	v_mul_f32_e32 v38, v237, v38
	v_mul_f32_e32 v39, v237, v39
	v_mul_f32_e32 v40, v237, v40
	v_mul_f32_e32 v41, v237, v41
	v_mul_f32_e32 v42, v237, v42
	v_mul_f32_e32 v43, v237, v43
	v_mul_f32_e32 v44, v237, v44
	v_mul_f32_e32 v45, v237, v45
	v_mul_f32_e32 v46, v237, v46
	v_mul_f32_e32 v47, v237, v47
	v_mul_f32_e32 v48, v237, v48
	v_mul_f32_e32 v49, v237, v49
	v_mul_f32_e32 v50, v237, v50
	v_mul_f32_e32 v51, v237, v51
	v_mul_f32_e32 v52, v237, v52
	v_mul_f32_e32 v53, v237, v53
	v_mul_f32_e32 v54, v237, v54
	v_mul_f32_e32 v55, v237, v55
	v_mul_f32_e32 v56, v237, v56
	v_mul_f32_e32 v57, v237, v57
	v_mul_f32_e32 v58, v237, v58
	v_mul_f32_e32 v59, v237, v59
	v_mul_f32_e32 v60, v237, v60
	v_mul_f32_e32 v61, v237, v61
	v_mul_f32_e32 v62, v237, v62
	v_mul_f32_e32 v63, v237, v63
	ds_write_b128 v241, v[32:35] offset:0
	ds_write_b128 v241, v[48:51] offset:128
	ds_write_b128 v241, v[36:39] offset:32
	ds_write_b128 v241, v[52:55] offset:160
	ds_write_b128 v241, v[40:43] offset:64
	ds_write_b128 v241, v[56:59] offset:192
	ds_write_b128 v241, v[44:47] offset:96
	ds_write_b128 v241, v[60:63] offset:224
	s_waitcnt lgkmcnt(0)
	ds_read_b128 v[32:35], v242 offset:0
	ds_read_b128 v[36:39], v242 offset:1088
	ds_read_b128 v[40:43], v242 offset:2176
	ds_read_b128 v[44:47], v242 offset:3264
	ds_read_b128 v[48:51], v242 offset:4352
	ds_read_b128 v[52:55], v242 offset:5440
	ds_read_b128 v[56:59], v242 offset:6528
	ds_read_b128 v[60:63], v242 offset:7616
	s_waitcnt lgkmcnt(7)
	s_add_u32 s31, s30, 0x400000
	buffer_store_dwordx4 v[32:35], v244, s[12:15], s31 offen nt sc1
	s_waitcnt lgkmcnt(6)
	s_add_u32 s31, s30, 0x404000
	buffer_store_dwordx4 v[36:39], v244, s[12:15], s31 offen nt sc1
	s_waitcnt lgkmcnt(5)
	s_add_u32 s31, s30, 0x408000
	buffer_store_dwordx4 v[40:43], v244, s[12:15], s31 offen nt sc1
	s_waitcnt lgkmcnt(4)
	s_add_u32 s31, s30, 0x40c000
	buffer_store_dwordx4 v[44:47], v244, s[12:15], s31 offen nt sc1
	s_waitcnt lgkmcnt(3)
	s_add_u32 s31, s30, 0x410000
	buffer_store_dwordx4 v[48:51], v244, s[12:15], s31 offen nt sc1
	s_waitcnt lgkmcnt(2)
	s_add_u32 s31, s30, 0x414000
	buffer_store_dwordx4 v[52:55], v244, s[12:15], s31 offen nt sc1
	s_waitcnt lgkmcnt(1)
	s_add_u32 s31, s30, 0x418000
	buffer_store_dwordx4 v[56:59], v244, s[12:15], s31 offen nt sc1
	s_waitcnt lgkmcnt(0)
	s_add_u32 s31, s30, 0x41c000
	buffer_store_dwordx4 v[60:63], v244, s[12:15], s31 offen nt sc1
	s_endpgm

.Lovfnm_a00p:
	v_max3_f32 v235, v64, v65, v66
	v_max3_f32 v235, v235, v67, v68
	v_max3_f32 v235, v235, v69, v70
	v_max3_f32 v235, v235, v71, v72
	v_max3_f32 v235, v235, v73, v74
	v_max3_f32 v235, v235, v75, v76
	v_max3_f32 v235, v235, v77, v78
	v_max_f32_e32 v235, v235, v79
	v_mov_b32_e32 v236, v235
	s_nop 1
	v_permlane32_swap_b32_e32 v235, v236
	v_max_f32_e32 v235, v235, v236
	v_max_f32_e32 v235, 0, v235
	v_exp_f32_e64 v237, -v235
	v_sub_f32_e32 v96, v96, v235
	v_sub_f32_e32 v97, v97, v235
	v_sub_f32_e32 v98, v98, v235
	v_sub_f32_e32 v99, v99, v235
	v_sub_f32_e32 v100, v100, v235
	v_sub_f32_e32 v101, v101, v235
	v_sub_f32_e32 v102, v102, v235
	v_sub_f32_e32 v103, v103, v235
	v_sub_f32_e32 v104, v104, v235
	v_sub_f32_e32 v105, v105, v235
	v_sub_f32_e32 v106, v106, v235
	v_sub_f32_e32 v107, v107, v235
	v_sub_f32_e32 v108, v108, v235
	v_sub_f32_e32 v109, v109, v235
	v_sub_f32_e32 v110, v110, v235
	v_sub_f32_e32 v111, v111, v235
	v_mul_f32_e32 v232, v232, v237
	v_mul_f32_e32 v0, v0, v237
	v_mul_f32_e32 v1, v1, v237
	v_mul_f32_e32 v2, v2, v237
	v_mul_f32_e32 v3, v3, v237
	v_mul_f32_e32 v4, v4, v237
	v_mul_f32_e32 v5, v5, v237
	v_mul_f32_e32 v6, v6, v237
	v_mul_f32_e32 v7, v7, v237
	v_mul_f32_e32 v8, v8, v237
	v_mul_f32_e32 v9, v9, v237
	v_mul_f32_e32 v10, v10, v237
	v_mul_f32_e32 v11, v11, v237
	v_mul_f32_e32 v12, v12, v237
	v_mul_f32_e32 v13, v13, v237
	v_mul_f32_e32 v14, v14, v237
	v_mul_f32_e32 v15, v15, v237
	v_mul_f32_e32 v16, v16, v237
	v_mul_f32_e32 v17, v17, v237
	v_mul_f32_e32 v18, v18, v237
	v_mul_f32_e32 v19, v19, v237
	v_mul_f32_e32 v20, v20, v237
	v_mul_f32_e32 v21, v21, v237
	v_mul_f32_e32 v22, v22, v237
	v_mul_f32_e32 v23, v23, v237
	v_mul_f32_e32 v24, v24, v237
	v_mul_f32_e32 v25, v25, v237
	v_mul_f32_e32 v26, v26, v237
	v_mul_f32_e32 v27, v27, v237
	v_mul_f32_e32 v28, v28, v237
	v_mul_f32_e32 v29, v29, v237
	v_mul_f32_e32 v30, v30, v237
	v_mul_f32_e32 v31, v31, v237
	v_sub_f32_e32 v64, v64, v235
	v_sub_f32_e32 v65, v65, v235
	v_sub_f32_e32 v66, v66, v235
	v_sub_f32_e32 v67, v67, v235
	v_sub_f32_e32 v68, v68, v235
	v_sub_f32_e32 v69, v69, v235
	v_sub_f32_e32 v70, v70, v235
	v_sub_f32_e32 v71, v71, v235
	v_sub_f32_e32 v72, v72, v235
	v_sub_f32_e32 v73, v73, v235
	v_sub_f32_e32 v74, v74, v235
	v_sub_f32_e32 v75, v75, v235
	v_sub_f32_e32 v76, v76, v235
	v_sub_f32_e32 v77, v77, v235
	v_sub_f32_e32 v78, v78, v235
	v_sub_f32_e32 v79, v79, v235
	v_exp_f32_e32 v64, v64
	v_exp_f32_e32 v65, v65
	v_exp_f32_e32 v66, v66
	v_exp_f32_e32 v67, v67
	v_exp_f32_e32 v68, v68
	v_exp_f32_e32 v69, v69
	v_exp_f32_e32 v70, v70
	v_exp_f32_e32 v71, v71
	v_exp_f32_e32 v72, v72
	v_exp_f32_e32 v73, v73
	v_exp_f32_e32 v74, v74
	v_exp_f32_e32 v75, v75
	v_exp_f32_e32 v76, v76
	v_exp_f32_e32 v77, v77
	v_exp_f32_e32 v78, v78
	v_exp_f32_e32 v79, v79
	s_nop 0
	v_add_f32_e32 v231, v64, v65
	v_add_f32_e32 v231, v231, v66
	v_add_f32_e32 v231, v231, v67
	v_add_f32_e32 v231, v231, v68
	v_add_f32_e32 v231, v231, v69
	v_add_f32_e32 v231, v231, v70
	v_add_f32_e32 v231, v231, v71
	v_add_f32_e32 v231, v231, v72
	v_add_f32_e32 v231, v231, v73
	v_add_f32_e32 v231, v231, v74
	v_add_f32_e32 v231, v231, v75
	v_add_f32_e32 v231, v231, v76
	v_add_f32_e32 v231, v231, v77
	v_add_f32_e32 v231, v231, v78
	v_add_f32_e32 v231, v231, v79
	v_cvt_pk_f16_f32 v160, v64, v65
	v_cvt_pk_f16_f32 v161, v66, v67
	v_cvt_pk_f16_f32 v162, v68, v69
	v_cvt_pk_f16_f32 v163, v70, v71
	v_cvt_pk_f16_f32 v164, v72, v73
	v_cvt_pk_f16_f32 v165, v74, v75
	v_cvt_pk_f16_f32 v166, v76, v77
	v_cvt_pk_f16_f32 v167, v78, v79
	s_branch .Lovfret_a00p
.Lovf_a01p:
	s_waitcnt lgkmcnt(0)
	s_nop 15
	s_nop 15
	s_nop 15
	ds_read_b128 v[168:171], v225 offset:4608
	ds_read_b128 v[172:175], v225 offset:4640
	s_waitcnt lgkmcnt(0)
	v_mfma_f32_32x32x16_f16 v[64:79], v[168:171], v[128:131], v[96:111]
	v_mfma_f32_32x32x16_f16 v[64:79], v[172:175], v[132:135], v[64:79]
	s_nop 15
	ds_read_b128 v[168:171], v225 offset:4672
	ds_read_b128 v[172:175], v225 offset:4704
	s_waitcnt lgkmcnt(0)
	v_mfma_f32_32x32x16_f16 v[64:79], v[168:171], v[136:139], v[64:79]
	v_mfma_f32_32x32x16_f16 v[64:79], v[172:175], v[140:143], v[64:79]
	s_nop 15
	s_nop 15
	s_cmp_eq_u64 s[20:21], -1
	s_cbranch_scc1 .Lovfnm_a01p
	v_lshrrev_b32_e64 v235, v234, s21
	v_bfe_u32 v236, v235, 0, 1
	v_cvt_f32_u32_e32 v236, v236
	v_sub_f32_e32 v236, 1.0, v236
	v_fmac_f32_e32 v64, s35, v236
	v_bfe_u32 v236, v235, 1, 1
	v_cvt_f32_u32_e32 v236, v236
	v_sub_f32_e32 v236, 1.0, v236
	v_fmac_f32_e32 v65, s35, v236
	v_bfe_u32 v236, v235, 2, 1
	v_cvt_f32_u32_e32 v236, v236
	v_sub_f32_e32 v236, 1.0, v236
	v_fmac_f32_e32 v66, s35, v236
	v_bfe_u32 v236, v235, 3, 1
	v_cvt_f32_u32_e32 v236, v236
	v_sub_f32_e32 v236, 1.0, v236
	v_fmac_f32_e32 v67, s35, v236
	v_bfe_u32 v236, v235, 8, 1
	v_cvt_f32_u32_e32 v236, v236
	v_sub_f32_e32 v236, 1.0, v236
	v_fmac_f32_e32 v68, s35, v236
	v_bfe_u32 v236, v235, 9, 1
	v_cvt_f32_u32_e32 v236, v236
	v_sub_f32_e32 v236, 1.0, v236
	v_fmac_f32_e32 v69, s35, v236
	v_bfe_u32 v236, v235, 10, 1
	v_cvt_f32_u32_e32 v236, v236
	v_sub_f32_e32 v236, 1.0, v236
	v_fmac_f32_e32 v70, s35, v236
	v_bfe_u32 v236, v235, 11, 1
	v_cvt_f32_u32_e32 v236, v236
	v_sub_f32_e32 v236, 1.0, v236
	v_fmac_f32_e32 v71, s35, v236
	v_bfe_u32 v236, v235, 16, 1
	v_cvt_f32_u32_e32 v236, v236
	v_sub_f32_e32 v236, 1.0, v236
	v_fmac_f32_e32 v72, s35, v236
	v_bfe_u32 v236, v235, 17, 1
	v_cvt_f32_u32_e32 v236, v236
	v_sub_f32_e32 v236, 1.0, v236
	v_fmac_f32_e32 v73, s35, v236
	v_bfe_u32 v236, v235, 18, 1
	v_cvt_f32_u32_e32 v236, v236
	v_sub_f32_e32 v236, 1.0, v236
	v_fmac_f32_e32 v74, s35, v236
	v_bfe_u32 v236, v235, 19, 1
	v_cvt_f32_u32_e32 v236, v236
	v_sub_f32_e32 v236, 1.0, v236
	v_fmac_f32_e32 v75, s35, v236
	v_bfe_u32 v236, v235, 24, 1
	v_cvt_f32_u32_e32 v236, v236
	v_sub_f32_e32 v236, 1.0, v236
	v_fmac_f32_e32 v76, s35, v236
	v_bfe_u32 v236, v235, 25, 1
	v_cvt_f32_u32_e32 v236, v236
	v_sub_f32_e32 v236, 1.0, v236
	v_fmac_f32_e32 v77, s35, v236
	v_bfe_u32 v236, v235, 26, 1
	v_cvt_f32_u32_e32 v236, v236
	v_sub_f32_e32 v236, 1.0, v236
	v_fmac_f32_e32 v78, s35, v236
	v_bfe_u32 v236, v235, 27, 1
	v_cvt_f32_u32_e32 v236, v236
	v_sub_f32_e32 v236, 1.0, v236
	v_fmac_f32_e32 v79, s35, v236
.Lovfnm_a01p:
	v_max3_f32 v235, v64, v65, v66
	v_max3_f32 v235, v235, v67, v68
	v_max3_f32 v235, v235, v69, v70
	v_max3_f32 v235, v235, v71, v72
	v_max3_f32 v235, v235, v73, v74
	v_max3_f32 v235, v235, v75, v76
	v_max3_f32 v235, v235, v77, v78
	v_max_f32_e32 v235, v235, v79
	v_mov_b32_e32 v236, v235
	s_nop 1
	v_permlane32_swap_b32_e32 v235, v236
	v_max_f32_e32 v235, v235, v236
	v_max_f32_e32 v235, 0, v235
	v_exp_f32_e64 v237, -v235
	v_sub_f32_e32 v96, v96, v235
	v_sub_f32_e32 v97, v97, v235
	v_sub_f32_e32 v98, v98, v235
	v_sub_f32_e32 v99, v99, v235
	v_sub_f32_e32 v100, v100, v235
	v_sub_f32_e32 v101, v101, v235
	v_sub_f32_e32 v102, v102, v235
	v_sub_f32_e32 v103, v103, v235
	v_sub_f32_e32 v104, v104, v235
	v_sub_f32_e32 v105, v105, v235
	v_sub_f32_e32 v106, v106, v235
	v_sub_f32_e32 v107, v107, v235
	v_sub_f32_e32 v108, v108, v235
	v_sub_f32_e32 v109, v109, v235
	v_sub_f32_e32 v110, v110, v235
	v_sub_f32_e32 v111, v111, v235
	v_mul_f32_e32 v232, v232, v237
	v_mul_f32_e32 v0, v0, v237
	v_mul_f32_e32 v1, v1, v237
	v_mul_f32_e32 v2, v2, v237
	v_mul_f32_e32 v3, v3, v237
	v_mul_f32_e32 v4, v4, v237
	v_mul_f32_e32 v5, v5, v237
	v_mul_f32_e32 v6, v6, v237
	v_mul_f32_e32 v7, v7, v237
	v_mul_f32_e32 v8, v8, v237
	v_mul_f32_e32 v9, v9, v237
	v_mul_f32_e32 v10, v10, v237
	v_mul_f32_e32 v11, v11, v237
	v_mul_f32_e32 v12, v12, v237
	v_mul_f32_e32 v13, v13, v237
	v_mul_f32_e32 v14, v14, v237
	v_mul_f32_e32 v15, v15, v237
	v_mul_f32_e32 v16, v16, v237
	v_mul_f32_e32 v17, v17, v237
	v_mul_f32_e32 v18, v18, v237
	v_mul_f32_e32 v19, v19, v237
	v_mul_f32_e32 v20, v20, v237
	v_mul_f32_e32 v21, v21, v237
	v_mul_f32_e32 v22, v22, v237
	v_mul_f32_e32 v23, v23, v237
	v_mul_f32_e32 v24, v24, v237
	v_mul_f32_e32 v25, v25, v237
	v_mul_f32_e32 v26, v26, v237
	v_mul_f32_e32 v27, v27, v237
	v_mul_f32_e32 v28, v28, v237
	v_mul_f32_e32 v29, v29, v237
	v_mul_f32_e32 v30, v30, v237
	v_mul_f32_e32 v31, v31, v237
	v_sub_f32_e32 v64, v64, v235
	v_sub_f32_e32 v65, v65, v235
	v_sub_f32_e32 v66, v66, v235
	v_sub_f32_e32 v67, v67, v235
	v_sub_f32_e32 v68, v68, v235
	v_sub_f32_e32 v69, v69, v235
	v_sub_f32_e32 v70, v70, v235
	v_sub_f32_e32 v71, v71, v235
	v_sub_f32_e32 v72, v72, v235
	v_sub_f32_e32 v73, v73, v235
	v_sub_f32_e32 v74, v74, v235
	v_sub_f32_e32 v75, v75, v235
	v_sub_f32_e32 v76, v76, v235
	v_sub_f32_e32 v77, v77, v235
	v_sub_f32_e32 v78, v78, v235
	v_sub_f32_e32 v79, v79, v235
	v_exp_f32_e32 v64, v64
	v_exp_f32_e32 v65, v65
	v_exp_f32_e32 v66, v66
	v_exp_f32_e32 v67, v67
	v_exp_f32_e32 v68, v68
	v_exp_f32_e32 v69, v69
	v_exp_f32_e32 v70, v70
	v_exp_f32_e32 v71, v71
	v_exp_f32_e32 v72, v72
	v_exp_f32_e32 v73, v73
	v_exp_f32_e32 v74, v74
	v_exp_f32_e32 v75, v75
	v_exp_f32_e32 v76, v76
	v_exp_f32_e32 v77, v77
	v_exp_f32_e32 v78, v78
	v_exp_f32_e32 v79, v79
	s_nop 0
	v_add_f32_e32 v231, v64, v65
	v_add_f32_e32 v231, v231, v66
	v_add_f32_e32 v231, v231, v67
	v_add_f32_e32 v231, v231, v68
	v_add_f32_e32 v231, v231, v69
	v_add_f32_e32 v231, v231, v70
	v_add_f32_e32 v231, v231, v71
	v_add_f32_e32 v231, v231, v72
	v_add_f32_e32 v231, v231, v73
	v_add_f32_e32 v231, v231, v74
	v_add_f32_e32 v231, v231, v75
	v_add_f32_e32 v231, v231, v76
	v_add_f32_e32 v231, v231, v77
	v_add_f32_e32 v231, v231, v78
	v_add_f32_e32 v231, v231, v79
	v_cvt_pk_f16_f32 v160, v64, v65
	v_cvt_pk_f16_f32 v161, v66, v67
	v_cvt_pk_f16_f32 v162, v68, v69
	v_cvt_pk_f16_f32 v163, v70, v71
	v_cvt_pk_f16_f32 v164, v72, v73
	v_cvt_pk_f16_f32 v165, v74, v75
	v_cvt_pk_f16_f32 v166, v76, v77
	v_cvt_pk_f16_f32 v167, v78, v79
	s_branch .Lovfret_a01p
.Lovf_a10p:
	s_waitcnt lgkmcnt(0)
	s_nop 15
	s_nop 15
	s_nop 15
	ds_read_b128 v[168:171], v225 offset:9216
	ds_read_b128 v[172:175], v225 offset:9248
	s_waitcnt lgkmcnt(0)
	v_mfma_f32_32x32x16_f16 v[64:79], v[168:171], v[128:131], v[96:111]
	v_mfma_f32_32x32x16_f16 v[64:79], v[172:175], v[132:135], v[64:79]
	s_nop 15
	ds_read_b128 v[168:171], v225 offset:9280
	ds_read_b128 v[172:175], v225 offset:9312
	s_waitcnt lgkmcnt(0)
	v_mfma_f32_32x32x16_f16 v[64:79], v[168:171], v[136:139], v[64:79]
	v_mfma_f32_32x32x16_f16 v[64:79], v[172:175], v[140:143], v[64:79]
	s_nop 15
	s_nop 15
	s_cmp_eq_u64 s[20:21], -1
	s_cbranch_scc1 .Lovfnm_a10p
	v_lshrrev_b32_e64 v235, v234, s20
	v_bfe_u32 v236, v235, 0, 1
	v_cvt_f32_u32_e32 v236, v236
	v_sub_f32_e32 v236, 1.0, v236
	v_fmac_f32_e32 v64, s35, v236
	v_bfe_u32 v236, v235, 1, 1
	v_cvt_f32_u32_e32 v236, v236
	v_sub_f32_e32 v236, 1.0, v236
	v_fmac_f32_e32 v65, s35, v236
	v_bfe_u32 v236, v235, 2, 1
	v_cvt_f32_u32_e32 v236, v236
	v_sub_f32_e32 v236, 1.0, v236
	v_fmac_f32_e32 v66, s35, v236
	v_bfe_u32 v236, v235, 3, 1
	v_cvt_f32_u32_e32 v236, v236
	v_sub_f32_e32 v236, 1.0, v236
	v_fmac_f32_e32 v67, s35, v236
	v_bfe_u32 v236, v235, 8, 1
	v_cvt_f32_u32_e32 v236, v236
	v_sub_f32_e32 v236, 1.0, v236
	v_fmac_f32_e32 v68, s35, v236
	v_bfe_u32 v236, v235, 9, 1
	v_cvt_f32_u32_e32 v236, v236
	v_sub_f32_e32 v236, 1.0, v236
	v_fmac_f32_e32 v69, s35, v236
	v_bfe_u32 v236, v235, 10, 1
	v_cvt_f32_u32_e32 v236, v236
	v_sub_f32_e32 v236, 1.0, v236
	v_fmac_f32_e32 v70, s35, v236
	v_bfe_u32 v236, v235, 11, 1
	v_cvt_f32_u32_e32 v236, v236
	v_sub_f32_e32 v236, 1.0, v236
	v_fmac_f32_e32 v71, s35, v236
	v_bfe_u32 v236, v235, 16, 1
	v_cvt_f32_u32_e32 v236, v236
	v_sub_f32_e32 v236, 1.0, v236
	v_fmac_f32_e32 v72, s35, v236
	v_bfe_u32 v236, v235, 17, 1
	v_cvt_f32_u32_e32 v236, v236
	v_sub_f32_e32 v236, 1.0, v236
	v_fmac_f32_e32 v73, s35, v236
	v_bfe_u32 v236, v235, 18, 1
	v_cvt_f32_u32_e32 v236, v236
	v_sub_f32_e32 v236, 1.0, v236
	v_fmac_f32_e32 v74, s35, v236
	v_bfe_u32 v236, v235, 19, 1
	v_cvt_f32_u32_e32 v236, v236
	v_sub_f32_e32 v236, 1.0, v236
	v_fmac_f32_e32 v75, s35, v236
	v_bfe_u32 v236, v235, 24, 1
	v_cvt_f32_u32_e32 v236, v236
	v_sub_f32_e32 v236, 1.0, v236
	v_fmac_f32_e32 v76, s35, v236
	v_bfe_u32 v236, v235, 25, 1
	v_cvt_f32_u32_e32 v236, v236
	v_sub_f32_e32 v236, 1.0, v236
	v_fmac_f32_e32 v77, s35, v236
	v_bfe_u32 v236, v235, 26, 1
	v_cvt_f32_u32_e32 v236, v236
	v_sub_f32_e32 v236, 1.0, v236
	v_fmac_f32_e32 v78, s35, v236
	v_bfe_u32 v236, v235, 27, 1
	v_cvt_f32_u32_e32 v236, v236
	v_sub_f32_e32 v236, 1.0, v236
	v_fmac_f32_e32 v79, s35, v236
.Lovfnm_a10p:
	v_max3_f32 v235, v64, v65, v66
	v_max3_f32 v235, v235, v67, v68
	v_max3_f32 v235, v235, v69, v70
	v_max3_f32 v235, v235, v71, v72
	v_max3_f32 v235, v235, v73, v74
	v_max3_f32 v235, v235, v75, v76
	v_max3_f32 v235, v235, v77, v78
	v_max_f32_e32 v235, v235, v79
	v_mov_b32_e32 v236, v235
	s_nop 1
	v_permlane32_swap_b32_e32 v235, v236
	v_max_f32_e32 v235, v235, v236
	v_max_f32_e32 v235, 0, v235
	v_exp_f32_e64 v237, -v235
	v_sub_f32_e32 v96, v96, v235
	v_sub_f32_e32 v97, v97, v235
	v_sub_f32_e32 v98, v98, v235
	v_sub_f32_e32 v99, v99, v235
	v_sub_f32_e32 v100, v100, v235
	v_sub_f32_e32 v101, v101, v235
	v_sub_f32_e32 v102, v102, v235
	v_sub_f32_e32 v103, v103, v235
	v_sub_f32_e32 v104, v104, v235
	v_sub_f32_e32 v105, v105, v235
	v_sub_f32_e32 v106, v106, v235
	v_sub_f32_e32 v107, v107, v235
	v_sub_f32_e32 v108, v108, v235
	v_sub_f32_e32 v109, v109, v235
	v_sub_f32_e32 v110, v110, v235
	v_sub_f32_e32 v111, v111, v235
	v_mul_f32_e32 v232, v232, v237
	v_mul_f32_e32 v0, v0, v237
	v_mul_f32_e32 v1, v1, v237
	v_mul_f32_e32 v2, v2, v237
	v_mul_f32_e32 v3, v3, v237
	v_mul_f32_e32 v4, v4, v237
	v_mul_f32_e32 v5, v5, v237
	v_mul_f32_e32 v6, v6, v237
	v_mul_f32_e32 v7, v7, v237
	v_mul_f32_e32 v8, v8, v237
	v_mul_f32_e32 v9, v9, v237
	v_mul_f32_e32 v10, v10, v237
	v_mul_f32_e32 v11, v11, v237
	v_mul_f32_e32 v12, v12, v237
	v_mul_f32_e32 v13, v13, v237
	v_mul_f32_e32 v14, v14, v237
	v_mul_f32_e32 v15, v15, v237
	v_mul_f32_e32 v16, v16, v237
	v_mul_f32_e32 v17, v17, v237
	v_mul_f32_e32 v18, v18, v237
	v_mul_f32_e32 v19, v19, v237
	v_mul_f32_e32 v20, v20, v237
	v_mul_f32_e32 v21, v21, v237
	v_mul_f32_e32 v22, v22, v237
	v_mul_f32_e32 v23, v23, v237
	v_mul_f32_e32 v24, v24, v237
	v_mul_f32_e32 v25, v25, v237
	v_mul_f32_e32 v26, v26, v237
	v_mul_f32_e32 v27, v27, v237
	v_mul_f32_e32 v28, v28, v237
	v_mul_f32_e32 v29, v29, v237
	v_mul_f32_e32 v30, v30, v237
	v_mul_f32_e32 v31, v31, v237
	v_sub_f32_e32 v64, v64, v235
	v_sub_f32_e32 v65, v65, v235
	v_sub_f32_e32 v66, v66, v235
	v_sub_f32_e32 v67, v67, v235
	v_sub_f32_e32 v68, v68, v235
	v_sub_f32_e32 v69, v69, v235
	v_sub_f32_e32 v70, v70, v235
	v_sub_f32_e32 v71, v71, v235
	v_sub_f32_e32 v72, v72, v235
	v_sub_f32_e32 v73, v73, v235
	v_sub_f32_e32 v74, v74, v235
	v_sub_f32_e32 v75, v75, v235
	v_sub_f32_e32 v76, v76, v235
	v_sub_f32_e32 v77, v77, v235
	v_sub_f32_e32 v78, v78, v235
	v_sub_f32_e32 v79, v79, v235
	v_exp_f32_e32 v64, v64
	v_exp_f32_e32 v65, v65
	v_exp_f32_e32 v66, v66
	v_exp_f32_e32 v67, v67
	v_exp_f32_e32 v68, v68
	v_exp_f32_e32 v69, v69
	v_exp_f32_e32 v70, v70
	v_exp_f32_e32 v71, v71
	v_exp_f32_e32 v72, v72
	v_exp_f32_e32 v73, v73
	v_exp_f32_e32 v74, v74
	v_exp_f32_e32 v75, v75
	v_exp_f32_e32 v76, v76
	v_exp_f32_e32 v77, v77
	v_exp_f32_e32 v78, v78
	v_exp_f32_e32 v79, v79
	s_nop 0
	v_add_f32_e32 v231, v64, v65
	v_add_f32_e32 v231, v231, v66
	v_add_f32_e32 v231, v231, v67
	v_add_f32_e32 v231, v231, v68
	v_add_f32_e32 v231, v231, v69
	v_add_f32_e32 v231, v231, v70
	v_add_f32_e32 v231, v231, v71
	v_add_f32_e32 v231, v231, v72
	v_add_f32_e32 v231, v231, v73
	v_add_f32_e32 v231, v231, v74
	v_add_f32_e32 v231, v231, v75
	v_add_f32_e32 v231, v231, v76
	v_add_f32_e32 v231, v231, v77
	v_add_f32_e32 v231, v231, v78
	v_add_f32_e32 v231, v231, v79
	v_cvt_pk_f16_f32 v160, v64, v65
	v_cvt_pk_f16_f32 v161, v66, v67
	v_cvt_pk_f16_f32 v162, v68, v69
	v_cvt_pk_f16_f32 v163, v70, v71
	v_cvt_pk_f16_f32 v164, v72, v73
	v_cvt_pk_f16_f32 v165, v74, v75
	v_cvt_pk_f16_f32 v166, v76, v77
	v_cvt_pk_f16_f32 v167, v78, v79
	s_branch .Lovfret_a10p
.Lovf_a11p:
	s_waitcnt lgkmcnt(0)
	s_nop 15
	s_nop 15
	s_nop 15
	ds_read_b128 v[168:171], v225 offset:13824
	ds_read_b128 v[172:175], v225 offset:13856
	s_waitcnt lgkmcnt(0)
	v_mfma_f32_32x32x16_f16 v[64:79], v[168:171], v[128:131], v[96:111]
	v_mfma_f32_32x32x16_f16 v[64:79], v[172:175], v[132:135], v[64:79]
	s_nop 15
	ds_read_b128 v[168:171], v225 offset:13888
	ds_read_b128 v[172:175], v225 offset:13920
	s_waitcnt lgkmcnt(0)
	v_mfma_f32_32x32x16_f16 v[64:79], v[168:171], v[136:139], v[64:79]
	v_mfma_f32_32x32x16_f16 v[64:79], v[172:175], v[140:143], v[64:79]
	s_nop 15
	s_nop 15
	s_cmp_eq_u64 s[20:21], -1
	s_cbranch_scc1 .Lovfnm_a11p
	v_lshrrev_b32_e64 v235, v234, s21
	v_bfe_u32 v236, v235, 0, 1
	v_cvt_f32_u32_e32 v236, v236
	v_sub_f32_e32 v236, 1.0, v236
	v_fmac_f32_e32 v64, s35, v236
	v_bfe_u32 v236, v235, 1, 1
	v_cvt_f32_u32_e32 v236, v236
	v_sub_f32_e32 v236, 1.0, v236
	v_fmac_f32_e32 v65, s35, v236
	v_bfe_u32 v236, v235, 2, 1
	v_cvt_f32_u32_e32 v236, v236
	v_sub_f32_e32 v236, 1.0, v236
	v_fmac_f32_e32 v66, s35, v236
	v_bfe_u32 v236, v235, 3, 1
	v_cvt_f32_u32_e32 v236, v236
	v_sub_f32_e32 v236, 1.0, v236
	v_fmac_f32_e32 v67, s35, v236
	v_bfe_u32 v236, v235, 8, 1
	v_cvt_f32_u32_e32 v236, v236
	v_sub_f32_e32 v236, 1.0, v236
	v_fmac_f32_e32 v68, s35, v236
	v_bfe_u32 v236, v235, 9, 1
	v_cvt_f32_u32_e32 v236, v236
	v_sub_f32_e32 v236, 1.0, v236
	v_fmac_f32_e32 v69, s35, v236
	v_bfe_u32 v236, v235, 10, 1
	v_cvt_f32_u32_e32 v236, v236
	v_sub_f32_e32 v236, 1.0, v236
	v_fmac_f32_e32 v70, s35, v236
	v_bfe_u32 v236, v235, 11, 1
	v_cvt_f32_u32_e32 v236, v236
	v_sub_f32_e32 v236, 1.0, v236
	v_fmac_f32_e32 v71, s35, v236
	v_bfe_u32 v236, v235, 16, 1
	v_cvt_f32_u32_e32 v236, v236
	v_sub_f32_e32 v236, 1.0, v236
	v_fmac_f32_e32 v72, s35, v236
	v_bfe_u32 v236, v235, 17, 1
	v_cvt_f32_u32_e32 v236, v236
	v_sub_f32_e32 v236, 1.0, v236
	v_fmac_f32_e32 v73, s35, v236
	v_bfe_u32 v236, v235, 18, 1
	v_cvt_f32_u32_e32 v236, v236
	v_sub_f32_e32 v236, 1.0, v236
	v_fmac_f32_e32 v74, s35, v236
	v_bfe_u32 v236, v235, 19, 1
	v_cvt_f32_u32_e32 v236, v236
	v_sub_f32_e32 v236, 1.0, v236
	v_fmac_f32_e32 v75, s35, v236
	v_bfe_u32 v236, v235, 24, 1
	v_cvt_f32_u32_e32 v236, v236
	v_sub_f32_e32 v236, 1.0, v236
	v_fmac_f32_e32 v76, s35, v236
	v_bfe_u32 v236, v235, 25, 1
	v_cvt_f32_u32_e32 v236, v236
	v_sub_f32_e32 v236, 1.0, v236
	v_fmac_f32_e32 v77, s35, v236
	v_bfe_u32 v236, v235, 26, 1
	v_cvt_f32_u32_e32 v236, v236
	v_sub_f32_e32 v236, 1.0, v236
	v_fmac_f32_e32 v78, s35, v236
	v_bfe_u32 v236, v235, 27, 1
	v_cvt_f32_u32_e32 v236, v236
	v_sub_f32_e32 v236, 1.0, v236
	v_fmac_f32_e32 v79, s35, v236
.Lovfnm_a11p:
	v_max3_f32 v235, v64, v65, v66
	v_max3_f32 v235, v235, v67, v68
	v_max3_f32 v235, v235, v69, v70
	v_max3_f32 v235, v235, v71, v72
	v_max3_f32 v235, v235, v73, v74
	v_max3_f32 v235, v235, v75, v76
	v_max3_f32 v235, v235, v77, v78
	v_max_f32_e32 v235, v235, v79
	v_mov_b32_e32 v236, v235
	s_nop 1
	v_permlane32_swap_b32_e32 v235, v236
	v_max_f32_e32 v235, v235, v236
	v_max_f32_e32 v235, 0, v235
	v_exp_f32_e64 v237, -v235
	v_sub_f32_e32 v96, v96, v235
	v_sub_f32_e32 v97, v97, v235
	v_sub_f32_e32 v98, v98, v235
	v_sub_f32_e32 v99, v99, v235
	v_sub_f32_e32 v100, v100, v235
	v_sub_f32_e32 v101, v101, v235
	v_sub_f32_e32 v102, v102, v235
	v_sub_f32_e32 v103, v103, v235
	v_sub_f32_e32 v104, v104, v235
	v_sub_f32_e32 v105, v105, v235
	v_sub_f32_e32 v106, v106, v235
	v_sub_f32_e32 v107, v107, v235
	v_sub_f32_e32 v108, v108, v235
	v_sub_f32_e32 v109, v109, v235
	v_sub_f32_e32 v110, v110, v235
	v_sub_f32_e32 v111, v111, v235
	v_mul_f32_e32 v232, v232, v237
	v_mul_f32_e32 v0, v0, v237
	v_mul_f32_e32 v1, v1, v237
	v_mul_f32_e32 v2, v2, v237
	v_mul_f32_e32 v3, v3, v237
	v_mul_f32_e32 v4, v4, v237
	v_mul_f32_e32 v5, v5, v237
	v_mul_f32_e32 v6, v6, v237
	v_mul_f32_e32 v7, v7, v237
	v_mul_f32_e32 v8, v8, v237
	v_mul_f32_e32 v9, v9, v237
	v_mul_f32_e32 v10, v10, v237
	v_mul_f32_e32 v11, v11, v237
	v_mul_f32_e32 v12, v12, v237
	v_mul_f32_e32 v13, v13, v237
	v_mul_f32_e32 v14, v14, v237
	v_mul_f32_e32 v15, v15, v237
	v_mul_f32_e32 v16, v16, v237
	v_mul_f32_e32 v17, v17, v237
	v_mul_f32_e32 v18, v18, v237
	v_mul_f32_e32 v19, v19, v237
	v_mul_f32_e32 v20, v20, v237
	v_mul_f32_e32 v21, v21, v237
	v_mul_f32_e32 v22, v22, v237
	v_mul_f32_e32 v23, v23, v237
	v_mul_f32_e32 v24, v24, v237
	v_mul_f32_e32 v25, v25, v237
	v_mul_f32_e32 v26, v26, v237
	v_mul_f32_e32 v27, v27, v237
	v_mul_f32_e32 v28, v28, v237
	v_mul_f32_e32 v29, v29, v237
	v_mul_f32_e32 v30, v30, v237
	v_mul_f32_e32 v31, v31, v237
	v_sub_f32_e32 v64, v64, v235
	v_sub_f32_e32 v65, v65, v235
	v_sub_f32_e32 v66, v66, v235
	v_sub_f32_e32 v67, v67, v235
	v_sub_f32_e32 v68, v68, v235
	v_sub_f32_e32 v69, v69, v235
	v_sub_f32_e32 v70, v70, v235
	v_sub_f32_e32 v71, v71, v235
	v_sub_f32_e32 v72, v72, v235
	v_sub_f32_e32 v73, v73, v235
	v_sub_f32_e32 v74, v74, v235
	v_sub_f32_e32 v75, v75, v235
	v_sub_f32_e32 v76, v76, v235
	v_sub_f32_e32 v77, v77, v235
	v_sub_f32_e32 v78, v78, v235
	v_sub_f32_e32 v79, v79, v235
	v_exp_f32_e32 v64, v64
	v_exp_f32_e32 v65, v65
	v_exp_f32_e32 v66, v66
	v_exp_f32_e32 v67, v67
	v_exp_f32_e32 v68, v68
	v_exp_f32_e32 v69, v69
	v_exp_f32_e32 v70, v70
	v_exp_f32_e32 v71, v71
	v_exp_f32_e32 v72, v72
	v_exp_f32_e32 v73, v73
	v_exp_f32_e32 v74, v74
	v_exp_f32_e32 v75, v75
	v_exp_f32_e32 v76, v76
	v_exp_f32_e32 v77, v77
	v_exp_f32_e32 v78, v78
	v_exp_f32_e32 v79, v79
	s_nop 0
	v_add_f32_e32 v231, v64, v65
	v_add_f32_e32 v231, v231, v66
	v_add_f32_e32 v231, v231, v67
	v_add_f32_e32 v231, v231, v68
	v_add_f32_e32 v231, v231, v69
	v_add_f32_e32 v231, v231, v70
	v_add_f32_e32 v231, v231, v71
	v_add_f32_e32 v231, v231, v72
	v_add_f32_e32 v231, v231, v73
	v_add_f32_e32 v231, v231, v74
	v_add_f32_e32 v231, v231, v75
	v_add_f32_e32 v231, v231, v76
	v_add_f32_e32 v231, v231, v77
	v_add_f32_e32 v231, v231, v78
	v_add_f32_e32 v231, v231, v79
	v_cvt_pk_f16_f32 v160, v64, v65
	v_cvt_pk_f16_f32 v161, v66, v67
	v_cvt_pk_f16_f32 v162, v68, v69
	v_cvt_pk_f16_f32 v163, v70, v71
	v_cvt_pk_f16_f32 v164, v72, v73
	v_cvt_pk_f16_f32 v165, v74, v75
	v_cvt_pk_f16_f32 v166, v76, v77
	v_cvt_pk_f16_f32 v167, v78, v79
	s_branch .Lovfret_a11p
.Lovf_a20p:
	s_waitcnt lgkmcnt(0)
	s_nop 15
	s_nop 15
	s_nop 15
	ds_read_b128 v[168:171], v225 offset:18432
	ds_read_b128 v[172:175], v225 offset:18464
	s_waitcnt lgkmcnt(0)
	v_mfma_f32_32x32x16_f16 v[64:79], v[168:171], v[128:131], v[96:111]
	v_mfma_f32_32x32x16_f16 v[64:79], v[172:175], v[132:135], v[64:79]
	s_nop 15
	ds_read_b128 v[168:171], v225 offset:18496
	ds_read_b128 v[172:175], v225 offset:18528
	s_waitcnt lgkmcnt(0)
	v_mfma_f32_32x32x16_f16 v[64:79], v[168:171], v[136:139], v[64:79]
	v_mfma_f32_32x32x16_f16 v[64:79], v[172:175], v[140:143], v[64:79]
	s_nop 15
	s_nop 15
	s_cmp_eq_u64 s[20:21], -1
	s_cbranch_scc1 .Lovfnm_a20p
	v_lshrrev_b32_e64 v235, v234, s20
	v_bfe_u32 v236, v235, 0, 1
	v_cvt_f32_u32_e32 v236, v236
	v_sub_f32_e32 v236, 1.0, v236
	v_fmac_f32_e32 v64, s35, v236
	v_bfe_u32 v236, v235, 1, 1
	v_cvt_f32_u32_e32 v236, v236
	v_sub_f32_e32 v236, 1.0, v236
	v_fmac_f32_e32 v65, s35, v236
	v_bfe_u32 v236, v235, 2, 1
	v_cvt_f32_u32_e32 v236, v236
	v_sub_f32_e32 v236, 1.0, v236
	v_fmac_f32_e32 v66, s35, v236
	v_bfe_u32 v236, v235, 3, 1
	v_cvt_f32_u32_e32 v236, v236
	v_sub_f32_e32 v236, 1.0, v236
	v_fmac_f32_e32 v67, s35, v236
	v_bfe_u32 v236, v235, 8, 1
	v_cvt_f32_u32_e32 v236, v236
	v_sub_f32_e32 v236, 1.0, v236
	v_fmac_f32_e32 v68, s35, v236
	v_bfe_u32 v236, v235, 9, 1
	v_cvt_f32_u32_e32 v236, v236
	v_sub_f32_e32 v236, 1.0, v236
	v_fmac_f32_e32 v69, s35, v236
	v_bfe_u32 v236, v235, 10, 1
	v_cvt_f32_u32_e32 v236, v236
	v_sub_f32_e32 v236, 1.0, v236
	v_fmac_f32_e32 v70, s35, v236
	v_bfe_u32 v236, v235, 11, 1
	v_cvt_f32_u32_e32 v236, v236
	v_sub_f32_e32 v236, 1.0, v236
	v_fmac_f32_e32 v71, s35, v236
	v_bfe_u32 v236, v235, 16, 1
	v_cvt_f32_u32_e32 v236, v236
	v_sub_f32_e32 v236, 1.0, v236
	v_fmac_f32_e32 v72, s35, v236
	v_bfe_u32 v236, v235, 17, 1
	v_cvt_f32_u32_e32 v236, v236
	v_sub_f32_e32 v236, 1.0, v236
	v_fmac_f32_e32 v73, s35, v236
	v_bfe_u32 v236, v235, 18, 1
	v_cvt_f32_u32_e32 v236, v236
	v_sub_f32_e32 v236, 1.0, v236
	v_fmac_f32_e32 v74, s35, v236
	v_bfe_u32 v236, v235, 19, 1
	v_cvt_f32_u32_e32 v236, v236
	v_sub_f32_e32 v236, 1.0, v236
	v_fmac_f32_e32 v75, s35, v236
	v_bfe_u32 v236, v235, 24, 1
	v_cvt_f32_u32_e32 v236, v236
	v_sub_f32_e32 v236, 1.0, v236
	v_fmac_f32_e32 v76, s35, v236
	v_bfe_u32 v236, v235, 25, 1
	v_cvt_f32_u32_e32 v236, v236
	v_sub_f32_e32 v236, 1.0, v236
	v_fmac_f32_e32 v77, s35, v236
	v_bfe_u32 v236, v235, 26, 1
	v_cvt_f32_u32_e32 v236, v236
	v_sub_f32_e32 v236, 1.0, v236
	v_fmac_f32_e32 v78, s35, v236
	v_bfe_u32 v236, v235, 27, 1
	v_cvt_f32_u32_e32 v236, v236
	v_sub_f32_e32 v236, 1.0, v236
	v_fmac_f32_e32 v79, s35, v236
.Lovfnm_a20p:
	v_max3_f32 v235, v64, v65, v66
	v_max3_f32 v235, v235, v67, v68
	v_max3_f32 v235, v235, v69, v70
	v_max3_f32 v235, v235, v71, v72
	v_max3_f32 v235, v235, v73, v74
	v_max3_f32 v235, v235, v75, v76
	v_max3_f32 v235, v235, v77, v78
	v_max_f32_e32 v235, v235, v79
	v_mov_b32_e32 v236, v235
	s_nop 1
	v_permlane32_swap_b32_e32 v235, v236
	v_max_f32_e32 v235, v235, v236
	v_max_f32_e32 v235, 0, v235
	v_exp_f32_e64 v237, -v235
	v_sub_f32_e32 v96, v96, v235
	v_sub_f32_e32 v97, v97, v235
	v_sub_f32_e32 v98, v98, v235
	v_sub_f32_e32 v99, v99, v235
	v_sub_f32_e32 v100, v100, v235
	v_sub_f32_e32 v101, v101, v235
	v_sub_f32_e32 v102, v102, v235
	v_sub_f32_e32 v103, v103, v235
	v_sub_f32_e32 v104, v104, v235
	v_sub_f32_e32 v105, v105, v235
	v_sub_f32_e32 v106, v106, v235
	v_sub_f32_e32 v107, v107, v235
	v_sub_f32_e32 v108, v108, v235
	v_sub_f32_e32 v109, v109, v235
	v_sub_f32_e32 v110, v110, v235
	v_sub_f32_e32 v111, v111, v235
	v_mul_f32_e32 v232, v232, v237
	v_mul_f32_e32 v0, v0, v237
	v_mul_f32_e32 v1, v1, v237
	v_mul_f32_e32 v2, v2, v237
	v_mul_f32_e32 v3, v3, v237
	v_mul_f32_e32 v4, v4, v237
	v_mul_f32_e32 v5, v5, v237
	v_mul_f32_e32 v6, v6, v237
	v_mul_f32_e32 v7, v7, v237
	v_mul_f32_e32 v8, v8, v237
	v_mul_f32_e32 v9, v9, v237
	v_mul_f32_e32 v10, v10, v237
	v_mul_f32_e32 v11, v11, v237
	v_mul_f32_e32 v12, v12, v237
	v_mul_f32_e32 v13, v13, v237
	v_mul_f32_e32 v14, v14, v237
	v_mul_f32_e32 v15, v15, v237
	v_mul_f32_e32 v16, v16, v237
	v_mul_f32_e32 v17, v17, v237
	v_mul_f32_e32 v18, v18, v237
	v_mul_f32_e32 v19, v19, v237
	v_mul_f32_e32 v20, v20, v237
	v_mul_f32_e32 v21, v21, v237
	v_mul_f32_e32 v22, v22, v237
	v_mul_f32_e32 v23, v23, v237
	v_mul_f32_e32 v24, v24, v237
	v_mul_f32_e32 v25, v25, v237
	v_mul_f32_e32 v26, v26, v237
	v_mul_f32_e32 v27, v27, v237
	v_mul_f32_e32 v28, v28, v237
	v_mul_f32_e32 v29, v29, v237
	v_mul_f32_e32 v30, v30, v237
	v_mul_f32_e32 v31, v31, v237
	v_sub_f32_e32 v64, v64, v235
	v_sub_f32_e32 v65, v65, v235
	v_sub_f32_e32 v66, v66, v235
	v_sub_f32_e32 v67, v67, v235
	v_sub_f32_e32 v68, v68, v235
	v_sub_f32_e32 v69, v69, v235
	v_sub_f32_e32 v70, v70, v235
	v_sub_f32_e32 v71, v71, v235
	v_sub_f32_e32 v72, v72, v235
	v_sub_f32_e32 v73, v73, v235
	v_sub_f32_e32 v74, v74, v235
	v_sub_f32_e32 v75, v75, v235
	v_sub_f32_e32 v76, v76, v235
	v_sub_f32_e32 v77, v77, v235
	v_sub_f32_e32 v78, v78, v235
	v_sub_f32_e32 v79, v79, v235
	v_exp_f32_e32 v64, v64
	v_exp_f32_e32 v65, v65
	v_exp_f32_e32 v66, v66
	v_exp_f32_e32 v67, v67
	v_exp_f32_e32 v68, v68
	v_exp_f32_e32 v69, v69
	v_exp_f32_e32 v70, v70
	v_exp_f32_e32 v71, v71
	v_exp_f32_e32 v72, v72
	v_exp_f32_e32 v73, v73
	v_exp_f32_e32 v74, v74
	v_exp_f32_e32 v75, v75
	v_exp_f32_e32 v76, v76
	v_exp_f32_e32 v77, v77
	v_exp_f32_e32 v78, v78
	v_exp_f32_e32 v79, v79
	s_nop 0
	v_add_f32_e32 v231, v64, v65
	v_add_f32_e32 v231, v231, v66
	v_add_f32_e32 v231, v231, v67
	v_add_f32_e32 v231, v231, v68
	v_add_f32_e32 v231, v231, v69
	v_add_f32_e32 v231, v231, v70
	v_add_f32_e32 v231, v231, v71
	v_add_f32_e32 v231, v231, v72
	v_add_f32_e32 v231, v231, v73
	v_add_f32_e32 v231, v231, v74
	v_add_f32_e32 v231, v231, v75
	v_add_f32_e32 v231, v231, v76
	v_add_f32_e32 v231, v231, v77
	v_add_f32_e32 v231, v231, v78
	v_add_f32_e32 v231, v231, v79
	v_cvt_pk_f16_f32 v160, v64, v65
	v_cvt_pk_f16_f32 v161, v66, v67
	v_cvt_pk_f16_f32 v162, v68, v69
	v_cvt_pk_f16_f32 v163, v70, v71
	v_cvt_pk_f16_f32 v164, v72, v73
	v_cvt_pk_f16_f32 v165, v74, v75
	v_cvt_pk_f16_f32 v166, v76, v77
	v_cvt_pk_f16_f32 v167, v78, v79
	s_branch .Lovfret_a20p
.Lovf_a21p:
	s_waitcnt lgkmcnt(0)
	s_nop 15
	s_nop 15
	s_nop 15
	ds_read_b128 v[168:171], v225 offset:23040
	ds_read_b128 v[172:175], v225 offset:23072
	s_waitcnt lgkmcnt(0)
	v_mfma_f32_32x32x16_f16 v[64:79], v[168:171], v[128:131], v[96:111]
	v_mfma_f32_32x32x16_f16 v[64:79], v[172:175], v[132:135], v[64:79]
	s_nop 15
	ds_read_b128 v[168:171], v225 offset:23104
	ds_read_b128 v[172:175], v225 offset:23136
	s_waitcnt lgkmcnt(0)
	v_mfma_f32_32x32x16_f16 v[64:79], v[168:171], v[136:139], v[64:79]
	v_mfma_f32_32x32x16_f16 v[64:79], v[172:175], v[140:143], v[64:79]
	s_nop 15
	s_nop 15
	s_cmp_eq_u64 s[20:21], -1
	s_cbranch_scc1 .Lovfnm_a21p
	v_lshrrev_b32_e64 v235, v234, s21
	v_bfe_u32 v236, v235, 0, 1
	v_cvt_f32_u32_e32 v236, v236
	v_sub_f32_e32 v236, 1.0, v236
	v_fmac_f32_e32 v64, s35, v236
	v_bfe_u32 v236, v235, 1, 1
	v_cvt_f32_u32_e32 v236, v236
	v_sub_f32_e32 v236, 1.0, v236
	v_fmac_f32_e32 v65, s35, v236
	v_bfe_u32 v236, v235, 2, 1
	v_cvt_f32_u32_e32 v236, v236
	v_sub_f32_e32 v236, 1.0, v236
	v_fmac_f32_e32 v66, s35, v236
	v_bfe_u32 v236, v235, 3, 1
	v_cvt_f32_u32_e32 v236, v236
	v_sub_f32_e32 v236, 1.0, v236
	v_fmac_f32_e32 v67, s35, v236
	v_bfe_u32 v236, v235, 8, 1
	v_cvt_f32_u32_e32 v236, v236
	v_sub_f32_e32 v236, 1.0, v236
	v_fmac_f32_e32 v68, s35, v236
	v_bfe_u32 v236, v235, 9, 1
	v_cvt_f32_u32_e32 v236, v236
	v_sub_f32_e32 v236, 1.0, v236
	v_fmac_f32_e32 v69, s35, v236
	v_bfe_u32 v236, v235, 10, 1
	v_cvt_f32_u32_e32 v236, v236
	v_sub_f32_e32 v236, 1.0, v236
	v_fmac_f32_e32 v70, s35, v236
	v_bfe_u32 v236, v235, 11, 1
	v_cvt_f32_u32_e32 v236, v236
	v_sub_f32_e32 v236, 1.0, v236
	v_fmac_f32_e32 v71, s35, v236
	v_bfe_u32 v236, v235, 16, 1
	v_cvt_f32_u32_e32 v236, v236
	v_sub_f32_e32 v236, 1.0, v236
	v_fmac_f32_e32 v72, s35, v236
	v_bfe_u32 v236, v235, 17, 1
	v_cvt_f32_u32_e32 v236, v236
	v_sub_f32_e32 v236, 1.0, v236
	v_fmac_f32_e32 v73, s35, v236
	v_bfe_u32 v236, v235, 18, 1
	v_cvt_f32_u32_e32 v236, v236
	v_sub_f32_e32 v236, 1.0, v236
	v_fmac_f32_e32 v74, s35, v236
	v_bfe_u32 v236, v235, 19, 1
	v_cvt_f32_u32_e32 v236, v236
	v_sub_f32_e32 v236, 1.0, v236
	v_fmac_f32_e32 v75, s35, v236
	v_bfe_u32 v236, v235, 24, 1
	v_cvt_f32_u32_e32 v236, v236
	v_sub_f32_e32 v236, 1.0, v236
	v_fmac_f32_e32 v76, s35, v236
	v_bfe_u32 v236, v235, 25, 1
	v_cvt_f32_u32_e32 v236, v236
	v_sub_f32_e32 v236, 1.0, v236
	v_fmac_f32_e32 v77, s35, v236
	v_bfe_u32 v236, v235, 26, 1
	v_cvt_f32_u32_e32 v236, v236
	v_sub_f32_e32 v236, 1.0, v236
	v_fmac_f32_e32 v78, s35, v236
	v_bfe_u32 v236, v235, 27, 1
	v_cvt_f32_u32_e32 v236, v236
	v_sub_f32_e32 v236, 1.0, v236
	v_fmac_f32_e32 v79, s35, v236
.Lovfnm_a21p:
	v_max3_f32 v235, v64, v65, v66
	v_max3_f32 v235, v235, v67, v68
	v_max3_f32 v235, v235, v69, v70
	v_max3_f32 v235, v235, v71, v72
	v_max3_f32 v235, v235, v73, v74
	v_max3_f32 v235, v235, v75, v76
	v_max3_f32 v235, v235, v77, v78
	v_max_f32_e32 v235, v235, v79
	v_mov_b32_e32 v236, v235
	s_nop 1
	v_permlane32_swap_b32_e32 v235, v236
	v_max_f32_e32 v235, v235, v236
	v_max_f32_e32 v235, 0, v235
	v_exp_f32_e64 v237, -v235
	v_sub_f32_e32 v96, v96, v235
	v_sub_f32_e32 v97, v97, v235
	v_sub_f32_e32 v98, v98, v235
	v_sub_f32_e32 v99, v99, v235
	v_sub_f32_e32 v100, v100, v235
	v_sub_f32_e32 v101, v101, v235
	v_sub_f32_e32 v102, v102, v235
	v_sub_f32_e32 v103, v103, v235
	v_sub_f32_e32 v104, v104, v235
	v_sub_f32_e32 v105, v105, v235
	v_sub_f32_e32 v106, v106, v235
	v_sub_f32_e32 v107, v107, v235
	v_sub_f32_e32 v108, v108, v235
	v_sub_f32_e32 v109, v109, v235
	v_sub_f32_e32 v110, v110, v235
	v_sub_f32_e32 v111, v111, v235
	v_mul_f32_e32 v232, v232, v237
	v_mul_f32_e32 v0, v0, v237
	v_mul_f32_e32 v1, v1, v237
	v_mul_f32_e32 v2, v2, v237
	v_mul_f32_e32 v3, v3, v237
	v_mul_f32_e32 v4, v4, v237
	v_mul_f32_e32 v5, v5, v237
	v_mul_f32_e32 v6, v6, v237
	v_mul_f32_e32 v7, v7, v237
	v_mul_f32_e32 v8, v8, v237
	v_mul_f32_e32 v9, v9, v237
	v_mul_f32_e32 v10, v10, v237
	v_mul_f32_e32 v11, v11, v237
	v_mul_f32_e32 v12, v12, v237
	v_mul_f32_e32 v13, v13, v237
	v_mul_f32_e32 v14, v14, v237
	v_mul_f32_e32 v15, v15, v237
	v_mul_f32_e32 v16, v16, v237
	v_mul_f32_e32 v17, v17, v237
	v_mul_f32_e32 v18, v18, v237
	v_mul_f32_e32 v19, v19, v237
	v_mul_f32_e32 v20, v20, v237
	v_mul_f32_e32 v21, v21, v237
	v_mul_f32_e32 v22, v22, v237
	v_mul_f32_e32 v23, v23, v237
	v_mul_f32_e32 v24, v24, v237
	v_mul_f32_e32 v25, v25, v237
	v_mul_f32_e32 v26, v26, v237
	v_mul_f32_e32 v27, v27, v237
	v_mul_f32_e32 v28, v28, v237
	v_mul_f32_e32 v29, v29, v237
	v_mul_f32_e32 v30, v30, v237
	v_mul_f32_e32 v31, v31, v237
	v_sub_f32_e32 v64, v64, v235
	v_sub_f32_e32 v65, v65, v235
	v_sub_f32_e32 v66, v66, v235
	v_sub_f32_e32 v67, v67, v235
	v_sub_f32_e32 v68, v68, v235
	v_sub_f32_e32 v69, v69, v235
	v_sub_f32_e32 v70, v70, v235
	v_sub_f32_e32 v71, v71, v235
	v_sub_f32_e32 v72, v72, v235
	v_sub_f32_e32 v73, v73, v235
	v_sub_f32_e32 v74, v74, v235
	v_sub_f32_e32 v75, v75, v235
	v_sub_f32_e32 v76, v76, v235
	v_sub_f32_e32 v77, v77, v235
	v_sub_f32_e32 v78, v78, v235
	v_sub_f32_e32 v79, v79, v235
	v_exp_f32_e32 v64, v64
	v_exp_f32_e32 v65, v65
	v_exp_f32_e32 v66, v66
	v_exp_f32_e32 v67, v67
	v_exp_f32_e32 v68, v68
	v_exp_f32_e32 v69, v69
	v_exp_f32_e32 v70, v70
	v_exp_f32_e32 v71, v71
	v_exp_f32_e32 v72, v72
	v_exp_f32_e32 v73, v73
	v_exp_f32_e32 v74, v74
	v_exp_f32_e32 v75, v75
	v_exp_f32_e32 v76, v76
	v_exp_f32_e32 v77, v77
	v_exp_f32_e32 v78, v78
	v_exp_f32_e32 v79, v79
	s_nop 0
	v_add_f32_e32 v231, v64, v65
	v_add_f32_e32 v231, v231, v66
	v_add_f32_e32 v231, v231, v67
	v_add_f32_e32 v231, v231, v68
	v_add_f32_e32 v231, v231, v69
	v_add_f32_e32 v231, v231, v70
	v_add_f32_e32 v231, v231, v71
	v_add_f32_e32 v231, v231, v72
	v_add_f32_e32 v231, v231, v73
	v_add_f32_e32 v231, v231, v74
	v_add_f32_e32 v231, v231, v75
	v_add_f32_e32 v231, v231, v76
	v_add_f32_e32 v231, v231, v77
	v_add_f32_e32 v231, v231, v78
	v_add_f32_e32 v231, v231, v79
	v_cvt_pk_f16_f32 v160, v64, v65
	v_cvt_pk_f16_f32 v161, v66, v67
	v_cvt_pk_f16_f32 v162, v68, v69
	v_cvt_pk_f16_f32 v163, v70, v71
	v_cvt_pk_f16_f32 v164, v72, v73
	v_cvt_pk_f16_f32 v165, v74, v75
	v_cvt_pk_f16_f32 v166, v76, v77
	v_cvt_pk_f16_f32 v167, v78, v79
	s_branch .Lovfret_a21p
.Lovf_a30p:
	s_waitcnt lgkmcnt(0)
	s_nop 15
	s_nop 15
	s_nop 15
	ds_read_b128 v[168:171], v225 offset:27648
	ds_read_b128 v[172:175], v225 offset:27680
	s_waitcnt lgkmcnt(0)
	v_mfma_f32_32x32x16_f16 v[64:79], v[168:171], v[128:131], v[96:111]
	v_mfma_f32_32x32x16_f16 v[64:79], v[172:175], v[132:135], v[64:79]
	s_nop 15
	ds_read_b128 v[168:171], v225 offset:27712
	ds_read_b128 v[172:175], v225 offset:27744
	s_waitcnt lgkmcnt(0)
	v_mfma_f32_32x32x16_f16 v[64:79], v[168:171], v[136:139], v[64:79]
	v_mfma_f32_32x32x16_f16 v[64:79], v[172:175], v[140:143], v[64:79]
	s_nop 15
	s_nop 15
	s_cmp_eq_u64 s[20:21], -1
	s_cbranch_scc1 .Lovfnm_a30p
	v_lshrrev_b32_e64 v235, v234, s20
	v_bfe_u32 v236, v235, 0, 1
	v_cvt_f32_u32_e32 v236, v236
	v_sub_f32_e32 v236, 1.0, v236
	v_fmac_f32_e32 v64, s35, v236
	v_bfe_u32 v236, v235, 1, 1
	v_cvt_f32_u32_e32 v236, v236
	v_sub_f32_e32 v236, 1.0, v236
	v_fmac_f32_e32 v65, s35, v236
	v_bfe_u32 v236, v235, 2, 1
	v_cvt_f32_u32_e32 v236, v236
	v_sub_f32_e32 v236, 1.0, v236
	v_fmac_f32_e32 v66, s35, v236
	v_bfe_u32 v236, v235, 3, 1
	v_cvt_f32_u32_e32 v236, v236
	v_sub_f32_e32 v236, 1.0, v236
	v_fmac_f32_e32 v67, s35, v236
	v_bfe_u32 v236, v235, 8, 1
	v_cvt_f32_u32_e32 v236, v236
	v_sub_f32_e32 v236, 1.0, v236
	v_fmac_f32_e32 v68, s35, v236
	v_bfe_u32 v236, v235, 9, 1
	v_cvt_f32_u32_e32 v236, v236
	v_sub_f32_e32 v236, 1.0, v236
	v_fmac_f32_e32 v69, s35, v236
	v_bfe_u32 v236, v235, 10, 1
	v_cvt_f32_u32_e32 v236, v236
	v_sub_f32_e32 v236, 1.0, v236
	v_fmac_f32_e32 v70, s35, v236
	v_bfe_u32 v236, v235, 11, 1
	v_cvt_f32_u32_e32 v236, v236
	v_sub_f32_e32 v236, 1.0, v236
	v_fmac_f32_e32 v71, s35, v236
	v_bfe_u32 v236, v235, 16, 1
	v_cvt_f32_u32_e32 v236, v236
	v_sub_f32_e32 v236, 1.0, v236
	v_fmac_f32_e32 v72, s35, v236
	v_bfe_u32 v236, v235, 17, 1
	v_cvt_f32_u32_e32 v236, v236
	v_sub_f32_e32 v236, 1.0, v236
	v_fmac_f32_e32 v73, s35, v236
	v_bfe_u32 v236, v235, 18, 1
	v_cvt_f32_u32_e32 v236, v236
	v_sub_f32_e32 v236, 1.0, v236
	v_fmac_f32_e32 v74, s35, v236
	v_bfe_u32 v236, v235, 19, 1
	v_cvt_f32_u32_e32 v236, v236
	v_sub_f32_e32 v236, 1.0, v236
	v_fmac_f32_e32 v75, s35, v236
	v_bfe_u32 v236, v235, 24, 1
	v_cvt_f32_u32_e32 v236, v236
	v_sub_f32_e32 v236, 1.0, v236
	v_fmac_f32_e32 v76, s35, v236
	v_bfe_u32 v236, v235, 25, 1
	v_cvt_f32_u32_e32 v236, v236
	v_sub_f32_e32 v236, 1.0, v236
	v_fmac_f32_e32 v77, s35, v236
	v_bfe_u32 v236, v235, 26, 1
	v_cvt_f32_u32_e32 v236, v236
	v_sub_f32_e32 v236, 1.0, v236
	v_fmac_f32_e32 v78, s35, v236
	v_bfe_u32 v236, v235, 27, 1
	v_cvt_f32_u32_e32 v236, v236
	v_sub_f32_e32 v236, 1.0, v236
	v_fmac_f32_e32 v79, s35, v236
.Lovfnm_a30p:
	v_max3_f32 v235, v64, v65, v66
	v_max3_f32 v235, v235, v67, v68
	v_max3_f32 v235, v235, v69, v70
	v_max3_f32 v235, v235, v71, v72
	v_max3_f32 v235, v235, v73, v74
	v_max3_f32 v235, v235, v75, v76
	v_max3_f32 v235, v235, v77, v78
	v_max_f32_e32 v235, v235, v79
	v_mov_b32_e32 v236, v235
	s_nop 1
	v_permlane32_swap_b32_e32 v235, v236
	v_max_f32_e32 v235, v235, v236
	v_max_f32_e32 v235, 0, v235
	v_exp_f32_e64 v237, -v235
	v_sub_f32_e32 v96, v96, v235
	v_sub_f32_e32 v97, v97, v235
	v_sub_f32_e32 v98, v98, v235
	v_sub_f32_e32 v99, v99, v235
	v_sub_f32_e32 v100, v100, v235
	v_sub_f32_e32 v101, v101, v235
	v_sub_f32_e32 v102, v102, v235
	v_sub_f32_e32 v103, v103, v235
	v_sub_f32_e32 v104, v104, v235
	v_sub_f32_e32 v105, v105, v235
	v_sub_f32_e32 v106, v106, v235
	v_sub_f32_e32 v107, v107, v235
	v_sub_f32_e32 v108, v108, v235
	v_sub_f32_e32 v109, v109, v235
	v_sub_f32_e32 v110, v110, v235
	v_sub_f32_e32 v111, v111, v235
	v_mul_f32_e32 v232, v232, v237
	v_mul_f32_e32 v0, v0, v237
	v_mul_f32_e32 v1, v1, v237
	v_mul_f32_e32 v2, v2, v237
	v_mul_f32_e32 v3, v3, v237
	v_mul_f32_e32 v4, v4, v237
	v_mul_f32_e32 v5, v5, v237
	v_mul_f32_e32 v6, v6, v237
	v_mul_f32_e32 v7, v7, v237
	v_mul_f32_e32 v8, v8, v237
	v_mul_f32_e32 v9, v9, v237
	v_mul_f32_e32 v10, v10, v237
	v_mul_f32_e32 v11, v11, v237
	v_mul_f32_e32 v12, v12, v237
	v_mul_f32_e32 v13, v13, v237
	v_mul_f32_e32 v14, v14, v237
	v_mul_f32_e32 v15, v15, v237
	v_mul_f32_e32 v16, v16, v237
	v_mul_f32_e32 v17, v17, v237
	v_mul_f32_e32 v18, v18, v237
	v_mul_f32_e32 v19, v19, v237
	v_mul_f32_e32 v20, v20, v237
	v_mul_f32_e32 v21, v21, v237
	v_mul_f32_e32 v22, v22, v237
	v_mul_f32_e32 v23, v23, v237
	v_mul_f32_e32 v24, v24, v237
	v_mul_f32_e32 v25, v25, v237
	v_mul_f32_e32 v26, v26, v237
	v_mul_f32_e32 v27, v27, v237
	v_mul_f32_e32 v28, v28, v237
	v_mul_f32_e32 v29, v29, v237
	v_mul_f32_e32 v30, v30, v237
	v_mul_f32_e32 v31, v31, v237
	v_sub_f32_e32 v64, v64, v235
	v_sub_f32_e32 v65, v65, v235
	v_sub_f32_e32 v66, v66, v235
	v_sub_f32_e32 v67, v67, v235
	v_sub_f32_e32 v68, v68, v235
	v_sub_f32_e32 v69, v69, v235
	v_sub_f32_e32 v70, v70, v235
	v_sub_f32_e32 v71, v71, v235
	v_sub_f32_e32 v72, v72, v235
	v_sub_f32_e32 v73, v73, v235
	v_sub_f32_e32 v74, v74, v235
	v_sub_f32_e32 v75, v75, v235
	v_sub_f32_e32 v76, v76, v235
	v_sub_f32_e32 v77, v77, v235
	v_sub_f32_e32 v78, v78, v235
	v_sub_f32_e32 v79, v79, v235
	v_exp_f32_e32 v64, v64
	v_exp_f32_e32 v65, v65
	v_exp_f32_e32 v66, v66
	v_exp_f32_e32 v67, v67
	v_exp_f32_e32 v68, v68
	v_exp_f32_e32 v69, v69
	v_exp_f32_e32 v70, v70
	v_exp_f32_e32 v71, v71
	v_exp_f32_e32 v72, v72
	v_exp_f32_e32 v73, v73
	v_exp_f32_e32 v74, v74
	v_exp_f32_e32 v75, v75
	v_exp_f32_e32 v76, v76
	v_exp_f32_e32 v77, v77
	v_exp_f32_e32 v78, v78
	v_exp_f32_e32 v79, v79
	s_nop 0
	v_add_f32_e32 v231, v64, v65
	v_add_f32_e32 v231, v231, v66
	v_add_f32_e32 v231, v231, v67
	v_add_f32_e32 v231, v231, v68
	v_add_f32_e32 v231, v231, v69
	v_add_f32_e32 v231, v231, v70
	v_add_f32_e32 v231, v231, v71
	v_add_f32_e32 v231, v231, v72
	v_add_f32_e32 v231, v231, v73
	v_add_f32_e32 v231, v231, v74
	v_add_f32_e32 v231, v231, v75
	v_add_f32_e32 v231, v231, v76
	v_add_f32_e32 v231, v231, v77
	v_add_f32_e32 v231, v231, v78
	v_add_f32_e32 v231, v231, v79
	v_cvt_pk_f16_f32 v160, v64, v65
	v_cvt_pk_f16_f32 v161, v66, v67
	v_cvt_pk_f16_f32 v162, v68, v69
	v_cvt_pk_f16_f32 v163, v70, v71
	v_cvt_pk_f16_f32 v164, v72, v73
	v_cvt_pk_f16_f32 v165, v74, v75
	v_cvt_pk_f16_f32 v166, v76, v77
	v_cvt_pk_f16_f32 v167, v78, v79
	s_branch .Lovfret_a30p
.Lovf_a31p:
	s_waitcnt lgkmcnt(0)
	s_nop 15
	s_nop 15
	s_nop 15
	ds_read_b128 v[168:171], v225 offset:32256
	ds_read_b128 v[172:175], v225 offset:32288
	s_waitcnt lgkmcnt(0)
	v_mfma_f32_32x32x16_f16 v[64:79], v[168:171], v[128:131], v[96:111]
	v_mfma_f32_32x32x16_f16 v[64:79], v[172:175], v[132:135], v[64:79]
	s_nop 15
	ds_read_b128 v[168:171], v225 offset:32320
	ds_read_b128 v[172:175], v225 offset:32352
	s_waitcnt lgkmcnt(0)
	v_mfma_f32_32x32x16_f16 v[64:79], v[168:171], v[136:139], v[64:79]
	v_mfma_f32_32x32x16_f16 v[64:79], v[172:175], v[140:143], v[64:79]
	s_nop 15
	s_nop 15
	s_cmp_eq_u64 s[20:21], -1
	s_cbranch_scc1 .Lovfnm_a31p
	v_lshrrev_b32_e64 v235, v234, s21
	v_bfe_u32 v236, v235, 0, 1
	v_cvt_f32_u32_e32 v236, v236
	v_sub_f32_e32 v236, 1.0, v236
	v_fmac_f32_e32 v64, s35, v236
	v_bfe_u32 v236, v235, 1, 1
	v_cvt_f32_u32_e32 v236, v236
	v_sub_f32_e32 v236, 1.0, v236
	v_fmac_f32_e32 v65, s35, v236
	v_bfe_u32 v236, v235, 2, 1
	v_cvt_f32_u32_e32 v236, v236
	v_sub_f32_e32 v236, 1.0, v236
	v_fmac_f32_e32 v66, s35, v236
	v_bfe_u32 v236, v235, 3, 1
	v_cvt_f32_u32_e32 v236, v236
	v_sub_f32_e32 v236, 1.0, v236
	v_fmac_f32_e32 v67, s35, v236
	v_bfe_u32 v236, v235, 8, 1
	v_cvt_f32_u32_e32 v236, v236
	v_sub_f32_e32 v236, 1.0, v236
	v_fmac_f32_e32 v68, s35, v236
	v_bfe_u32 v236, v235, 9, 1
	v_cvt_f32_u32_e32 v236, v236
	v_sub_f32_e32 v236, 1.0, v236
	v_fmac_f32_e32 v69, s35, v236
	v_bfe_u32 v236, v235, 10, 1
	v_cvt_f32_u32_e32 v236, v236
	v_sub_f32_e32 v236, 1.0, v236
	v_fmac_f32_e32 v70, s35, v236
	v_bfe_u32 v236, v235, 11, 1
	v_cvt_f32_u32_e32 v236, v236
	v_sub_f32_e32 v236, 1.0, v236
	v_fmac_f32_e32 v71, s35, v236
	v_bfe_u32 v236, v235, 16, 1
	v_cvt_f32_u32_e32 v236, v236
	v_sub_f32_e32 v236, 1.0, v236
	v_fmac_f32_e32 v72, s35, v236
	v_bfe_u32 v236, v235, 17, 1
	v_cvt_f32_u32_e32 v236, v236
	v_sub_f32_e32 v236, 1.0, v236
	v_fmac_f32_e32 v73, s35, v236
	v_bfe_u32 v236, v235, 18, 1
	v_cvt_f32_u32_e32 v236, v236
	v_sub_f32_e32 v236, 1.0, v236
	v_fmac_f32_e32 v74, s35, v236
	v_bfe_u32 v236, v235, 19, 1
	v_cvt_f32_u32_e32 v236, v236
	v_sub_f32_e32 v236, 1.0, v236
	v_fmac_f32_e32 v75, s35, v236
	v_bfe_u32 v236, v235, 24, 1
	v_cvt_f32_u32_e32 v236, v236
	v_sub_f32_e32 v236, 1.0, v236
	v_fmac_f32_e32 v76, s35, v236
	v_bfe_u32 v236, v235, 25, 1
	v_cvt_f32_u32_e32 v236, v236
	v_sub_f32_e32 v236, 1.0, v236
	v_fmac_f32_e32 v77, s35, v236
	v_bfe_u32 v236, v235, 26, 1
	v_cvt_f32_u32_e32 v236, v236
	v_sub_f32_e32 v236, 1.0, v236
	v_fmac_f32_e32 v78, s35, v236
	v_bfe_u32 v236, v235, 27, 1
	v_cvt_f32_u32_e32 v236, v236
	v_sub_f32_e32 v236, 1.0, v236
	v_fmac_f32_e32 v79, s35, v236
.Lovfnm_a31p:
	v_max3_f32 v235, v64, v65, v66
	v_max3_f32 v235, v235, v67, v68
	v_max3_f32 v235, v235, v69, v70
	v_max3_f32 v235, v235, v71, v72
	v_max3_f32 v235, v235, v73, v74
	v_max3_f32 v235, v235, v75, v76
	v_max3_f32 v235, v235, v77, v78
	v_max_f32_e32 v235, v235, v79
	v_mov_b32_e32 v236, v235
	s_nop 1
	v_permlane32_swap_b32_e32 v235, v236
	v_max_f32_e32 v235, v235, v236
	v_max_f32_e32 v235, 0, v235
	v_exp_f32_e64 v237, -v235
	v_sub_f32_e32 v96, v96, v235
	v_sub_f32_e32 v97, v97, v235
	v_sub_f32_e32 v98, v98, v235
	v_sub_f32_e32 v99, v99, v235
	v_sub_f32_e32 v100, v100, v235
	v_sub_f32_e32 v101, v101, v235
	v_sub_f32_e32 v102, v102, v235
	v_sub_f32_e32 v103, v103, v235
	v_sub_f32_e32 v104, v104, v235
	v_sub_f32_e32 v105, v105, v235
	v_sub_f32_e32 v106, v106, v235
	v_sub_f32_e32 v107, v107, v235
	v_sub_f32_e32 v108, v108, v235
	v_sub_f32_e32 v109, v109, v235
	v_sub_f32_e32 v110, v110, v235
	v_sub_f32_e32 v111, v111, v235
	v_mul_f32_e32 v232, v232, v237
	v_mul_f32_e32 v0, v0, v237
	v_mul_f32_e32 v1, v1, v237
	v_mul_f32_e32 v2, v2, v237
	v_mul_f32_e32 v3, v3, v237
	v_mul_f32_e32 v4, v4, v237
	v_mul_f32_e32 v5, v5, v237
	v_mul_f32_e32 v6, v6, v237
	v_mul_f32_e32 v7, v7, v237
	v_mul_f32_e32 v8, v8, v237
	v_mul_f32_e32 v9, v9, v237
	v_mul_f32_e32 v10, v10, v237
	v_mul_f32_e32 v11, v11, v237
	v_mul_f32_e32 v12, v12, v237
	v_mul_f32_e32 v13, v13, v237
	v_mul_f32_e32 v14, v14, v237
	v_mul_f32_e32 v15, v15, v237
	v_mul_f32_e32 v16, v16, v237
	v_mul_f32_e32 v17, v17, v237
	v_mul_f32_e32 v18, v18, v237
	v_mul_f32_e32 v19, v19, v237
	v_mul_f32_e32 v20, v20, v237
	v_mul_f32_e32 v21, v21, v237
	v_mul_f32_e32 v22, v22, v237
	v_mul_f32_e32 v23, v23, v237
	v_mul_f32_e32 v24, v24, v237
	v_mul_f32_e32 v25, v25, v237
	v_mul_f32_e32 v26, v26, v237
	v_mul_f32_e32 v27, v27, v237
	v_mul_f32_e32 v28, v28, v237
	v_mul_f32_e32 v29, v29, v237
	v_mul_f32_e32 v30, v30, v237
	v_mul_f32_e32 v31, v31, v237
	v_sub_f32_e32 v64, v64, v235
	v_sub_f32_e32 v65, v65, v235
	v_sub_f32_e32 v66, v66, v235
	v_sub_f32_e32 v67, v67, v235
	v_sub_f32_e32 v68, v68, v235
	v_sub_f32_e32 v69, v69, v235
	v_sub_f32_e32 v70, v70, v235
	v_sub_f32_e32 v71, v71, v235
	v_sub_f32_e32 v72, v72, v235
	v_sub_f32_e32 v73, v73, v235
	v_sub_f32_e32 v74, v74, v235
	v_sub_f32_e32 v75, v75, v235
	v_sub_f32_e32 v76, v76, v235
	v_sub_f32_e32 v77, v77, v235
	v_sub_f32_e32 v78, v78, v235
	v_sub_f32_e32 v79, v79, v235
	v_exp_f32_e32 v64, v64
	v_exp_f32_e32 v65, v65
	v_exp_f32_e32 v66, v66
	v_exp_f32_e32 v67, v67
	v_exp_f32_e32 v68, v68
	v_exp_f32_e32 v69, v69
	v_exp_f32_e32 v70, v70
	v_exp_f32_e32 v71, v71
	v_exp_f32_e32 v72, v72
	v_exp_f32_e32 v73, v73
	v_exp_f32_e32 v74, v74
	v_exp_f32_e32 v75, v75
	v_exp_f32_e32 v76, v76
	v_exp_f32_e32 v77, v77
	v_exp_f32_e32 v78, v78
	v_exp_f32_e32 v79, v79
	s_nop 0
	v_add_f32_e32 v231, v64, v65
	v_add_f32_e32 v231, v231, v66
	v_add_f32_e32 v231, v231, v67
	v_add_f32_e32 v231, v231, v68
	v_add_f32_e32 v231, v231, v69
	v_add_f32_e32 v231, v231, v70
	v_add_f32_e32 v231, v231, v71
	v_add_f32_e32 v231, v231, v72
	v_add_f32_e32 v231, v231, v73
	v_add_f32_e32 v231, v231, v74
	v_add_f32_e32 v231, v231, v75
	v_add_f32_e32 v231, v231, v76
	v_add_f32_e32 v231, v231, v77
	v_add_f32_e32 v231, v231, v78
	v_add_f32_e32 v231, v231, v79
	v_cvt_pk_f16_f32 v160, v64, v65
	v_cvt_pk_f16_f32 v161, v66, v67
	v_cvt_pk_f16_f32 v162, v68, v69
	v_cvt_pk_f16_f32 v163, v70, v71
	v_cvt_pk_f16_f32 v164, v72, v73
	v_cvt_pk_f16_f32 v165, v74, v75
	v_cvt_pk_f16_f32 v166, v76, v77
	v_cvt_pk_f16_f32 v167, v78, v79
	s_branch .Lovfret_a31p
.Lovf_a00:
	s_waitcnt lgkmcnt(0)
	s_nop 15
	s_nop 15
	s_nop 15
	ds_read_b128 v[168:171], v225 offset:0
	ds_read_b128 v[172:175], v225 offset:32
	s_waitcnt lgkmcnt(0)
	v_mfma_f32_32x32x16_f16 v[64:79], v[168:171], v[128:131], v[96:111]
	v_mfma_f32_32x32x16_f16 v[64:79], v[172:175], v[132:135], v[64:79]
	s_nop 15
	ds_read_b128 v[168:171], v225 offset:64
	ds_read_b128 v[172:175], v225 offset:96
	s_waitcnt lgkmcnt(0)
	v_mfma_f32_32x32x16_f16 v[64:79], v[168:171], v[136:139], v[64:79]
	v_mfma_f32_32x32x16_f16 v[64:79], v[172:175], v[140:143], v[64:79]
	s_nop 15
	s_nop 15
	s_cmp_eq_u64 s[20:21], -1
	s_cbranch_scc1 .Lovfnm_a00
	v_lshrrev_b32_e64 v235, v234, s20
	v_bfe_u32 v236, v235, 0, 1
	v_cvt_f32_u32_e32 v236, v236
	v_sub_f32_e32 v236, 1.0, v236
	v_fmac_f32_e32 v64, s35, v236
	v_bfe_u32 v236, v235, 1, 1
	v_cvt_f32_u32_e32 v236, v236
	v_sub_f32_e32 v236, 1.0, v236
	v_fmac_f32_e32 v65, s35, v236
	v_bfe_u32 v236, v235, 2, 1
	v_cvt_f32_u32_e32 v236, v236
	v_sub_f32_e32 v236, 1.0, v236
	v_fmac_f32_e32 v66, s35, v236
	v_bfe_u32 v236, v235, 3, 1
	v_cvt_f32_u32_e32 v236, v236
	v_sub_f32_e32 v236, 1.0, v236
	v_fmac_f32_e32 v67, s35, v236
	v_bfe_u32 v236, v235, 8, 1
	v_cvt_f32_u32_e32 v236, v236
	v_sub_f32_e32 v236, 1.0, v236
	v_fmac_f32_e32 v68, s35, v236
	v_bfe_u32 v236, v235, 9, 1
	v_cvt_f32_u32_e32 v236, v236
	v_sub_f32_e32 v236, 1.0, v236
	v_fmac_f32_e32 v69, s35, v236
	v_bfe_u32 v236, v235, 10, 1
	v_cvt_f32_u32_e32 v236, v236
	v_sub_f32_e32 v236, 1.0, v236
	v_fmac_f32_e32 v70, s35, v236
	v_bfe_u32 v236, v235, 11, 1
	v_cvt_f32_u32_e32 v236, v236
	v_sub_f32_e32 v236, 1.0, v236
	v_fmac_f32_e32 v71, s35, v236
	v_bfe_u32 v236, v235, 16, 1
	v_cvt_f32_u32_e32 v236, v236
	v_sub_f32_e32 v236, 1.0, v236
	v_fmac_f32_e32 v72, s35, v236
	v_bfe_u32 v236, v235, 17, 1
	v_cvt_f32_u32_e32 v236, v236
	v_sub_f32_e32 v236, 1.0, v236
	v_fmac_f32_e32 v73, s35, v236
	v_bfe_u32 v236, v235, 18, 1
	v_cvt_f32_u32_e32 v236, v236
	v_sub_f32_e32 v236, 1.0, v236
	v_fmac_f32_e32 v74, s35, v236
	v_bfe_u32 v236, v235, 19, 1
	v_cvt_f32_u32_e32 v236, v236
	v_sub_f32_e32 v236, 1.0, v236
	v_fmac_f32_e32 v75, s35, v236
	v_bfe_u32 v236, v235, 24, 1
	v_cvt_f32_u32_e32 v236, v236
	v_sub_f32_e32 v236, 1.0, v236
	v_fmac_f32_e32 v76, s35, v236
	v_bfe_u32 v236, v235, 25, 1
	v_cvt_f32_u32_e32 v236, v236
	v_sub_f32_e32 v236, 1.0, v236
	v_fmac_f32_e32 v77, s35, v236
	v_bfe_u32 v236, v235, 26, 1
	v_cvt_f32_u32_e32 v236, v236
	v_sub_f32_e32 v236, 1.0, v236
	v_fmac_f32_e32 v78, s35, v236
	v_bfe_u32 v236, v235, 27, 1
	v_cvt_f32_u32_e32 v236, v236
	v_sub_f32_e32 v236, 1.0, v236
	v_fmac_f32_e32 v79, s35, v236

.Lovfnm_b31:
	v_max3_f32 v235, v80, v81, v82
	v_max3_f32 v235, v235, v83, v84
	v_max3_f32 v235, v235, v85, v86
	v_max3_f32 v235, v235, v87, v88
	v_max3_f32 v235, v235, v89, v90
	v_max3_f32 v235, v235, v91, v92
	v_max3_f32 v235, v235, v93, v94
	v_max_f32_e32 v235, v235, v95
	v_mov_b32_e32 v236, v235
	s_nop 1
	v_permlane32_swap_b32_e32 v235, v236
	v_max_f32_e32 v235, v235, v236
	v_max_f32_e32 v235, 0, v235
	v_exp_f32_e64 v237, -v235
	v_sub_f32_e32 v112, v112, v235
	v_sub_f32_e32 v113, v113, v235
	v_sub_f32_e32 v114, v114, v235
	v_sub_f32_e32 v115, v115, v235
	v_sub_f32_e32 v116, v116, v235
	v_sub_f32_e32 v117, v117, v235
	v_sub_f32_e32 v118, v118, v235
	v_sub_f32_e32 v119, v119, v235
	v_sub_f32_e32 v120, v120, v235
	v_sub_f32_e32 v121, v121, v235
	v_sub_f32_e32 v122, v122, v235
	v_sub_f32_e32 v123, v123, v235
	v_sub_f32_e32 v124, v124, v235
	v_sub_f32_e32 v125, v125, v235
	v_sub_f32_e32 v126, v126, v235
	v_sub_f32_e32 v127, v127, v235
	v_mul_f32_e32 v233, v233, v237
	v_mul_f32_e32 v32, v32, v237
	v_mul_f32_e32 v33, v33, v237
	v_mul_f32_e32 v34, v34, v237
	v_mul_f32_e32 v35, v35, v237
	v_mul_f32_e32 v36, v36, v237
	v_mul_f32_e32 v37, v37, v237
	v_mul_f32_e32 v38, v38, v237
	v_mul_f32_e32 v39, v39, v237
	v_mul_f32_e32 v40, v40, v237
	v_mul_f32_e32 v41, v41, v237
	v_mul_f32_e32 v42, v42, v237
	v_mul_f32_e32 v43, v43, v237
	v_mul_f32_e32 v44, v44, v237
	v_mul_f32_e32 v45, v45, v237
	v_mul_f32_e32 v46, v46, v237
	v_mul_f32_e32 v47, v47, v237
	v_mul_f32_e32 v48, v48, v237
	v_mul_f32_e32 v49, v49, v237
	v_mul_f32_e32 v50, v50, v237
	v_mul_f32_e32 v51, v51, v237
	v_mul_f32_e32 v52, v52, v237
	v_mul_f32_e32 v53, v53, v237
	v_mul_f32_e32 v54, v54, v237
	v_mul_f32_e32 v55, v55, v237
	v_mul_f32_e32 v56, v56, v237
	v_mul_f32_e32 v57, v57, v237
	v_mul_f32_e32 v58, v58, v237
	v_mul_f32_e32 v59, v59, v237
	v_mul_f32_e32 v60, v60, v237
	v_mul_f32_e32 v61, v61, v237
	v_mul_f32_e32 v62, v62, v237
	v_mul_f32_e32 v63, v63, v237
	v_sub_f32_e32 v80, v80, v235
	v_sub_f32_e32 v81, v81, v235
	v_sub_f32_e32 v82, v82, v235
	v_sub_f32_e32 v83, v83, v235
	v_sub_f32_e32 v84, v84, v235
	v_sub_f32_e32 v85, v85, v235
	v_sub_f32_e32 v86, v86, v235
	v_sub_f32_e32 v87, v87, v235
	v_sub_f32_e32 v88, v88, v235
	v_sub_f32_e32 v89, v89, v235
	v_sub_f32_e32 v90, v90, v235
	v_sub_f32_e32 v91, v91, v235
	v_sub_f32_e32 v92, v92, v235
	v_sub_f32_e32 v93, v93, v235
	v_sub_f32_e32 v94, v94, v235
	v_sub_f32_e32 v95, v95, v235
	v_exp_f32_e32 v80, v80
	v_exp_f32_e32 v81, v81
	v_exp_f32_e32 v82, v82
	v_exp_f32_e32 v83, v83
	v_exp_f32_e32 v84, v84
	v_exp_f32_e32 v85, v85
	v_exp_f32_e32 v86, v86
	v_exp_f32_e32 v87, v87
	v_exp_f32_e32 v88, v88
	v_exp_f32_e32 v89, v89
	v_exp_f32_e32 v90, v90
	v_exp_f32_e32 v91, v91
	v_exp_f32_e32 v92, v92
	v_exp_f32_e32 v93, v93
	v_exp_f32_e32 v94, v94
	v_exp_f32_e32 v95, v95
	s_nop 0
	v_add_f32_e32 v231, v80, v81
	v_add_f32_e32 v231, v231, v82
	v_add_f32_e32 v231, v231, v83
	v_add_f32_e32 v231, v231, v84
	v_add_f32_e32 v231, v231, v85
	v_add_f32_e32 v231, v231, v86
	v_add_f32_e32 v231, v231, v87
	v_add_f32_e32 v231, v231, v88
	v_add_f32_e32 v231, v231, v89
	v_add_f32_e32 v231, v231, v90
	v_add_f32_e32 v231, v231, v91
	v_add_f32_e32 v231, v231, v92
	v_add_f32_e32 v231, v231, v93
	v_add_f32_e32 v231, v231, v94
	v_add_f32_e32 v231, v231, v95
	v_cvt_pk_f16_f32 v168, v80, v81
	v_cvt_pk_f16_f32 v169, v82, v83
	v_cvt_pk_f16_f32 v170, v84, v85
	v_cvt_pk_f16_f32 v171, v86, v87
	v_cvt_pk_f16_f32 v172, v88, v89
	v_cvt_pk_f16_f32 v173, v90, v91
	v_cvt_pk_f16_f32 v174, v92, v93
	v_cvt_pk_f16_f32 v175, v94, v95
	s_branch .Lovfret_b31
.Lovf_b00q:
	s_waitcnt lgkmcnt(0)
	s_nop 15
	s_nop 15
	s_nop 15
	ds_read_b128 v[160:163], v225 offset:0
	ds_read_b128 v[164:167], v225 offset:32
	s_waitcnt lgkmcnt(0)
	v_mfma_f32_32x32x16_f16 v[80:95], v[160:163], v[144:147], v[112:127]
	v_mfma_f32_32x32x16_f16 v[80:95], v[164:167], v[148:151], v[80:95]
	s_nop 15
	ds_read_b128 v[160:163], v225 offset:64
	ds_read_b128 v[164:167], v225 offset:96
	s_waitcnt lgkmcnt(0)
	v_mfma_f32_32x32x16_f16 v[80:95], v[160:163], v[152:155], v[80:95]
	v_mfma_f32_32x32x16_f16 v[80:95], v[164:167], v[156:159], v[80:95]
	s_nop 15
	s_nop 15
	s_cmp_eq_u64 s[20:21], -1
	s_cbranch_scc1 .Lovfnm_b00q
	v_lshrrev_b32_e64 v235, v234, s20
	v_bfe_u32 v236, v235, 0, 1
	v_cvt_f32_u32_e32 v236, v236
	v_sub_f32_e32 v236, 1.0, v236
	v_fmac_f32_e32 v80, s35, v236
	v_bfe_u32 v236, v235, 1, 1
	v_cvt_f32_u32_e32 v236, v236
	v_sub_f32_e32 v236, 1.0, v236
	v_fmac_f32_e32 v81, s35, v236
	v_bfe_u32 v236, v235, 2, 1
	v_cvt_f32_u32_e32 v236, v236
	v_sub_f32_e32 v236, 1.0, v236
	v_fmac_f32_e32 v82, s35, v236
	v_bfe_u32 v236, v235, 3, 1
	v_cvt_f32_u32_e32 v236, v236
	v_sub_f32_e32 v236, 1.0, v236
	v_fmac_f32_e32 v83, s35, v236
	v_bfe_u32 v236, v235, 8, 1
	v_cvt_f32_u32_e32 v236, v236
	v_sub_f32_e32 v236, 1.0, v236
	v_fmac_f32_e32 v84, s35, v236
	v_bfe_u32 v236, v235, 9, 1
	v_cvt_f32_u32_e32 v236, v236
	v_sub_f32_e32 v236, 1.0, v236
	v_fmac_f32_e32 v85, s35, v236
	v_bfe_u32 v236, v235, 10, 1
	v_cvt_f32_u32_e32 v236, v236
	v_sub_f32_e32 v236, 1.0, v236
	v_fmac_f32_e32 v86, s35, v236
	v_bfe_u32 v236, v235, 11, 1
	v_cvt_f32_u32_e32 v236, v236
	v_sub_f32_e32 v236, 1.0, v236
	v_fmac_f32_e32 v87, s35, v236
	v_bfe_u32 v236, v235, 16, 1
	v_cvt_f32_u32_e32 v236, v236
	v_sub_f32_e32 v236, 1.0, v236
	v_fmac_f32_e32 v88, s35, v236
	v_bfe_u32 v236, v235, 17, 1
	v_cvt_f32_u32_e32 v236, v236
	v_sub_f32_e32 v236, 1.0, v236
	v_fmac_f32_e32 v89, s35, v236
	v_bfe_u32 v236, v235, 18, 1
	v_cvt_f32_u32_e32 v236, v236
	v_sub_f32_e32 v236, 1.0, v236
	v_fmac_f32_e32 v90, s35, v236
	v_bfe_u32 v236, v235, 19, 1
	v_cvt_f32_u32_e32 v236, v236
	v_sub_f32_e32 v236, 1.0, v236
	v_fmac_f32_e32 v91, s35, v236
	v_bfe_u32 v236, v235, 24, 1
	v_cvt_f32_u32_e32 v236, v236
	v_sub_f32_e32 v236, 1.0, v236
	v_fmac_f32_e32 v92, s35, v236
	v_bfe_u32 v236, v235, 25, 1
	v_cvt_f32_u32_e32 v236, v236
	v_sub_f32_e32 v236, 1.0, v236
	v_fmac_f32_e32 v93, s35, v236
	v_bfe_u32 v236, v235, 26, 1
	v_cvt_f32_u32_e32 v236, v236
	v_sub_f32_e32 v236, 1.0, v236
	v_fmac_f32_e32 v94, s35, v236
	v_bfe_u32 v236, v235, 27, 1
	v_cvt_f32_u32_e32 v236, v236
	v_sub_f32_e32 v236, 1.0, v236
	v_fmac_f32_e32 v95, s35, v236
.Lovfnm_b00q:
	v_max3_f32 v235, v80, v81, v82
	v_max3_f32 v235, v235, v83, v84
	v_max3_f32 v235, v235, v85, v86
	v_max3_f32 v235, v235, v87, v88
	v_max3_f32 v235, v235, v89, v90
	v_max3_f32 v235, v235, v91, v92
	v_max3_f32 v235, v235, v93, v94
	v_max_f32_e32 v235, v235, v95
	v_mov_b32_e32 v236, v235
	s_nop 1
	v_permlane32_swap_b32_e32 v235, v236
	v_max_f32_e32 v235, v235, v236
	v_max_f32_e32 v235, 0, v235
	v_exp_f32_e64 v237, -v235
	v_sub_f32_e32 v112, v112, v235
	v_sub_f32_e32 v113, v113, v235
	v_sub_f32_e32 v114, v114, v235
	v_sub_f32_e32 v115, v115, v235
	v_sub_f32_e32 v116, v116, v235
	v_sub_f32_e32 v117, v117, v235
	v_sub_f32_e32 v118, v118, v235
	v_sub_f32_e32 v119, v119, v235
	v_sub_f32_e32 v120, v120, v235
	v_sub_f32_e32 v121, v121, v235
	v_sub_f32_e32 v122, v122, v235
	v_sub_f32_e32 v123, v123, v235
	v_sub_f32_e32 v124, v124, v235
	v_sub_f32_e32 v125, v125, v235
	v_sub_f32_e32 v126, v126, v235
	v_sub_f32_e32 v127, v127, v235
	v_mul_f32_e32 v233, v233, v237
	v_mul_f32_e32 v32, v32, v237
	v_mul_f32_e32 v33, v33, v237
	v_mul_f32_e32 v34, v34, v237
	v_mul_f32_e32 v35, v35, v237
	v_mul_f32_e32 v36, v36, v237
	v_mul_f32_e32 v37, v37, v237
	v_mul_f32_e32 v38, v38, v237
	v_mul_f32_e32 v39, v39, v237
	v_mul_f32_e32 v40, v40, v237
	v_mul_f32_e32 v41, v41, v237
	v_mul_f32_e32 v42, v42, v237
	v_mul_f32_e32 v43, v43, v237
	v_mul_f32_e32 v44, v44, v237
	v_mul_f32_e32 v45, v45, v237
	v_mul_f32_e32 v46, v46, v237
	v_mul_f32_e32 v47, v47, v237
	v_mul_f32_e32 v48, v48, v237
	v_mul_f32_e32 v49, v49, v237
	v_mul_f32_e32 v50, v50, v237
	v_mul_f32_e32 v51, v51, v237
	v_mul_f32_e32 v52, v52, v237
	v_mul_f32_e32 v53, v53, v237
	v_mul_f32_e32 v54, v54, v237
	v_mul_f32_e32 v55, v55, v237
	v_mul_f32_e32 v56, v56, v237
	v_mul_f32_e32 v57, v57, v237
	v_mul_f32_e32 v58, v58, v237
	v_mul_f32_e32 v59, v59, v237
	v_mul_f32_e32 v60, v60, v237
	v_mul_f32_e32 v61, v61, v237
	v_mul_f32_e32 v62, v62, v237
	v_mul_f32_e32 v63, v63, v237
	v_sub_f32_e32 v80, v80, v235
	v_sub_f32_e32 v81, v81, v235
	v_sub_f32_e32 v82, v82, v235
	v_sub_f32_e32 v83, v83, v235
	v_sub_f32_e32 v84, v84, v235
	v_sub_f32_e32 v85, v85, v235
	v_sub_f32_e32 v86, v86, v235
	v_sub_f32_e32 v87, v87, v235
	v_sub_f32_e32 v88, v88, v235
	v_sub_f32_e32 v89, v89, v235
	v_sub_f32_e32 v90, v90, v235
	v_sub_f32_e32 v91, v91, v235
	v_sub_f32_e32 v92, v92, v235
	v_sub_f32_e32 v93, v93, v235
	v_sub_f32_e32 v94, v94, v235
	v_sub_f32_e32 v95, v95, v235
	v_exp_f32_e32 v80, v80
	v_exp_f32_e32 v81, v81
	v_exp_f32_e32 v82, v82
	v_exp_f32_e32 v83, v83
	v_exp_f32_e32 v84, v84
	v_exp_f32_e32 v85, v85
	v_exp_f32_e32 v86, v86
	v_exp_f32_e32 v87, v87
	v_exp_f32_e32 v88, v88
	v_exp_f32_e32 v89, v89
	v_exp_f32_e32 v90, v90
	v_exp_f32_e32 v91, v91
	v_exp_f32_e32 v92, v92
	v_exp_f32_e32 v93, v93
	v_exp_f32_e32 v94, v94
	v_exp_f32_e32 v95, v95
	s_nop 0
	v_add_f32_e32 v231, v80, v81
	v_add_f32_e32 v231, v231, v82
	v_add_f32_e32 v231, v231, v83
	v_add_f32_e32 v231, v231, v84
	v_add_f32_e32 v231, v231, v85
	v_add_f32_e32 v231, v231, v86
	v_add_f32_e32 v231, v231, v87
	v_add_f32_e32 v231, v231, v88
	v_add_f32_e32 v231, v231, v89
	v_add_f32_e32 v231, v231, v90
	v_add_f32_e32 v231, v231, v91
	v_add_f32_e32 v231, v231, v92
	v_add_f32_e32 v231, v231, v93
	v_add_f32_e32 v231, v231, v94
	v_add_f32_e32 v231, v231, v95
	v_cvt_pk_f16_f32 v168, v80, v81
	v_cvt_pk_f16_f32 v169, v82, v83
	v_cvt_pk_f16_f32 v170, v84, v85
	v_cvt_pk_f16_f32 v171, v86, v87
	v_cvt_pk_f16_f32 v172, v88, v89
	v_cvt_pk_f16_f32 v173, v90, v91
	v_cvt_pk_f16_f32 v174, v92, v93
	v_cvt_pk_f16_f32 v175, v94, v95
	s_branch .Lovfret_b00q
.Lovf_b01q:
	s_waitcnt lgkmcnt(0)
	s_nop 15
	s_nop 15
	s_nop 15
	ds_read_b128 v[160:163], v225 offset:4608
	ds_read_b128 v[164:167], v225 offset:4640
	s_waitcnt lgkmcnt(0)
	v_mfma_f32_32x32x16_f16 v[80:95], v[160:163], v[144:147], v[112:127]
	v_mfma_f32_32x32x16_f16 v[80:95], v[164:167], v[148:151], v[80:95]
	s_nop 15
	ds_read_b128 v[160:163], v225 offset:4672
	ds_read_b128 v[164:167], v225 offset:4704
	s_waitcnt lgkmcnt(0)
	v_mfma_f32_32x32x16_f16 v[80:95], v[160:163], v[152:155], v[80:95]
	v_mfma_f32_32x32x16_f16 v[80:95], v[164:167], v[156:159], v[80:95]
	s_nop 15
	s_nop 15
	s_cmp_eq_u64 s[20:21], -1
	s_cbranch_scc1 .Lovfnm_b01q
	v_lshrrev_b32_e64 v235, v234, s21
	v_bfe_u32 v236, v235, 0, 1
	v_cvt_f32_u32_e32 v236, v236
	v_sub_f32_e32 v236, 1.0, v236
	v_fmac_f32_e32 v80, s35, v236
	v_bfe_u32 v236, v235, 1, 1
	v_cvt_f32_u32_e32 v236, v236
	v_sub_f32_e32 v236, 1.0, v236
	v_fmac_f32_e32 v81, s35, v236
	v_bfe_u32 v236, v235, 2, 1
	v_cvt_f32_u32_e32 v236, v236
	v_sub_f32_e32 v236, 1.0, v236
	v_fmac_f32_e32 v82, s35, v236
	v_bfe_u32 v236, v235, 3, 1
	v_cvt_f32_u32_e32 v236, v236
	v_sub_f32_e32 v236, 1.0, v236
	v_fmac_f32_e32 v83, s35, v236
	v_bfe_u32 v236, v235, 8, 1
	v_cvt_f32_u32_e32 v236, v236
	v_sub_f32_e32 v236, 1.0, v236
	v_fmac_f32_e32 v84, s35, v236
	v_bfe_u32 v236, v235, 9, 1
	v_cvt_f32_u32_e32 v236, v236
	v_sub_f32_e32 v236, 1.0, v236
	v_fmac_f32_e32 v85, s35, v236
	v_bfe_u32 v236, v235, 10, 1
	v_cvt_f32_u32_e32 v236, v236
	v_sub_f32_e32 v236, 1.0, v236
	v_fmac_f32_e32 v86, s35, v236
	v_bfe_u32 v236, v235, 11, 1
	v_cvt_f32_u32_e32 v236, v236
	v_sub_f32_e32 v236, 1.0, v236
	v_fmac_f32_e32 v87, s35, v236
	v_bfe_u32 v236, v235, 16, 1
	v_cvt_f32_u32_e32 v236, v236
	v_sub_f32_e32 v236, 1.0, v236
	v_fmac_f32_e32 v88, s35, v236
	v_bfe_u32 v236, v235, 17, 1
	v_cvt_f32_u32_e32 v236, v236
	v_sub_f32_e32 v236, 1.0, v236
	v_fmac_f32_e32 v89, s35, v236
	v_bfe_u32 v236, v235, 18, 1
	v_cvt_f32_u32_e32 v236, v236
	v_sub_f32_e32 v236, 1.0, v236
	v_fmac_f32_e32 v90, s35, v236
	v_bfe_u32 v236, v235, 19, 1
	v_cvt_f32_u32_e32 v236, v236
	v_sub_f32_e32 v236, 1.0, v236
	v_fmac_f32_e32 v91, s35, v236
	v_bfe_u32 v236, v235, 24, 1
	v_cvt_f32_u32_e32 v236, v236
	v_sub_f32_e32 v236, 1.0, v236
	v_fmac_f32_e32 v92, s35, v236
	v_bfe_u32 v236, v235, 25, 1
	v_cvt_f32_u32_e32 v236, v236
	v_sub_f32_e32 v236, 1.0, v236
	v_fmac_f32_e32 v93, s35, v236
	v_bfe_u32 v236, v235, 26, 1
	v_cvt_f32_u32_e32 v236, v236
	v_sub_f32_e32 v236, 1.0, v236
	v_fmac_f32_e32 v94, s35, v236
	v_bfe_u32 v236, v235, 27, 1
	v_cvt_f32_u32_e32 v236, v236
	v_sub_f32_e32 v236, 1.0, v236
	v_fmac_f32_e32 v95, s35, v236
.Lovfnm_b01q:
	v_max3_f32 v235, v80, v81, v82
	v_max3_f32 v235, v235, v83, v84
	v_max3_f32 v235, v235, v85, v86
	v_max3_f32 v235, v235, v87, v88
	v_max3_f32 v235, v235, v89, v90
	v_max3_f32 v235, v235, v91, v92
	v_max3_f32 v235, v235, v93, v94
	v_max_f32_e32 v235, v235, v95
	v_mov_b32_e32 v236, v235
	s_nop 1
	v_permlane32_swap_b32_e32 v235, v236
	v_max_f32_e32 v235, v235, v236
	v_max_f32_e32 v235, 0, v235
	v_exp_f32_e64 v237, -v235
	v_sub_f32_e32 v112, v112, v235
	v_sub_f32_e32 v113, v113, v235
	v_sub_f32_e32 v114, v114, v235
	v_sub_f32_e32 v115, v115, v235
	v_sub_f32_e32 v116, v116, v235
	v_sub_f32_e32 v117, v117, v235
	v_sub_f32_e32 v118, v118, v235
	v_sub_f32_e32 v119, v119, v235
	v_sub_f32_e32 v120, v120, v235
	v_sub_f32_e32 v121, v121, v235
	v_sub_f32_e32 v122, v122, v235
	v_sub_f32_e32 v123, v123, v235
	v_sub_f32_e32 v124, v124, v235
	v_sub_f32_e32 v125, v125, v235
	v_sub_f32_e32 v126, v126, v235
	v_sub_f32_e32 v127, v127, v235
	v_mul_f32_e32 v233, v233, v237
	v_mul_f32_e32 v32, v32, v237
	v_mul_f32_e32 v33, v33, v237
	v_mul_f32_e32 v34, v34, v237
	v_mul_f32_e32 v35, v35, v237
	v_mul_f32_e32 v36, v36, v237
	v_mul_f32_e32 v37, v37, v237
	v_mul_f32_e32 v38, v38, v237
	v_mul_f32_e32 v39, v39, v237
	v_mul_f32_e32 v40, v40, v237
	v_mul_f32_e32 v41, v41, v237
	v_mul_f32_e32 v42, v42, v237
	v_mul_f32_e32 v43, v43, v237
	v_mul_f32_e32 v44, v44, v237
	v_mul_f32_e32 v45, v45, v237
	v_mul_f32_e32 v46, v46, v237
	v_mul_f32_e32 v47, v47, v237
	v_mul_f32_e32 v48, v48, v237
	v_mul_f32_e32 v49, v49, v237
	v_mul_f32_e32 v50, v50, v237
	v_mul_f32_e32 v51, v51, v237
	v_mul_f32_e32 v52, v52, v237
	v_mul_f32_e32 v53, v53, v237
	v_mul_f32_e32 v54, v54, v237
	v_mul_f32_e32 v55, v55, v237
	v_mul_f32_e32 v56, v56, v237
	v_mul_f32_e32 v57, v57, v237
	v_mul_f32_e32 v58, v58, v237
	v_mul_f32_e32 v59, v59, v237
	v_mul_f32_e32 v60, v60, v237
	v_mul_f32_e32 v61, v61, v237
	v_mul_f32_e32 v62, v62, v237
	v_mul_f32_e32 v63, v63, v237
	v_sub_f32_e32 v80, v80, v235
	v_sub_f32_e32 v81, v81, v235
	v_sub_f32_e32 v82, v82, v235
	v_sub_f32_e32 v83, v83, v235
	v_sub_f32_e32 v84, v84, v235
	v_sub_f32_e32 v85, v85, v235
	v_sub_f32_e32 v86, v86, v235
	v_sub_f32_e32 v87, v87, v235
	v_sub_f32_e32 v88, v88, v235
	v_sub_f32_e32 v89, v89, v235
	v_sub_f32_e32 v90, v90, v235
	v_sub_f32_e32 v91, v91, v235
	v_sub_f32_e32 v92, v92, v235
	v_sub_f32_e32 v93, v93, v235
	v_sub_f32_e32 v94, v94, v235
	v_sub_f32_e32 v95, v95, v235
	v_exp_f32_e32 v80, v80
	v_exp_f32_e32 v81, v81
	v_exp_f32_e32 v82, v82
	v_exp_f32_e32 v83, v83
	v_exp_f32_e32 v84, v84
	v_exp_f32_e32 v85, v85
	v_exp_f32_e32 v86, v86
	v_exp_f32_e32 v87, v87
	v_exp_f32_e32 v88, v88
	v_exp_f32_e32 v89, v89
	v_exp_f32_e32 v90, v90
	v_exp_f32_e32 v91, v91
	v_exp_f32_e32 v92, v92
	v_exp_f32_e32 v93, v93
	v_exp_f32_e32 v94, v94
	v_exp_f32_e32 v95, v95
	s_nop 0
	v_add_f32_e32 v231, v80, v81
	v_add_f32_e32 v231, v231, v82
	v_add_f32_e32 v231, v231, v83
	v_add_f32_e32 v231, v231, v84
	v_add_f32_e32 v231, v231, v85
	v_add_f32_e32 v231, v231, v86
	v_add_f32_e32 v231, v231, v87
	v_add_f32_e32 v231, v231, v88
	v_add_f32_e32 v231, v231, v89
	v_add_f32_e32 v231, v231, v90
	v_add_f32_e32 v231, v231, v91
	v_add_f32_e32 v231, v231, v92
	v_add_f32_e32 v231, v231, v93
	v_add_f32_e32 v231, v231, v94
	v_add_f32_e32 v231, v231, v95
	v_cvt_pk_f16_f32 v168, v80, v81
	v_cvt_pk_f16_f32 v169, v82, v83
	v_cvt_pk_f16_f32 v170, v84, v85
	v_cvt_pk_f16_f32 v171, v86, v87
	v_cvt_pk_f16_f32 v172, v88, v89
	v_cvt_pk_f16_f32 v173, v90, v91
	v_cvt_pk_f16_f32 v174, v92, v93
	v_cvt_pk_f16_f32 v175, v94, v95
	s_branch .Lovfret_b01q
.Lovf_b10q:
	s_waitcnt lgkmcnt(0)
	s_nop 15
	s_nop 15
	s_nop 15
	ds_read_b128 v[160:163], v225 offset:9216
	ds_read_b128 v[164:167], v225 offset:9248
	s_waitcnt lgkmcnt(0)
	v_mfma_f32_32x32x16_f16 v[80:95], v[160:163], v[144:147], v[112:127]
	v_mfma_f32_32x32x16_f16 v[80:95], v[164:167], v[148:151], v[80:95]
	s_nop 15
	ds_read_b128 v[160:163], v225 offset:9280
	ds_read_b128 v[164:167], v225 offset:9312
	s_waitcnt lgkmcnt(0)
	v_mfma_f32_32x32x16_f16 v[80:95], v[160:163], v[152:155], v[80:95]
	v_mfma_f32_32x32x16_f16 v[80:95], v[164:167], v[156:159], v[80:95]
	s_nop 15
	s_nop 15
	s_cmp_eq_u64 s[20:21], -1
	s_cbranch_scc1 .Lovfnm_b10q
	v_lshrrev_b32_e64 v235, v234, s20
	v_bfe_u32 v236, v235, 0, 1
	v_cvt_f32_u32_e32 v236, v236
	v_sub_f32_e32 v236, 1.0, v236
	v_fmac_f32_e32 v80, s35, v236
	v_bfe_u32 v236, v235, 1, 1
	v_cvt_f32_u32_e32 v236, v236
	v_sub_f32_e32 v236, 1.0, v236
	v_fmac_f32_e32 v81, s35, v236
	v_bfe_u32 v236, v235, 2, 1
	v_cvt_f32_u32_e32 v236, v236
	v_sub_f32_e32 v236, 1.0, v236
	v_fmac_f32_e32 v82, s35, v236
	v_bfe_u32 v236, v235, 3, 1
	v_cvt_f32_u32_e32 v236, v236
	v_sub_f32_e32 v236, 1.0, v236
	v_fmac_f32_e32 v83, s35, v236
	v_bfe_u32 v236, v235, 8, 1
	v_cvt_f32_u32_e32 v236, v236
	v_sub_f32_e32 v236, 1.0, v236
	v_fmac_f32_e32 v84, s35, v236
	v_bfe_u32 v236, v235, 9, 1
	v_cvt_f32_u32_e32 v236, v236
	v_sub_f32_e32 v236, 1.0, v236
	v_fmac_f32_e32 v85, s35, v236
	v_bfe_u32 v236, v235, 10, 1
	v_cvt_f32_u32_e32 v236, v236
	v_sub_f32_e32 v236, 1.0, v236
	v_fmac_f32_e32 v86, s35, v236
	v_bfe_u32 v236, v235, 11, 1
	v_cvt_f32_u32_e32 v236, v236
	v_sub_f32_e32 v236, 1.0, v236
	v_fmac_f32_e32 v87, s35, v236
	v_bfe_u32 v236, v235, 16, 1
	v_cvt_f32_u32_e32 v236, v236
	v_sub_f32_e32 v236, 1.0, v236
	v_fmac_f32_e32 v88, s35, v236
	v_bfe_u32 v236, v235, 17, 1
	v_cvt_f32_u32_e32 v236, v236
	v_sub_f32_e32 v236, 1.0, v236
	v_fmac_f32_e32 v89, s35, v236
	v_bfe_u32 v236, v235, 18, 1
	v_cvt_f32_u32_e32 v236, v236
	v_sub_f32_e32 v236, 1.0, v236
	v_fmac_f32_e32 v90, s35, v236
	v_bfe_u32 v236, v235, 19, 1
	v_cvt_f32_u32_e32 v236, v236
	v_sub_f32_e32 v236, 1.0, v236
	v_fmac_f32_e32 v91, s35, v236
	v_bfe_u32 v236, v235, 24, 1
	v_cvt_f32_u32_e32 v236, v236
	v_sub_f32_e32 v236, 1.0, v236
	v_fmac_f32_e32 v92, s35, v236
	v_bfe_u32 v236, v235, 25, 1
	v_cvt_f32_u32_e32 v236, v236
	v_sub_f32_e32 v236, 1.0, v236
	v_fmac_f32_e32 v93, s35, v236
	v_bfe_u32 v236, v235, 26, 1
	v_cvt_f32_u32_e32 v236, v236
	v_sub_f32_e32 v236, 1.0, v236
	v_fmac_f32_e32 v94, s35, v236
	v_bfe_u32 v236, v235, 27, 1
	v_cvt_f32_u32_e32 v236, v236
	v_sub_f32_e32 v236, 1.0, v236
	v_fmac_f32_e32 v95, s35, v236
.Lovfnm_b10q:
	v_max3_f32 v235, v80, v81, v82
	v_max3_f32 v235, v235, v83, v84
	v_max3_f32 v235, v235, v85, v86
	v_max3_f32 v235, v235, v87, v88
	v_max3_f32 v235, v235, v89, v90
	v_max3_f32 v235, v235, v91, v92
	v_max3_f32 v235, v235, v93, v94
	v_max_f32_e32 v235, v235, v95
	v_mov_b32_e32 v236, v235
	s_nop 1
	v_permlane32_swap_b32_e32 v235, v236
	v_max_f32_e32 v235, v235, v236
	v_max_f32_e32 v235, 0, v235
	v_exp_f32_e64 v237, -v235
	v_sub_f32_e32 v112, v112, v235
	v_sub_f32_e32 v113, v113, v235
	v_sub_f32_e32 v114, v114, v235
	v_sub_f32_e32 v115, v115, v235
	v_sub_f32_e32 v116, v116, v235
	v_sub_f32_e32 v117, v117, v235
	v_sub_f32_e32 v118, v118, v235
	v_sub_f32_e32 v119, v119, v235
	v_sub_f32_e32 v120, v120, v235
	v_sub_f32_e32 v121, v121, v235
	v_sub_f32_e32 v122, v122, v235
	v_sub_f32_e32 v123, v123, v235
	v_sub_f32_e32 v124, v124, v235
	v_sub_f32_e32 v125, v125, v235
	v_sub_f32_e32 v126, v126, v235
	v_sub_f32_e32 v127, v127, v235
	v_mul_f32_e32 v233, v233, v237
	v_mul_f32_e32 v32, v32, v237
	v_mul_f32_e32 v33, v33, v237
	v_mul_f32_e32 v34, v34, v237
	v_mul_f32_e32 v35, v35, v237
	v_mul_f32_e32 v36, v36, v237
	v_mul_f32_e32 v37, v37, v237
	v_mul_f32_e32 v38, v38, v237
	v_mul_f32_e32 v39, v39, v237
	v_mul_f32_e32 v40, v40, v237
	v_mul_f32_e32 v41, v41, v237
	v_mul_f32_e32 v42, v42, v237
	v_mul_f32_e32 v43, v43, v237
	v_mul_f32_e32 v44, v44, v237
	v_mul_f32_e32 v45, v45, v237
	v_mul_f32_e32 v46, v46, v237
	v_mul_f32_e32 v47, v47, v237
	v_mul_f32_e32 v48, v48, v237
	v_mul_f32_e32 v49, v49, v237
	v_mul_f32_e32 v50, v50, v237
	v_mul_f32_e32 v51, v51, v237
	v_mul_f32_e32 v52, v52, v237
	v_mul_f32_e32 v53, v53, v237
	v_mul_f32_e32 v54, v54, v237
	v_mul_f32_e32 v55, v55, v237
	v_mul_f32_e32 v56, v56, v237
	v_mul_f32_e32 v57, v57, v237
	v_mul_f32_e32 v58, v58, v237
	v_mul_f32_e32 v59, v59, v237
	v_mul_f32_e32 v60, v60, v237
	v_mul_f32_e32 v61, v61, v237
	v_mul_f32_e32 v62, v62, v237
	v_mul_f32_e32 v63, v63, v237
	v_sub_f32_e32 v80, v80, v235
	v_sub_f32_e32 v81, v81, v235
	v_sub_f32_e32 v82, v82, v235
	v_sub_f32_e32 v83, v83, v235
	v_sub_f32_e32 v84, v84, v235
	v_sub_f32_e32 v85, v85, v235
	v_sub_f32_e32 v86, v86, v235
	v_sub_f32_e32 v87, v87, v235
	v_sub_f32_e32 v88, v88, v235
	v_sub_f32_e32 v89, v89, v235
	v_sub_f32_e32 v90, v90, v235
	v_sub_f32_e32 v91, v91, v235
	v_sub_f32_e32 v92, v92, v235
	v_sub_f32_e32 v93, v93, v235
	v_sub_f32_e32 v94, v94, v235
	v_sub_f32_e32 v95, v95, v235
	v_exp_f32_e32 v80, v80
	v_exp_f32_e32 v81, v81
	v_exp_f32_e32 v82, v82
	v_exp_f32_e32 v83, v83
	v_exp_f32_e32 v84, v84
	v_exp_f32_e32 v85, v85
	v_exp_f32_e32 v86, v86
	v_exp_f32_e32 v87, v87
	v_exp_f32_e32 v88, v88
	v_exp_f32_e32 v89, v89
	v_exp_f32_e32 v90, v90
	v_exp_f32_e32 v91, v91
	v_exp_f32_e32 v92, v92
	v_exp_f32_e32 v93, v93
	v_exp_f32_e32 v94, v94
	v_exp_f32_e32 v95, v95
	s_nop 0
	v_add_f32_e32 v231, v80, v81
	v_add_f32_e32 v231, v231, v82
	v_add_f32_e32 v231, v231, v83
	v_add_f32_e32 v231, v231, v84
	v_add_f32_e32 v231, v231, v85
	v_add_f32_e32 v231, v231, v86
	v_add_f32_e32 v231, v231, v87
	v_add_f32_e32 v231, v231, v88
	v_add_f32_e32 v231, v231, v89
	v_add_f32_e32 v231, v231, v90
	v_add_f32_e32 v231, v231, v91
	v_add_f32_e32 v231, v231, v92
	v_add_f32_e32 v231, v231, v93
	v_add_f32_e32 v231, v231, v94
	v_add_f32_e32 v231, v231, v95
	v_cvt_pk_f16_f32 v168, v80, v81
	v_cvt_pk_f16_f32 v169, v82, v83
	v_cvt_pk_f16_f32 v170, v84, v85
	v_cvt_pk_f16_f32 v171, v86, v87
	v_cvt_pk_f16_f32 v172, v88, v89
	v_cvt_pk_f16_f32 v173, v90, v91
	v_cvt_pk_f16_f32 v174, v92, v93
	v_cvt_pk_f16_f32 v175, v94, v95
	s_branch .Lovfret_b10q
.Lovf_b11q:
	s_waitcnt lgkmcnt(0)
	s_nop 15
	s_nop 15
	s_nop 15
	ds_read_b128 v[160:163], v225 offset:13824
	ds_read_b128 v[164:167], v225 offset:13856
	s_waitcnt lgkmcnt(0)
	v_mfma_f32_32x32x16_f16 v[80:95], v[160:163], v[144:147], v[112:127]
	v_mfma_f32_32x32x16_f16 v[80:95], v[164:167], v[148:151], v[80:95]
	s_nop 15
	ds_read_b128 v[160:163], v225 offset:13888
	ds_read_b128 v[164:167], v225 offset:13920
	s_waitcnt lgkmcnt(0)
	v_mfma_f32_32x32x16_f16 v[80:95], v[160:163], v[152:155], v[80:95]
	v_mfma_f32_32x32x16_f16 v[80:95], v[164:167], v[156:159], v[80:95]
	s_nop 15
	s_nop 15
	s_cmp_eq_u64 s[20:21], -1
	s_cbranch_scc1 .Lovfnm_b11q
	v_lshrrev_b32_e64 v235, v234, s21
	v_bfe_u32 v236, v235, 0, 1
	v_cvt_f32_u32_e32 v236, v236
	v_sub_f32_e32 v236, 1.0, v236
	v_fmac_f32_e32 v80, s35, v236
	v_bfe_u32 v236, v235, 1, 1
	v_cvt_f32_u32_e32 v236, v236
	v_sub_f32_e32 v236, 1.0, v236
	v_fmac_f32_e32 v81, s35, v236
	v_bfe_u32 v236, v235, 2, 1
	v_cvt_f32_u32_e32 v236, v236
	v_sub_f32_e32 v236, 1.0, v236
	v_fmac_f32_e32 v82, s35, v236
	v_bfe_u32 v236, v235, 3, 1
	v_cvt_f32_u32_e32 v236, v236
	v_sub_f32_e32 v236, 1.0, v236
	v_fmac_f32_e32 v83, s35, v236
	v_bfe_u32 v236, v235, 8, 1
	v_cvt_f32_u32_e32 v236, v236
	v_sub_f32_e32 v236, 1.0, v236
	v_fmac_f32_e32 v84, s35, v236
	v_bfe_u32 v236, v235, 9, 1
	v_cvt_f32_u32_e32 v236, v236
	v_sub_f32_e32 v236, 1.0, v236
	v_fmac_f32_e32 v85, s35, v236
	v_bfe_u32 v236, v235, 10, 1
	v_cvt_f32_u32_e32 v236, v236
	v_sub_f32_e32 v236, 1.0, v236
	v_fmac_f32_e32 v86, s35, v236
	v_bfe_u32 v236, v235, 11, 1
	v_cvt_f32_u32_e32 v236, v236
	v_sub_f32_e32 v236, 1.0, v236
	v_fmac_f32_e32 v87, s35, v236
	v_bfe_u32 v236, v235, 16, 1
	v_cvt_f32_u32_e32 v236, v236
	v_sub_f32_e32 v236, 1.0, v236
	v_fmac_f32_e32 v88, s35, v236
	v_bfe_u32 v236, v235, 17, 1
	v_cvt_f32_u32_e32 v236, v236
	v_sub_f32_e32 v236, 1.0, v236
	v_fmac_f32_e32 v89, s35, v236
	v_bfe_u32 v236, v235, 18, 1
	v_cvt_f32_u32_e32 v236, v236
	v_sub_f32_e32 v236, 1.0, v236
	v_fmac_f32_e32 v90, s35, v236
	v_bfe_u32 v236, v235, 19, 1
	v_cvt_f32_u32_e32 v236, v236
	v_sub_f32_e32 v236, 1.0, v236
	v_fmac_f32_e32 v91, s35, v236
	v_bfe_u32 v236, v235, 24, 1
	v_cvt_f32_u32_e32 v236, v236
	v_sub_f32_e32 v236, 1.0, v236
	v_fmac_f32_e32 v92, s35, v236
	v_bfe_u32 v236, v235, 25, 1
	v_cvt_f32_u32_e32 v236, v236
	v_sub_f32_e32 v236, 1.0, v236
	v_fmac_f32_e32 v93, s35, v236
	v_bfe_u32 v236, v235, 26, 1
	v_cvt_f32_u32_e32 v236, v236
	v_sub_f32_e32 v236, 1.0, v236
	v_fmac_f32_e32 v94, s35, v236
	v_bfe_u32 v236, v235, 27, 1
	v_cvt_f32_u32_e32 v236, v236
	v_sub_f32_e32 v236, 1.0, v236
	v_fmac_f32_e32 v95, s35, v236
.Lovfnm_b11q:
	v_max3_f32 v235, v80, v81, v82
	v_max3_f32 v235, v235, v83, v84
	v_max3_f32 v235, v235, v85, v86
	v_max3_f32 v235, v235, v87, v88
	v_max3_f32 v235, v235, v89, v90
	v_max3_f32 v235, v235, v91, v92
	v_max3_f32 v235, v235, v93, v94
	v_max_f32_e32 v235, v235, v95
	v_mov_b32_e32 v236, v235
	s_nop 1
	v_permlane32_swap_b32_e32 v235, v236
	v_max_f32_e32 v235, v235, v236
	v_max_f32_e32 v235, 0, v235
	v_exp_f32_e64 v237, -v235
	v_sub_f32_e32 v112, v112, v235
	v_sub_f32_e32 v113, v113, v235
	v_sub_f32_e32 v114, v114, v235
	v_sub_f32_e32 v115, v115, v235
	v_sub_f32_e32 v116, v116, v235
	v_sub_f32_e32 v117, v117, v235
	v_sub_f32_e32 v118, v118, v235
	v_sub_f32_e32 v119, v119, v235
	v_sub_f32_e32 v120, v120, v235
	v_sub_f32_e32 v121, v121, v235
	v_sub_f32_e32 v122, v122, v235
	v_sub_f32_e32 v123, v123, v235
	v_sub_f32_e32 v124, v124, v235
	v_sub_f32_e32 v125, v125, v235
	v_sub_f32_e32 v126, v126, v235
	v_sub_f32_e32 v127, v127, v235
	v_mul_f32_e32 v233, v233, v237
	v_mul_f32_e32 v32, v32, v237
	v_mul_f32_e32 v33, v33, v237
	v_mul_f32_e32 v34, v34, v237
	v_mul_f32_e32 v35, v35, v237
	v_mul_f32_e32 v36, v36, v237
	v_mul_f32_e32 v37, v37, v237
	v_mul_f32_e32 v38, v38, v237
	v_mul_f32_e32 v39, v39, v237
	v_mul_f32_e32 v40, v40, v237
	v_mul_f32_e32 v41, v41, v237
	v_mul_f32_e32 v42, v42, v237
	v_mul_f32_e32 v43, v43, v237
	v_mul_f32_e32 v44, v44, v237
	v_mul_f32_e32 v45, v45, v237
	v_mul_f32_e32 v46, v46, v237
	v_mul_f32_e32 v47, v47, v237
	v_mul_f32_e32 v48, v48, v237
	v_mul_f32_e32 v49, v49, v237
	v_mul_f32_e32 v50, v50, v237
	v_mul_f32_e32 v51, v51, v237
	v_mul_f32_e32 v52, v52, v237
	v_mul_f32_e32 v53, v53, v237
	v_mul_f32_e32 v54, v54, v237
	v_mul_f32_e32 v55, v55, v237
	v_mul_f32_e32 v56, v56, v237
	v_mul_f32_e32 v57, v57, v237
	v_mul_f32_e32 v58, v58, v237
	v_mul_f32_e32 v59, v59, v237
	v_mul_f32_e32 v60, v60, v237
	v_mul_f32_e32 v61, v61, v237
	v_mul_f32_e32 v62, v62, v237
	v_mul_f32_e32 v63, v63, v237
	v_sub_f32_e32 v80, v80, v235
	v_sub_f32_e32 v81, v81, v235
	v_sub_f32_e32 v82, v82, v235
	v_sub_f32_e32 v83, v83, v235
	v_sub_f32_e32 v84, v84, v235
	v_sub_f32_e32 v85, v85, v235
	v_sub_f32_e32 v86, v86, v235
	v_sub_f32_e32 v87, v87, v235
	v_sub_f32_e32 v88, v88, v235
	v_sub_f32_e32 v89, v89, v235
	v_sub_f32_e32 v90, v90, v235
	v_sub_f32_e32 v91, v91, v235
	v_sub_f32_e32 v92, v92, v235
	v_sub_f32_e32 v93, v93, v235
	v_sub_f32_e32 v94, v94, v235
	v_sub_f32_e32 v95, v95, v235
	v_exp_f32_e32 v80, v80
	v_exp_f32_e32 v81, v81
	v_exp_f32_e32 v82, v82
	v_exp_f32_e32 v83, v83
	v_exp_f32_e32 v84, v84
	v_exp_f32_e32 v85, v85
	v_exp_f32_e32 v86, v86
	v_exp_f32_e32 v87, v87
	v_exp_f32_e32 v88, v88
	v_exp_f32_e32 v89, v89
	v_exp_f32_e32 v90, v90
	v_exp_f32_e32 v91, v91
	v_exp_f32_e32 v92, v92
	v_exp_f32_e32 v93, v93
	v_exp_f32_e32 v94, v94
	v_exp_f32_e32 v95, v95
	s_nop 0
	v_add_f32_e32 v231, v80, v81
	v_add_f32_e32 v231, v231, v82
	v_add_f32_e32 v231, v231, v83
	v_add_f32_e32 v231, v231, v84
	v_add_f32_e32 v231, v231, v85
	v_add_f32_e32 v231, v231, v86
	v_add_f32_e32 v231, v231, v87
	v_add_f32_e32 v231, v231, v88
	v_add_f32_e32 v231, v231, v89
	v_add_f32_e32 v231, v231, v90
	v_add_f32_e32 v231, v231, v91
	v_add_f32_e32 v231, v231, v92
	v_add_f32_e32 v231, v231, v93
	v_add_f32_e32 v231, v231, v94
	v_add_f32_e32 v231, v231, v95
	v_cvt_pk_f16_f32 v168, v80, v81
	v_cvt_pk_f16_f32 v169, v82, v83
	v_cvt_pk_f16_f32 v170, v84, v85
	v_cvt_pk_f16_f32 v171, v86, v87
	v_cvt_pk_f16_f32 v172, v88, v89
	v_cvt_pk_f16_f32 v173, v90, v91
	v_cvt_pk_f16_f32 v174, v92, v93
	v_cvt_pk_f16_f32 v175, v94, v95
	s_branch .Lovfret_b11q
.Lovf_b20q:
	s_waitcnt lgkmcnt(0)
	s_nop 15
	s_nop 15
	s_nop 15
	ds_read_b128 v[160:163], v225 offset:18432
	ds_read_b128 v[164:167], v225 offset:18464
	s_waitcnt lgkmcnt(0)
	v_mfma_f32_32x32x16_f16 v[80:95], v[160:163], v[144:147], v[112:127]
	v_mfma_f32_32x32x16_f16 v[80:95], v[164:167], v[148:151], v[80:95]
	s_nop 15
	ds_read_b128 v[160:163], v225 offset:18496
	ds_read_b128 v[164:167], v225 offset:18528
	s_waitcnt lgkmcnt(0)
	v_mfma_f32_32x32x16_f16 v[80:95], v[160:163], v[152:155], v[80:95]
	v_mfma_f32_32x32x16_f16 v[80:95], v[164:167], v[156:159], v[80:95]
	s_nop 15
	s_nop 15
	s_cmp_eq_u64 s[20:21], -1
	s_cbranch_scc1 .Lovfnm_b20q
	v_lshrrev_b32_e64 v235, v234, s20
	v_bfe_u32 v236, v235, 0, 1
	v_cvt_f32_u32_e32 v236, v236
	v_sub_f32_e32 v236, 1.0, v236
	v_fmac_f32_e32 v80, s35, v236
	v_bfe_u32 v236, v235, 1, 1
	v_cvt_f32_u32_e32 v236, v236
	v_sub_f32_e32 v236, 1.0, v236
	v_fmac_f32_e32 v81, s35, v236
	v_bfe_u32 v236, v235, 2, 1
	v_cvt_f32_u32_e32 v236, v236
	v_sub_f32_e32 v236, 1.0, v236
	v_fmac_f32_e32 v82, s35, v236
	v_bfe_u32 v236, v235, 3, 1
	v_cvt_f32_u32_e32 v236, v236
	v_sub_f32_e32 v236, 1.0, v236
	v_fmac_f32_e32 v83, s35, v236
	v_bfe_u32 v236, v235, 8, 1
	v_cvt_f32_u32_e32 v236, v236
	v_sub_f32_e32 v236, 1.0, v236
	v_fmac_f32_e32 v84, s35, v236
	v_bfe_u32 v236, v235, 9, 1
	v_cvt_f32_u32_e32 v236, v236
	v_sub_f32_e32 v236, 1.0, v236
	v_fmac_f32_e32 v85, s35, v236
	v_bfe_u32 v236, v235, 10, 1
	v_cvt_f32_u32_e32 v236, v236
	v_sub_f32_e32 v236, 1.0, v236
	v_fmac_f32_e32 v86, s35, v236
	v_bfe_u32 v236, v235, 11, 1
	v_cvt_f32_u32_e32 v236, v236
	v_sub_f32_e32 v236, 1.0, v236
	v_fmac_f32_e32 v87, s35, v236
	v_bfe_u32 v236, v235, 16, 1
	v_cvt_f32_u32_e32 v236, v236
	v_sub_f32_e32 v236, 1.0, v236
	v_fmac_f32_e32 v88, s35, v236
	v_bfe_u32 v236, v235, 17, 1
	v_cvt_f32_u32_e32 v236, v236
	v_sub_f32_e32 v236, 1.0, v236
	v_fmac_f32_e32 v89, s35, v236
	v_bfe_u32 v236, v235, 18, 1
	v_cvt_f32_u32_e32 v236, v236
	v_sub_f32_e32 v236, 1.0, v236
	v_fmac_f32_e32 v90, s35, v236
	v_bfe_u32 v236, v235, 19, 1
	v_cvt_f32_u32_e32 v236, v236
	v_sub_f32_e32 v236, 1.0, v236
	v_fmac_f32_e32 v91, s35, v236
	v_bfe_u32 v236, v235, 24, 1
	v_cvt_f32_u32_e32 v236, v236
	v_sub_f32_e32 v236, 1.0, v236
	v_fmac_f32_e32 v92, s35, v236
	v_bfe_u32 v236, v235, 25, 1
	v_cvt_f32_u32_e32 v236, v236
	v_sub_f32_e32 v236, 1.0, v236
	v_fmac_f32_e32 v93, s35, v236
	v_bfe_u32 v236, v235, 26, 1
	v_cvt_f32_u32_e32 v236, v236
	v_sub_f32_e32 v236, 1.0, v236
	v_fmac_f32_e32 v94, s35, v236
	v_bfe_u32 v236, v235, 27, 1
	v_cvt_f32_u32_e32 v236, v236
	v_sub_f32_e32 v236, 1.0, v236
	v_fmac_f32_e32 v95, s35, v236
.Lovfnm_b20q:
	v_max3_f32 v235, v80, v81, v82
	v_max3_f32 v235, v235, v83, v84
	v_max3_f32 v235, v235, v85, v86
	v_max3_f32 v235, v235, v87, v88
	v_max3_f32 v235, v235, v89, v90
	v_max3_f32 v235, v235, v91, v92
	v_max3_f32 v235, v235, v93, v94
	v_max_f32_e32 v235, v235, v95
	v_mov_b32_e32 v236, v235
	s_nop 1
	v_permlane32_swap_b32_e32 v235, v236
	v_max_f32_e32 v235, v235, v236
	v_max_f32_e32 v235, 0, v235
	v_exp_f32_e64 v237, -v235
	v_sub_f32_e32 v112, v112, v235
	v_sub_f32_e32 v113, v113, v235
	v_sub_f32_e32 v114, v114, v235
	v_sub_f32_e32 v115, v115, v235
	v_sub_f32_e32 v116, v116, v235
	v_sub_f32_e32 v117, v117, v235
	v_sub_f32_e32 v118, v118, v235
	v_sub_f32_e32 v119, v119, v235
	v_sub_f32_e32 v120, v120, v235
	v_sub_f32_e32 v121, v121, v235
	v_sub_f32_e32 v122, v122, v235
	v_sub_f32_e32 v123, v123, v235
	v_sub_f32_e32 v124, v124, v235
	v_sub_f32_e32 v125, v125, v235
	v_sub_f32_e32 v126, v126, v235
	v_sub_f32_e32 v127, v127, v235
	v_mul_f32_e32 v233, v233, v237
	v_mul_f32_e32 v32, v32, v237
	v_mul_f32_e32 v33, v33, v237
	v_mul_f32_e32 v34, v34, v237
	v_mul_f32_e32 v35, v35, v237
	v_mul_f32_e32 v36, v36, v237
	v_mul_f32_e32 v37, v37, v237
	v_mul_f32_e32 v38, v38, v237
	v_mul_f32_e32 v39, v39, v237
	v_mul_f32_e32 v40, v40, v237
	v_mul_f32_e32 v41, v41, v237
	v_mul_f32_e32 v42, v42, v237
	v_mul_f32_e32 v43, v43, v237
	v_mul_f32_e32 v44, v44, v237
	v_mul_f32_e32 v45, v45, v237
	v_mul_f32_e32 v46, v46, v237
	v_mul_f32_e32 v47, v47, v237
	v_mul_f32_e32 v48, v48, v237
	v_mul_f32_e32 v49, v49, v237
	v_mul_f32_e32 v50, v50, v237
	v_mul_f32_e32 v51, v51, v237
	v_mul_f32_e32 v52, v52, v237
	v_mul_f32_e32 v53, v53, v237
	v_mul_f32_e32 v54, v54, v237
	v_mul_f32_e32 v55, v55, v237
	v_mul_f32_e32 v56, v56, v237
	v_mul_f32_e32 v57, v57, v237
	v_mul_f32_e32 v58, v58, v237
	v_mul_f32_e32 v59, v59, v237
	v_mul_f32_e32 v60, v60, v237
	v_mul_f32_e32 v61, v61, v237
	v_mul_f32_e32 v62, v62, v237
	v_mul_f32_e32 v63, v63, v237
	v_sub_f32_e32 v80, v80, v235
	v_sub_f32_e32 v81, v81, v235
	v_sub_f32_e32 v82, v82, v235
	v_sub_f32_e32 v83, v83, v235
	v_sub_f32_e32 v84, v84, v235
	v_sub_f32_e32 v85, v85, v235
	v_sub_f32_e32 v86, v86, v235
	v_sub_f32_e32 v87, v87, v235
	v_sub_f32_e32 v88, v88, v235
	v_sub_f32_e32 v89, v89, v235
	v_sub_f32_e32 v90, v90, v235
	v_sub_f32_e32 v91, v91, v235
	v_sub_f32_e32 v92, v92, v235
	v_sub_f32_e32 v93, v93, v235
	v_sub_f32_e32 v94, v94, v235
	v_sub_f32_e32 v95, v95, v235
	v_exp_f32_e32 v80, v80
	v_exp_f32_e32 v81, v81
	v_exp_f32_e32 v82, v82
	v_exp_f32_e32 v83, v83
	v_exp_f32_e32 v84, v84
	v_exp_f32_e32 v85, v85
	v_exp_f32_e32 v86, v86
	v_exp_f32_e32 v87, v87
	v_exp_f32_e32 v88, v88
	v_exp_f32_e32 v89, v89
	v_exp_f32_e32 v90, v90
	v_exp_f32_e32 v91, v91
	v_exp_f32_e32 v92, v92
	v_exp_f32_e32 v93, v93
	v_exp_f32_e32 v94, v94
	v_exp_f32_e32 v95, v95
	s_nop 0
	v_add_f32_e32 v231, v80, v81
	v_add_f32_e32 v231, v231, v82
	v_add_f32_e32 v231, v231, v83
	v_add_f32_e32 v231, v231, v84
	v_add_f32_e32 v231, v231, v85
	v_add_f32_e32 v231, v231, v86
	v_add_f32_e32 v231, v231, v87
	v_add_f32_e32 v231, v231, v88
	v_add_f32_e32 v231, v231, v89
	v_add_f32_e32 v231, v231, v90
	v_add_f32_e32 v231, v231, v91
	v_add_f32_e32 v231, v231, v92
	v_add_f32_e32 v231, v231, v93
	v_add_f32_e32 v231, v231, v94
	v_add_f32_e32 v231, v231, v95
	v_cvt_pk_f16_f32 v168, v80, v81
	v_cvt_pk_f16_f32 v169, v82, v83
	v_cvt_pk_f16_f32 v170, v84, v85
	v_cvt_pk_f16_f32 v171, v86, v87
	v_cvt_pk_f16_f32 v172, v88, v89
	v_cvt_pk_f16_f32 v173, v90, v91
	v_cvt_pk_f16_f32 v174, v92, v93
	v_cvt_pk_f16_f32 v175, v94, v95
	s_branch .Lovfret_b20q
.Lovf_b21q:
	s_waitcnt lgkmcnt(0)
	s_nop 15
	s_nop 15
	s_nop 15
	ds_read_b128 v[160:163], v225 offset:23040
	ds_read_b128 v[164:167], v225 offset:23072
	s_waitcnt lgkmcnt(0)
	v_mfma_f32_32x32x16_f16 v[80:95], v[160:163], v[144:147], v[112:127]
	v_mfma_f32_32x32x16_f16 v[80:95], v[164:167], v[148:151], v[80:95]
	s_nop 15
	ds_read_b128 v[160:163], v225 offset:23104
	ds_read_b128 v[164:167], v225 offset:23136
	s_waitcnt lgkmcnt(0)
	v_mfma_f32_32x32x16_f16 v[80:95], v[160:163], v[152:155], v[80:95]
	v_mfma_f32_32x32x16_f16 v[80:95], v[164:167], v[156:159], v[80:95]
	s_nop 15
	s_nop 15
	s_cmp_eq_u64 s[20:21], -1
	s_cbranch_scc1 .Lovfnm_b21q
	v_lshrrev_b32_e64 v235, v234, s21
	v_bfe_u32 v236, v235, 0, 1
	v_cvt_f32_u32_e32 v236, v236
	v_sub_f32_e32 v236, 1.0, v236
	v_fmac_f32_e32 v80, s35, v236
	v_bfe_u32 v236, v235, 1, 1
	v_cvt_f32_u32_e32 v236, v236
	v_sub_f32_e32 v236, 1.0, v236
	v_fmac_f32_e32 v81, s35, v236
	v_bfe_u32 v236, v235, 2, 1
	v_cvt_f32_u32_e32 v236, v236
	v_sub_f32_e32 v236, 1.0, v236
	v_fmac_f32_e32 v82, s35, v236
	v_bfe_u32 v236, v235, 3, 1
	v_cvt_f32_u32_e32 v236, v236
	v_sub_f32_e32 v236, 1.0, v236
	v_fmac_f32_e32 v83, s35, v236
	v_bfe_u32 v236, v235, 8, 1
	v_cvt_f32_u32_e32 v236, v236
	v_sub_f32_e32 v236, 1.0, v236
	v_fmac_f32_e32 v84, s35, v236
	v_bfe_u32 v236, v235, 9, 1
	v_cvt_f32_u32_e32 v236, v236
	v_sub_f32_e32 v236, 1.0, v236
	v_fmac_f32_e32 v85, s35, v236
	v_bfe_u32 v236, v235, 10, 1
	v_cvt_f32_u32_e32 v236, v236
	v_sub_f32_e32 v236, 1.0, v236
	v_fmac_f32_e32 v86, s35, v236
	v_bfe_u32 v236, v235, 11, 1
	v_cvt_f32_u32_e32 v236, v236
	v_sub_f32_e32 v236, 1.0, v236
	v_fmac_f32_e32 v87, s35, v236
	v_bfe_u32 v236, v235, 16, 1
	v_cvt_f32_u32_e32 v236, v236
	v_sub_f32_e32 v236, 1.0, v236
	v_fmac_f32_e32 v88, s35, v236
	v_bfe_u32 v236, v235, 17, 1
	v_cvt_f32_u32_e32 v236, v236
	v_sub_f32_e32 v236, 1.0, v236
	v_fmac_f32_e32 v89, s35, v236
	v_bfe_u32 v236, v235, 18, 1
	v_cvt_f32_u32_e32 v236, v236
	v_sub_f32_e32 v236, 1.0, v236
	v_fmac_f32_e32 v90, s35, v236
	v_bfe_u32 v236, v235, 19, 1
	v_cvt_f32_u32_e32 v236, v236
	v_sub_f32_e32 v236, 1.0, v236
	v_fmac_f32_e32 v91, s35, v236
	v_bfe_u32 v236, v235, 24, 1
	v_cvt_f32_u32_e32 v236, v236
	v_sub_f32_e32 v236, 1.0, v236
	v_fmac_f32_e32 v92, s35, v236
	v_bfe_u32 v236, v235, 25, 1
	v_cvt_f32_u32_e32 v236, v236
	v_sub_f32_e32 v236, 1.0, v236
	v_fmac_f32_e32 v93, s35, v236
	v_bfe_u32 v236, v235, 26, 1
	v_cvt_f32_u32_e32 v236, v236
	v_sub_f32_e32 v236, 1.0, v236
	v_fmac_f32_e32 v94, s35, v236
	v_bfe_u32 v236, v235, 27, 1
	v_cvt_f32_u32_e32 v236, v236
	v_sub_f32_e32 v236, 1.0, v236
	v_fmac_f32_e32 v95, s35, v236
.Lovfnm_b21q:
	v_max3_f32 v235, v80, v81, v82
	v_max3_f32 v235, v235, v83, v84
	v_max3_f32 v235, v235, v85, v86
	v_max3_f32 v235, v235, v87, v88
	v_max3_f32 v235, v235, v89, v90
	v_max3_f32 v235, v235, v91, v92
	v_max3_f32 v235, v235, v93, v94
	v_max_f32_e32 v235, v235, v95
	v_mov_b32_e32 v236, v235
	s_nop 1
	v_permlane32_swap_b32_e32 v235, v236
	v_max_f32_e32 v235, v235, v236
	v_max_f32_e32 v235, 0, v235
	v_exp_f32_e64 v237, -v235
	v_sub_f32_e32 v112, v112, v235
	v_sub_f32_e32 v113, v113, v235
	v_sub_f32_e32 v114, v114, v235
	v_sub_f32_e32 v115, v115, v235
	v_sub_f32_e32 v116, v116, v235
	v_sub_f32_e32 v117, v117, v235
	v_sub_f32_e32 v118, v118, v235
	v_sub_f32_e32 v119, v119, v235
	v_sub_f32_e32 v120, v120, v235
	v_sub_f32_e32 v121, v121, v235
	v_sub_f32_e32 v122, v122, v235
	v_sub_f32_e32 v123, v123, v235
	v_sub_f32_e32 v124, v124, v235
	v_sub_f32_e32 v125, v125, v235
	v_sub_f32_e32 v126, v126, v235
	v_sub_f32_e32 v127, v127, v235
	v_mul_f32_e32 v233, v233, v237
	v_mul_f32_e32 v32, v32, v237
	v_mul_f32_e32 v33, v33, v237
	v_mul_f32_e32 v34, v34, v237
	v_mul_f32_e32 v35, v35, v237
	v_mul_f32_e32 v36, v36, v237
	v_mul_f32_e32 v37, v37, v237
	v_mul_f32_e32 v38, v38, v237
	v_mul_f32_e32 v39, v39, v237
	v_mul_f32_e32 v40, v40, v237
	v_mul_f32_e32 v41, v41, v237
	v_mul_f32_e32 v42, v42, v237
	v_mul_f32_e32 v43, v43, v237
	v_mul_f32_e32 v44, v44, v237
	v_mul_f32_e32 v45, v45, v237
	v_mul_f32_e32 v46, v46, v237
	v_mul_f32_e32 v47, v47, v237
	v_mul_f32_e32 v48, v48, v237
	v_mul_f32_e32 v49, v49, v237
	v_mul_f32_e32 v50, v50, v237
	v_mul_f32_e32 v51, v51, v237
	v_mul_f32_e32 v52, v52, v237
	v_mul_f32_e32 v53, v53, v237
	v_mul_f32_e32 v54, v54, v237
	v_mul_f32_e32 v55, v55, v237
	v_mul_f32_e32 v56, v56, v237
	v_mul_f32_e32 v57, v57, v237
	v_mul_f32_e32 v58, v58, v237
	v_mul_f32_e32 v59, v59, v237
	v_mul_f32_e32 v60, v60, v237
	v_mul_f32_e32 v61, v61, v237
	v_mul_f32_e32 v62, v62, v237
	v_mul_f32_e32 v63, v63, v237
	v_sub_f32_e32 v80, v80, v235
	v_sub_f32_e32 v81, v81, v235
	v_sub_f32_e32 v82, v82, v235
	v_sub_f32_e32 v83, v83, v235
	v_sub_f32_e32 v84, v84, v235
	v_sub_f32_e32 v85, v85, v235
	v_sub_f32_e32 v86, v86, v235
	v_sub_f32_e32 v87, v87, v235
	v_sub_f32_e32 v88, v88, v235
	v_sub_f32_e32 v89, v89, v235
	v_sub_f32_e32 v90, v90, v235
	v_sub_f32_e32 v91, v91, v235
	v_sub_f32_e32 v92, v92, v235
	v_sub_f32_e32 v93, v93, v235
	v_sub_f32_e32 v94, v94, v235
	v_sub_f32_e32 v95, v95, v235
	v_exp_f32_e32 v80, v80
	v_exp_f32_e32 v81, v81
	v_exp_f32_e32 v82, v82
	v_exp_f32_e32 v83, v83
	v_exp_f32_e32 v84, v84
	v_exp_f32_e32 v85, v85
	v_exp_f32_e32 v86, v86
	v_exp_f32_e32 v87, v87
	v_exp_f32_e32 v88, v88
	v_exp_f32_e32 v89, v89
	v_exp_f32_e32 v90, v90
	v_exp_f32_e32 v91, v91
	v_exp_f32_e32 v92, v92
	v_exp_f32_e32 v93, v93
	v_exp_f32_e32 v94, v94
	v_exp_f32_e32 v95, v95
	s_nop 0
	v_add_f32_e32 v231, v80, v81
	v_add_f32_e32 v231, v231, v82
	v_add_f32_e32 v231, v231, v83
	v_add_f32_e32 v231, v231, v84
	v_add_f32_e32 v231, v231, v85
	v_add_f32_e32 v231, v231, v86
	v_add_f32_e32 v231, v231, v87
	v_add_f32_e32 v231, v231, v88
	v_add_f32_e32 v231, v231, v89
	v_add_f32_e32 v231, v231, v90
	v_add_f32_e32 v231, v231, v91
	v_add_f32_e32 v231, v231, v92
	v_add_f32_e32 v231, v231, v93
	v_add_f32_e32 v231, v231, v94
	v_add_f32_e32 v231, v231, v95
	v_cvt_pk_f16_f32 v168, v80, v81
	v_cvt_pk_f16_f32 v169, v82, v83
	v_cvt_pk_f16_f32 v170, v84, v85
	v_cvt_pk_f16_f32 v171, v86, v87
	v_cvt_pk_f16_f32 v172, v88, v89
	v_cvt_pk_f16_f32 v173, v90, v91
	v_cvt_pk_f16_f32 v174, v92, v93
	v_cvt_pk_f16_f32 v175, v94, v95
	s_branch .Lovfret_b21q
.Lovf_b30q:
	s_waitcnt lgkmcnt(0)
	s_nop 15
	s_nop 15
	s_nop 15
	ds_read_b128 v[160:163], v225 offset:27648
	ds_read_b128 v[164:167], v225 offset:27680
	s_waitcnt lgkmcnt(0)
	v_mfma_f32_32x32x16_f16 v[80:95], v[160:163], v[144:147], v[112:127]
	v_mfma_f32_32x32x16_f16 v[80:95], v[164:167], v[148:151], v[80:95]
	s_nop 15
	ds_read_b128 v[160:163], v225 offset:27712
	ds_read_b128 v[164:167], v225 offset:27744
	s_waitcnt lgkmcnt(0)
	v_mfma_f32_32x32x16_f16 v[80:95], v[160:163], v[152:155], v[80:95]
	v_mfma_f32_32x32x16_f16 v[80:95], v[164:167], v[156:159], v[80:95]
	s_nop 15
	s_nop 15
	s_cmp_eq_u64 s[20:21], -1
	s_cbranch_scc1 .Lovfnm_b30q
	v_lshrrev_b32_e64 v235, v234, s20
	v_bfe_u32 v236, v235, 0, 1
	v_cvt_f32_u32_e32 v236, v236
	v_sub_f32_e32 v236, 1.0, v236
	v_fmac_f32_e32 v80, s35, v236
	v_bfe_u32 v236, v235, 1, 1
	v_cvt_f32_u32_e32 v236, v236
	v_sub_f32_e32 v236, 1.0, v236
	v_fmac_f32_e32 v81, s35, v236
	v_bfe_u32 v236, v235, 2, 1
	v_cvt_f32_u32_e32 v236, v236
	v_sub_f32_e32 v236, 1.0, v236
	v_fmac_f32_e32 v82, s35, v236
	v_bfe_u32 v236, v235, 3, 1
	v_cvt_f32_u32_e32 v236, v236
	v_sub_f32_e32 v236, 1.0, v236
	v_fmac_f32_e32 v83, s35, v236
	v_bfe_u32 v236, v235, 8, 1
	v_cvt_f32_u32_e32 v236, v236
	v_sub_f32_e32 v236, 1.0, v236
	v_fmac_f32_e32 v84, s35, v236
	v_bfe_u32 v236, v235, 9, 1
	v_cvt_f32_u32_e32 v236, v236
	v_sub_f32_e32 v236, 1.0, v236
	v_fmac_f32_e32 v85, s35, v236
	v_bfe_u32 v236, v235, 10, 1
	v_cvt_f32_u32_e32 v236, v236
	v_sub_f32_e32 v236, 1.0, v236
	v_fmac_f32_e32 v86, s35, v236
	v_bfe_u32 v236, v235, 11, 1
	v_cvt_f32_u32_e32 v236, v236
	v_sub_f32_e32 v236, 1.0, v236
	v_fmac_f32_e32 v87, s35, v236
	v_bfe_u32 v236, v235, 16, 1
	v_cvt_f32_u32_e32 v236, v236
	v_sub_f32_e32 v236, 1.0, v236
	v_fmac_f32_e32 v88, s35, v236
	v_bfe_u32 v236, v235, 17, 1
	v_cvt_f32_u32_e32 v236, v236
	v_sub_f32_e32 v236, 1.0, v236
	v_fmac_f32_e32 v89, s35, v236
	v_bfe_u32 v236, v235, 18, 1
	v_cvt_f32_u32_e32 v236, v236
	v_sub_f32_e32 v236, 1.0, v236
	v_fmac_f32_e32 v90, s35, v236
	v_bfe_u32 v236, v235, 19, 1
	v_cvt_f32_u32_e32 v236, v236
	v_sub_f32_e32 v236, 1.0, v236
	v_fmac_f32_e32 v91, s35, v236
	v_bfe_u32 v236, v235, 24, 1
	v_cvt_f32_u32_e32 v236, v236
	v_sub_f32_e32 v236, 1.0, v236
	v_fmac_f32_e32 v92, s35, v236
	v_bfe_u32 v236, v235, 25, 1
	v_cvt_f32_u32_e32 v236, v236
	v_sub_f32_e32 v236, 1.0, v236
	v_fmac_f32_e32 v93, s35, v236
	v_bfe_u32 v236, v235, 26, 1
	v_cvt_f32_u32_e32 v236, v236
	v_sub_f32_e32 v236, 1.0, v236
	v_fmac_f32_e32 v94, s35, v236
	v_bfe_u32 v236, v235, 27, 1
	v_cvt_f32_u32_e32 v236, v236
	v_sub_f32_e32 v236, 1.0, v236
	v_fmac_f32_e32 v95, s35, v236
.Lovfnm_b30q:
	v_max3_f32 v235, v80, v81, v82
	v_max3_f32 v235, v235, v83, v84
	v_max3_f32 v235, v235, v85, v86
	v_max3_f32 v235, v235, v87, v88
	v_max3_f32 v235, v235, v89, v90
	v_max3_f32 v235, v235, v91, v92
	v_max3_f32 v235, v235, v93, v94
	v_max_f32_e32 v235, v235, v95
	v_mov_b32_e32 v236, v235
	s_nop 1
	v_permlane32_swap_b32_e32 v235, v236
	v_max_f32_e32 v235, v235, v236
	v_max_f32_e32 v235, 0, v235
	v_exp_f32_e64 v237, -v235
	v_sub_f32_e32 v112, v112, v235
	v_sub_f32_e32 v113, v113, v235
	v_sub_f32_e32 v114, v114, v235
	v_sub_f32_e32 v115, v115, v235
	v_sub_f32_e32 v116, v116, v235
	v_sub_f32_e32 v117, v117, v235
	v_sub_f32_e32 v118, v118, v235
	v_sub_f32_e32 v119, v119, v235
	v_sub_f32_e32 v120, v120, v235
	v_sub_f32_e32 v121, v121, v235
	v_sub_f32_e32 v122, v122, v235
	v_sub_f32_e32 v123, v123, v235
	v_sub_f32_e32 v124, v124, v235
	v_sub_f32_e32 v125, v125, v235
	v_sub_f32_e32 v126, v126, v235
	v_sub_f32_e32 v127, v127, v235
	v_mul_f32_e32 v233, v233, v237
	v_mul_f32_e32 v32, v32, v237
	v_mul_f32_e32 v33, v33, v237
	v_mul_f32_e32 v34, v34, v237
	v_mul_f32_e32 v35, v35, v237
	v_mul_f32_e32 v36, v36, v237
	v_mul_f32_e32 v37, v37, v237
	v_mul_f32_e32 v38, v38, v237
	v_mul_f32_e32 v39, v39, v237
	v_mul_f32_e32 v40, v40, v237
	v_mul_f32_e32 v41, v41, v237
	v_mul_f32_e32 v42, v42, v237
	v_mul_f32_e32 v43, v43, v237
	v_mul_f32_e32 v44, v44, v237
	v_mul_f32_e32 v45, v45, v237
	v_mul_f32_e32 v46, v46, v237
	v_mul_f32_e32 v47, v47, v237
	v_mul_f32_e32 v48, v48, v237
	v_mul_f32_e32 v49, v49, v237
	v_mul_f32_e32 v50, v50, v237
	v_mul_f32_e32 v51, v51, v237
	v_mul_f32_e32 v52, v52, v237
	v_mul_f32_e32 v53, v53, v237
	v_mul_f32_e32 v54, v54, v237
	v_mul_f32_e32 v55, v55, v237
	v_mul_f32_e32 v56, v56, v237
	v_mul_f32_e32 v57, v57, v237
	v_mul_f32_e32 v58, v58, v237
	v_mul_f32_e32 v59, v59, v237
	v_mul_f32_e32 v60, v60, v237
	v_mul_f32_e32 v61, v61, v237
	v_mul_f32_e32 v62, v62, v237
	v_mul_f32_e32 v63, v63, v237
	v_sub_f32_e32 v80, v80, v235
	v_sub_f32_e32 v81, v81, v235
	v_sub_f32_e32 v82, v82, v235
	v_sub_f32_e32 v83, v83, v235
	v_sub_f32_e32 v84, v84, v235
	v_sub_f32_e32 v85, v85, v235
	v_sub_f32_e32 v86, v86, v235
	v_sub_f32_e32 v87, v87, v235
	v_sub_f32_e32 v88, v88, v235
	v_sub_f32_e32 v89, v89, v235
	v_sub_f32_e32 v90, v90, v235
	v_sub_f32_e32 v91, v91, v235
	v_sub_f32_e32 v92, v92, v235
	v_sub_f32_e32 v93, v93, v235
	v_sub_f32_e32 v94, v94, v235
	v_sub_f32_e32 v95, v95, v235
	v_exp_f32_e32 v80, v80
	v_exp_f32_e32 v81, v81
	v_exp_f32_e32 v82, v82
	v_exp_f32_e32 v83, v83
	v_exp_f32_e32 v84, v84
	v_exp_f32_e32 v85, v85
	v_exp_f32_e32 v86, v86
	v_exp_f32_e32 v87, v87
	v_exp_f32_e32 v88, v88
	v_exp_f32_e32 v89, v89
	v_exp_f32_e32 v90, v90
	v_exp_f32_e32 v91, v91
	v_exp_f32_e32 v92, v92
	v_exp_f32_e32 v93, v93
	v_exp_f32_e32 v94, v94
	v_exp_f32_e32 v95, v95
	s_nop 0
	v_add_f32_e32 v231, v80, v81
	v_add_f32_e32 v231, v231, v82
	v_add_f32_e32 v231, v231, v83
	v_add_f32_e32 v231, v231, v84
	v_add_f32_e32 v231, v231, v85
	v_add_f32_e32 v231, v231, v86
	v_add_f32_e32 v231, v231, v87
	v_add_f32_e32 v231, v231, v88
	v_add_f32_e32 v231, v231, v89
	v_add_f32_e32 v231, v231, v90
	v_add_f32_e32 v231, v231, v91
	v_add_f32_e32 v231, v231, v92
	v_add_f32_e32 v231, v231, v93
	v_add_f32_e32 v231, v231, v94
	v_add_f32_e32 v231, v231, v95
	v_cvt_pk_f16_f32 v168, v80, v81
	v_cvt_pk_f16_f32 v169, v82, v83
	v_cvt_pk_f16_f32 v170, v84, v85
	v_cvt_pk_f16_f32 v171, v86, v87
	v_cvt_pk_f16_f32 v172, v88, v89
	v_cvt_pk_f16_f32 v173, v90, v91
	v_cvt_pk_f16_f32 v174, v92, v93
	v_cvt_pk_f16_f32 v175, v94, v95
	s_branch .Lovfret_b30q
.Lovf_b31q:
	s_waitcnt lgkmcnt(0)
	s_nop 15
	s_nop 15
	s_nop 15
	ds_read_b128 v[160:163], v225 offset:32256
	ds_read_b128 v[164:167], v225 offset:32288
	s_waitcnt lgkmcnt(0)
	v_mfma_f32_32x32x16_f16 v[80:95], v[160:163], v[144:147], v[112:127]
	v_mfma_f32_32x32x16_f16 v[80:95], v[164:167], v[148:151], v[80:95]
	s_nop 15
	ds_read_b128 v[160:163], v225 offset:32320
	ds_read_b128 v[164:167], v225 offset:32352
	s_waitcnt lgkmcnt(0)
	v_mfma_f32_32x32x16_f16 v[80:95], v[160:163], v[152:155], v[80:95]
	v_mfma_f32_32x32x16_f16 v[80:95], v[164:167], v[156:159], v[80:95]
	s_nop 15
	s_nop 15
	s_cmp_eq_u64 s[20:21], -1
	s_cbranch_scc1 .Lovfnm_b31q
	v_lshrrev_b32_e64 v235, v234, s21
	v_bfe_u32 v236, v235, 0, 1
	v_cvt_f32_u32_e32 v236, v236
	v_sub_f32_e32 v236, 1.0, v236
	v_fmac_f32_e32 v80, s35, v236
	v_bfe_u32 v236, v235, 1, 1
	v_cvt_f32_u32_e32 v236, v236
	v_sub_f32_e32 v236, 1.0, v236
	v_fmac_f32_e32 v81, s35, v236
	v_bfe_u32 v236, v235, 2, 1
	v_cvt_f32_u32_e32 v236, v236
	v_sub_f32_e32 v236, 1.0, v236
	v_fmac_f32_e32 v82, s35, v236
	v_bfe_u32 v236, v235, 3, 1
	v_cvt_f32_u32_e32 v236, v236
	v_sub_f32_e32 v236, 1.0, v236
	v_fmac_f32_e32 v83, s35, v236
	v_bfe_u32 v236, v235, 8, 1
	v_cvt_f32_u32_e32 v236, v236
	v_sub_f32_e32 v236, 1.0, v236
	v_fmac_f32_e32 v84, s35, v236
	v_bfe_u32 v236, v235, 9, 1
	v_cvt_f32_u32_e32 v236, v236
	v_sub_f32_e32 v236, 1.0, v236
	v_fmac_f32_e32 v85, s35, v236
	v_bfe_u32 v236, v235, 10, 1
	v_cvt_f32_u32_e32 v236, v236
	v_sub_f32_e32 v236, 1.0, v236
	v_fmac_f32_e32 v86, s35, v236
	v_bfe_u32 v236, v235, 11, 1
	v_cvt_f32_u32_e32 v236, v236
	v_sub_f32_e32 v236, 1.0, v236
	v_fmac_f32_e32 v87, s35, v236
	v_bfe_u32 v236, v235, 16, 1
	v_cvt_f32_u32_e32 v236, v236
	v_sub_f32_e32 v236, 1.0, v236
	v_fmac_f32_e32 v88, s35, v236
	v_bfe_u32 v236, v235, 17, 1
	v_cvt_f32_u32_e32 v236, v236
	v_sub_f32_e32 v236, 1.0, v236
	v_fmac_f32_e32 v89, s35, v236
	v_bfe_u32 v236, v235, 18, 1
	v_cvt_f32_u32_e32 v236, v236
	v_sub_f32_e32 v236, 1.0, v236
	v_fmac_f32_e32 v90, s35, v236
	v_bfe_u32 v236, v235, 19, 1
	v_cvt_f32_u32_e32 v236, v236
	v_sub_f32_e32 v236, 1.0, v236
	v_fmac_f32_e32 v91, s35, v236
	v_bfe_u32 v236, v235, 24, 1
	v_cvt_f32_u32_e32 v236, v236
	v_sub_f32_e32 v236, 1.0, v236
	v_fmac_f32_e32 v92, s35, v236
	v_bfe_u32 v236, v235, 25, 1
	v_cvt_f32_u32_e32 v236, v236
	v_sub_f32_e32 v236, 1.0, v236
	v_fmac_f32_e32 v93, s35, v236
	v_bfe_u32 v236, v235, 26, 1
	v_cvt_f32_u32_e32 v236, v236
	v_sub_f32_e32 v236, 1.0, v236
	v_fmac_f32_e32 v94, s35, v236
	v_bfe_u32 v236, v235, 27, 1
	v_cvt_f32_u32_e32 v236, v236
	v_sub_f32_e32 v236, 1.0, v236
	v_fmac_f32_e32 v95, s35, v236
